# P4 conv_task: remaining 6 token rows of each run touched into L2 right after the first pair is issued (serialized load pairs then hit L2), on top of v63
# speedup vs baseline: 1.0124x; 1.0124x over previous
; #define LAS __attribute__((address_space(3)))
; __device__ __forceinline__ unsigned pk2(float lo, float hi) { const f32x2 v = {lo, hi}; return __builtin_bit_cast(unsigned, __builtin_convertvector(v, hwbf16x2)); }
; __device__ __forceinline__ float fsigmoid(float x) { return __builtin_amdgcn_rcpf(1.0f + __expf(-x)); }
; __device__ __forceinline__ void unpack8(const v4u q, float (&d)[8]) { d[0] = bflo(q.x); d[1] = bfhi(q.x); d[2] = bflo(q.y); d[3] = bfhi(q.y); d[4] = bflo(q.z); d[5] = bfhi(q.z); d[6] = bflo(q.w); d[7] = bfhi(q.w); }
; template <bool TR, bool SCALE>
; __device__ __forceinline__ void conv_task(const Params& p, const bf16* proj, size_t trow0, int tl0, int run, int xcol, LAS bf16* dst, int d0, const LAS float* sc) {
;     ...
;     const int l0 = run * 8; const bf16* src = proj + (trow0 + l0) * PROJ_LD + COL_XBC + xcol;
;     float r0[8], r1[8], r2[8];
;     { const int pos = tl0 + l0; v4u q0 = (v4u){0u, 0u, 0u, 0u}, q1 = q0, q2 = q0;
;       if (pos - 3 >= 0) q0 = *(const v4u*)(src - 3 * PROJ_LD);
;       if (pos - 2 >= 0) q1 = *(const v4u*)(src - 2 * PROJ_LD);
;       if (pos - 1 >= 0) q2 = *(const v4u*)(src - 1 * PROJ_LD);
;       unpack8(q0, r0); unpack8(q1, r1); unpack8(q2, r2); }
; #pragma unroll
;     for (int i = 0; i < 8; i += 2) {
;         float r3[8], r4[8], o0[8], o1[8];
;         unpack8(*(const v4u*)(src + (size_t)i * PROJ_LD), r3); unpack8(*(const v4u*)(src + (size_t)(i + 1) * PROJ_LD), r4);
; #pragma unroll
;         for (int j = 0; j < 8; ++j) { const float a0 = bb[j] + w[0][j] * r0[j] + w[1][j] * r1[j] + w[2][j] * r2[j] + w[3][j] * r3[j];
;             const float a1 = bb[j] + w[0][j] * r1[j] + w[1][j] * r2[j] + w[2][j] * r3[j] + w[3][j] * r4[j];
;             o0[j] = a0 * fsigmoid(a0); o1[j] = a1 * fsigmoid(a1); }
;         if constexpr (TR) {
;             float s0 = 1.f, s1 = 1.f; if constexpr (SCALE) { s0 = sc[l0 + i]; s1 = sc[l0 + i + 1]; }
; #pragma unroll
;             for (int j = 0; j < 8; ++j) *(LAS unsigned*)(dst + (d0 + j) * SPT + l0 + i) = pk2(o0[j] * s0, o1[j] * s1);
.LBB0_444:
	s_or_b64 exec, exec, s[10:11]
	global_load_dwordx4 v[58:61], v[62:63], off
	v_add_co_u32_e32 v54, vcc, 0x1000, v62
	s_waitcnt vmcnt(1)
	v_lshlrev_b32_e32 v64, 16, v46
	v_addc_co_u32_e32 v55, vcc, 0, v63, vcc
	global_load_dwordx4 v[54:57], v[54:55], off offset:3584
	v_add_co_u32_e32 v248, vcc, s79, v62
	s_nop 1
	v_addc_co_u32_e32 v249, vcc, 0, v63, vcc
	global_load_dword v246, v[248:249], off offset:3072
	v_add_co_u32_e32 v248, vcc, s81, v62
	s_nop 1
	v_addc_co_u32_e32 v249, vcc, 0, v63, vcc
	global_load_dword v246, v[248:249], off offset:2560
	v_add_co_u32_e32 v248, vcc, s82, v62
	s_nop 1
	v_addc_co_u32_e32 v249, vcc, 0, v63, vcc
	global_load_dword v246, v[248:249], off offset:2048
	v_add_co_u32_e32 v248, vcc, s83, v62
	s_nop 1
	v_addc_co_u32_e32 v249, vcc, 0, v63, vcc
	global_load_dword v246, v[248:249], off offset:1536
	v_add_co_u32_e32 v248, vcc, s92, v62
	s_nop 1
	v_addc_co_u32_e32 v249, vcc, 0, v63, vcc
	global_load_dword v246, v[248:249], off offset:1024
	v_add_co_u32_e32 v248, vcc, s93, v62
	s_nop 1
	v_addc_co_u32_e32 v249, vcc, 0, v63, vcc
	global_load_dword v246, v[248:249], off offset:512
	v_and_b32_e32 v65, 0xffff0000, v46
	v_lshlrev_b32_e32 v70, 16, v42
	v_and_b32_e32 v71, 0xffff0000, v42
	v_pk_fma_f32 v[64:65], v[22:23], v[64:65], v[38:39]
	v_lshlrev_b32_e32 v66, 16, v50
	v_and_b32_e32 v67, 0xffff0000, v50
	v_pk_fma_f32 v[64:65], v[26:27], v[70:71], v[64:65]
	v_pk_fma_f32 v[70:71], v[22:23], v[70:71], v[38:39]
	v_pk_fma_f32 v[64:65], v[30:31], v[66:67], v[64:65]
	v_pk_fma_f32 v[70:71], v[26:27], v[66:67], v[70:71]
	v_lshlrev_b32_e32 v46, 16, v47
	v_and_b32_e32 v47, 0xffff0000, v47
	v_pk_fma_f32 v[46:47], v[24:25], v[46:47], v[40:41]
	v_lshlrev_b32_e32 v74, 16, v44
	v_and_b32_e32 v75, 0xffff0000, v44
	v_lshlrev_b32_e32 v76, 16, v52
	v_and_b32_e32 v77, 0xffff0000, v52
	v_lshlrev_b32_e32 v78, 16, v53
	v_and_b32_e32 v79, 0xffff0000, v53
	s_waitcnt vmcnt(1)
	v_lshlrev_b32_e32 v68, 16, v58
	v_and_b32_e32 v69, 0xffff0000, v58
	v_pk_fma_f32 v[64:65], v[34:35], v[68:69], v[64:65]
	v_pk_fma_f32 v[70:71], v[30:31], v[68:69], v[70:71]
	v_mul_f32_e32 v42, 0xbfb8aa3b, v64
	v_exp_f32_e32 v42, v42
	v_lshlrev_b32_e32 v58, 16, v59
	v_and_b32_e32 v59, 0xffff0000, v59
	s_waitcnt vmcnt(0)
	v_lshlrev_b32_e32 v52, 16, v57
	v_add_f32_e32 v42, 1.0, v42
	v_rcp_f32_e32 v72, v42
	v_mul_f32_e32 v42, 0xbfb8aa3b, v65
	v_exp_f32_e32 v42, v42
	v_and_b32_e32 v53, 0xffff0000, v57
	v_add_f32_e32 v42, 1.0, v42
	v_rcp_f32_e32 v73, v42
	s_nop 0
	v_pk_mul_f32 v[80:81], v[64:65], v[72:73]
	v_lshlrev_b32_e32 v64, 16, v54
	v_and_b32_e32 v65, 0xffff0000, v54
	v_pk_fma_f32 v[70:71], v[34:35], v[64:65], v[70:71]
	s_nop 0
	v_mul_f32_e32 v42, 0xbfb8aa3b, v70
	v_exp_f32_e32 v42, v42
	s_nop 0
	v_add_f32_e32 v42, 1.0, v42
	v_rcp_f32_e32 v72, v42
	v_mul_f32_e32 v42, 0xbfb8aa3b, v71
	v_exp_f32_e32 v42, v42
	s_nop 0
	v_add_f32_e32 v42, 1.0, v42
	v_rcp_f32_e32 v73, v42
	v_lshlrev_b32_e32 v42, 16, v43
	v_and_b32_e32 v43, 0xffff0000, v43
	v_pk_fma_f32 v[46:47], v[28:29], v[42:43], v[46:47]
	v_pk_mul_f32 v[86:87], v[70:71], v[72:73]
	v_lshlrev_b32_e32 v70, 16, v51
	v_and_b32_e32 v71, 0xffff0000, v51
	v_pk_fma_f32 v[46:47], v[32:33], v[70:71], v[46:47]
	v_pk_fma_f32 v[42:43], v[24:25], v[42:43], v[40:41]
	v_pk_fma_f32 v[46:47], v[36:37], v[58:59], v[46:47]
	v_pk_fma_f32 v[42:43], v[28:29], v[70:71], v[42:43]
	v_mul_f32_e32 v50, 0xbfb8aa3b, v46
	v_mul_f32_e32 v51, 0xbfb8aa3b, v47
	v_exp_f32_e32 v50, v50
	v_exp_f32_e32 v51, v51
	v_pk_fma_f32 v[42:43], v[32:33], v[58:59], v[42:43]
	v_lshlrev_b32_e32 v72, 16, v60
	v_add_f32_e32 v50, 1.0, v50
	v_add_f32_e32 v51, 1.0, v51
	v_rcp_f32_e32 v50, v50
	v_rcp_f32_e32 v51, v51
	v_and_b32_e32 v73, 0xffff0000, v60
	v_pk_mul_f32 v[46:47], v[46:47], v[50:51]
	v_lshlrev_b32_e32 v50, 16, v55
	v_and_b32_e32 v51, 0xffff0000, v55
	v_pk_fma_f32 v[42:43], v[36:37], v[50:51], v[42:43]
	s_nop 0
	v_mul_f32_e32 v54, 0xbfb8aa3b, v42
	v_mul_f32_e32 v55, 0xbfb8aa3b, v43
	v_exp_f32_e32 v54, v54
	v_exp_f32_e32 v55, v55
	v_add_f32_e32 v54, 1.0, v54
	v_add_f32_e32 v55, 1.0, v55
	v_rcp_f32_e32 v54, v54
	v_rcp_f32_e32 v55, v55
	s_nop 0
	v_pk_mul_f32 v[92:93], v[42:43], v[54:55]
	v_lshlrev_b32_e32 v42, 16, v48
	v_and_b32_e32 v43, 0xffff0000, v48
	v_pk_fma_f32 v[42:43], v[2:3], v[42:43], v[18:19]
	s_nop 0
	v_pk_fma_f32 v[42:43], v[6:7], v[74:75], v[42:43]
	s_nop 0
	v_pk_fma_f32 v[42:43], v[10:11], v[76:77], v[42:43]
	s_nop 0
	v_pk_fma_f32 v[42:43], v[14:15], v[72:73], v[42:43]
	s_nop 0
	v_mul_f32_e32 v44, 0xbfb8aa3b, v42
	v_exp_f32_e32 v44, v44
	s_nop 0
	v_add_f32_e32 v44, 1.0, v44
	v_rcp_f32_e32 v54, v44
	v_mul_f32_e32 v44, 0xbfb8aa3b, v43
	v_exp_f32_e32 v44, v44
	s_nop 0
	v_add_f32_e32 v44, 1.0, v44
	v_rcp_f32_e32 v55, v44
	s_nop 0
	v_pk_mul_f32 v[90:91], v[42:43], v[54:55]
	v_pk_fma_f32 v[42:43], v[2:3], v[74:75], v[18:19]
	v_lshlrev_b32_e32 v54, 16, v56
	v_pk_fma_f32 v[42:43], v[6:7], v[76:77], v[42:43]
	v_and_b32_e32 v55, 0xffff0000, v56
	v_pk_fma_f32 v[42:43], v[10:11], v[72:73], v[42:43]
	s_nop 0
	v_pk_fma_f32 v[42:43], v[14:15], v[54:55], v[42:43]
	s_nop 0
	v_mul_f32_e32 v44, 0xbfb8aa3b, v42
	v_exp_f32_e32 v44, v44
	s_nop 0
	v_add_f32_e32 v44, 1.0, v44
	v_rcp_f32_e32 v74, v44
	v_mul_f32_e32 v44, 0xbfb8aa3b, v43
	v_exp_f32_e32 v44, v44
	s_nop 0
	v_add_f32_e32 v44, 1.0, v44
	v_rcp_f32_e32 v75, v44
	v_lshlrev_b32_e32 v44, 16, v45
	v_and_b32_e32 v45, 0xffff0000, v45
	v_pk_mul_f32 v[94:95], v[42:43], v[74:75]
	v_lshlrev_b32_e32 v42, 16, v49
	v_and_b32_e32 v43, 0xffff0000, v49
	v_pk_fma_f32 v[42:43], v[4:5], v[42:43], v[20:21]
	v_lshlrev_b32_e32 v74, 16, v61
	v_pk_fma_f32 v[42:43], v[8:9], v[44:45], v[42:43]
	v_and_b32_e32 v75, 0xffff0000, v61
; #define LAS __attribute__((address_space(3)))
; __device__ __forceinline__ unsigned pk2(float lo, float hi) { const f32x2 v = {lo, hi}; return __builtin_bit_cast(unsigned, __builtin_convertvector(v, hwbf16x2)); }
; __device__ __forceinline__ float fsigmoid(float x) { return __builtin_amdgcn_rcpf(1.0f + __expf(-x)); }
; __device__ __forceinline__ void unpack8(const v4u q, float (&d)[8]) { d[0] = bflo(q.x); d[1] = bfhi(q.x); d[2] = bflo(q.y); d[3] = bfhi(q.y); d[4] = bflo(q.z); d[5] = bfhi(q.z); d[6] = bflo(q.w); d[7] = bfhi(q.w); }
; template <bool TR, bool SCALE>
; __device__ __forceinline__ void conv_task(const Params& p, const bf16* proj, size_t trow0, int tl0, int run, int xcol, LAS bf16* dst, int d0, const LAS float* sc) {
;     ...
;     for (int i = 0; i < 8; i += 2) {
;         float r3[8], r4[8], o0[8], o1[8];
;         unpack8(*(const v4u*)(src + (size_t)i * PROJ_LD), r3); unpack8(*(const v4u*)(src + (size_t)(i + 1) * PROJ_LD), r4);
; #pragma unroll
;         for (int j = 0; j < 8; ++j) { const float a0 = bb[j] + w[0][j] * r0[j] + w[1][j] * r1[j] + w[2][j] * r2[j] + w[3][j] * r3[j];
;             const float a1 = bb[j] + w[0][j] * r1[j] + w[1][j] * r2[j] + w[2][j] * r3[j] + w[3][j] * r4[j];
;             o0[j] = a0 * fsigmoid(a0); o1[j] = a1 * fsigmoid(a1); }
;         if constexpr (TR) {
;             float s0 = 1.f, s1 = 1.f; if constexpr (SCALE) { s0 = sc[l0 + i]; s1 = sc[l0 + i + 1]; }
; #pragma unroll
;             for (int j = 0; j < 8; ++j) *(LAS unsigned*)(dst + (d0 + j) * SPT + l0 + i) = pk2(o0[j] * s0, o1[j] * s1);
;         } else {
;             *(LAS v4u*)(dst + (l0 + i) * SPT + d0) = (v4u){pk2(o0[0], o0[1]), pk2(o0[2], o0[3]), pk2(o0[4], o0[5]), pk2(o0[6], o0[7])};
;             *(LAS v4u*)(dst + (l0 + i + 1) * SPT + d0) = (v4u){pk2(o1[0], o1[1]), pk2(o1[2], o1[3]), pk2(o1[4], o1[5]), pk2(o1[6], o1[7])};
;         }
; #pragma unroll
;         for (int j = 0; j < 8; ++j) { r0[j] = r2[j]; r1[j] = r3[j]; r2[j] = r4[j]; }
	v_pk_fma_f32 v[42:43], v[12:13], v[78:79], v[42:43]
	s_nop 0
	v_pk_fma_f32 v[42:43], v[16:17], v[74:75], v[42:43]
	s_nop 0
	v_mul_f32_e32 v48, 0xbfb8aa3b, v42
	v_mul_f32_e32 v49, 0xbfb8aa3b, v43
	v_exp_f32_e32 v48, v48
	v_exp_f32_e32 v49, v49
	v_add_f32_e32 v48, 1.0, v48
	v_add_f32_e32 v49, 1.0, v49
	v_rcp_f32_e32 v48, v48
	v_rcp_f32_e32 v49, v49
	s_nop 0
	v_pk_mul_f32 v[48:49], v[42:43], v[48:49]
	v_pk_fma_f32 v[42:43], v[4:5], v[44:45], v[20:21]
	s_nop 0
	v_pk_fma_f32 v[42:43], v[8:9], v[78:79], v[42:43]
	s_nop 0
	v_pk_fma_f32 v[42:43], v[12:13], v[74:75], v[42:43]
	s_nop 0
	v_pk_fma_f32 v[42:43], v[16:17], v[52:53], v[42:43]
	s_nop 0
	v_mul_f32_e32 v44, 0xbfb8aa3b, v42
	v_mul_f32_e32 v45, 0xbfb8aa3b, v43
	v_exp_f32_e32 v44, v44
	v_exp_f32_e32 v45, v45
	v_add_f32_e32 v44, 1.0, v44
	v_add_f32_e32 v45, 1.0, v45
	v_rcp_f32_e32 v44, v44
	v_rcp_f32_e32 v45, v45
	s_nop 0
	v_pk_mul_f32 v[56:57], v[42:43], v[44:45]
	v_cvt_pk_bf16_f32 v42, v80, v81
	v_cvt_pk_bf16_f32 v43, v46, v47
	v_cvt_pk_bf16_f32 v44, v90, v91
	v_cvt_pk_bf16_f32 v45, v48, v49
	v_lshl_add_u32 v90, v88, 1, v85
	ds_write_b128 v90, v[42:45]
	v_cvt_pk_bf16_f32 v42, v86, v87
	v_cvt_pk_bf16_f32 v43, v92, v93
	v_cvt_pk_bf16_f32 v44, v94, v95
	v_cvt_pk_bf16_f32 v45, v56, v57
	ds_write_b128 v90, v[42:45] offset:272
	v_add_co_u32_e32 v42, vcc, s79, v62
	v_pk_fma_f32 v[56:57], v[22:23], v[66:67], v[38:39]
	s_nop 0
	v_addc_co_u32_e32 v43, vcc, 0, v63, vcc
	global_load_dwordx4 v[42:45], v[42:43], off offset:3072
	v_add_co_u32_e32 v46, vcc, s81, v62
	v_pk_fma_f32 v[56:57], v[26:27], v[68:69], v[56:57]
	s_nop 0
	v_addc_co_u32_e32 v47, vcc, 0, v63, vcc
	global_load_dwordx4 v[46:49], v[46:47], off offset:2560
	v_pk_fma_f32 v[56:57], v[30:31], v[64:65], v[56:57]
	s_waitcnt vmcnt(1)
	v_lshlrev_b32_e32 v86, 16, v42
	v_and_b32_e32 v87, 0xffff0000, v42
	v_pk_fma_f32 v[56:57], v[34:35], v[86:87], v[56:57]
	v_lshlrev_b32_e32 v80, 16, v43
	v_mul_f32_e32 v42, 0xbfb8aa3b, v56
	v_exp_f32_e32 v42, v42
	s_waitcnt vmcnt(0)
	v_lshlrev_b32_e32 v66, 16, v46
	v_and_b32_e32 v67, 0xffff0000, v46
	v_and_b32_e32 v81, 0xffff0000, v43
	v_add_f32_e32 v42, 1.0, v42
	v_rcp_f32_e32 v60, v42
	v_mul_f32_e32 v42, 0xbfb8aa3b, v57
	v_exp_f32_e32 v42, v42
	v_lshlrev_b32_e32 v88, 16, v44
	v_and_b32_e32 v89, 0xffff0000, v44
	v_add_f32_e32 v42, 1.0, v42
	v_rcp_f32_e32 v61, v42
	s_nop 0
	v_pk_mul_f32 v[92:93], v[56:57], v[60:61]
	v_pk_fma_f32 v[56:57], v[22:23], v[68:69], v[38:39]
	s_nop 0
	v_pk_fma_f32 v[56:57], v[26:27], v[64:65], v[56:57]
	v_pk_fma_f32 v[64:65], v[22:23], v[64:65], v[38:39]
	v_pk_fma_f32 v[56:57], v[30:31], v[86:87], v[56:57]
	v_pk_fma_f32 v[64:65], v[26:27], v[86:87], v[64:65]
	v_pk_fma_f32 v[56:57], v[34:35], v[66:67], v[56:57]
	v_pk_fma_f32 v[64:65], v[30:31], v[66:67], v[64:65]
	v_mul_f32_e32 v42, 0xbfb8aa3b, v56
	v_exp_f32_e32 v42, v42
	s_nop 0
	v_add_f32_e32 v42, 1.0, v42
	v_rcp_f32_e32 v60, v42
	v_mul_f32_e32 v42, 0xbfb8aa3b, v57
	v_exp_f32_e32 v42, v42
	s_nop 0
	v_add_f32_e32 v42, 1.0, v42
	v_rcp_f32_e32 v61, v42
	v_pk_fma_f32 v[42:43], v[24:25], v[70:71], v[40:41]
	v_pk_mul_f32 v[68:69], v[56:57], v[60:61]
	v_pk_fma_f32 v[42:43], v[28:29], v[58:59], v[42:43]
	v_lshlrev_b32_e32 v60, 16, v47
	v_pk_fma_f32 v[42:43], v[32:33], v[50:51], v[42:43]
	v_and_b32_e32 v61, 0xffff0000, v47
	v_pk_fma_f32 v[42:43], v[36:37], v[80:81], v[42:43]
	s_nop 0
	v_mul_f32_e32 v46, 0xbfb8aa3b, v42
	v_exp_f32_e32 v46, v46
	s_nop 0
	v_add_f32_e32 v46, 1.0, v46
	v_rcp_f32_e32 v56, v46
	v_mul_f32_e32 v46, 0xbfb8aa3b, v43
	v_exp_f32_e32 v46, v46
	s_nop 0
	v_add_f32_e32 v46, 1.0, v46
	v_rcp_f32_e32 v57, v46
	s_nop 0
	v_pk_mul_f32 v[70:71], v[42:43], v[56:57]
	v_pk_fma_f32 v[42:43], v[24:25], v[58:59], v[40:41]
	v_lshlrev_b32_e32 v58, 16, v48
	v_pk_fma_f32 v[42:43], v[28:29], v[50:51], v[42:43]
	v_and_b32_e32 v59, 0xffff0000, v48
	v_pk_fma_f32 v[42:43], v[32:33], v[80:81], v[42:43]
	s_nop 0
	v_pk_fma_f32 v[42:43], v[36:37], v[60:61], v[42:43]
	s_nop 0
	v_mul_f32_e32 v46, 0xbfb8aa3b, v42
	v_mul_f32_e32 v47, 0xbfb8aa3b, v43
	v_exp_f32_e32 v46, v46
	v_exp_f32_e32 v47, v47
	v_add_f32_e32 v46, 1.0, v46
	v_add_f32_e32 v47, 1.0, v47
	v_rcp_f32_e32 v46, v46
	v_rcp_f32_e32 v47, v47
	s_nop 0
	v_pk_mul_f32 v[46:47], v[42:43], v[46:47]
	v_pk_fma_f32 v[42:43], v[2:3], v[76:77], v[18:19]
	s_nop 0
	v_pk_fma_f32 v[42:43], v[6:7], v[72:73], v[42:43]
	s_nop 0
	v_pk_fma_f32 v[42:43], v[10:11], v[54:55], v[42:43]
	s_nop 0
	v_pk_fma_f32 v[42:43], v[14:15], v[88:89], v[42:43]
	s_nop 0
	v_mul_f32_e32 v44, 0xbfb8aa3b, v42
	v_exp_f32_e32 v44, v44
	s_nop 0
	v_add_f32_e32 v44, 1.0, v44
	v_rcp_f32_e32 v56, v44
	v_mul_f32_e32 v44, 0xbfb8aa3b, v43
	v_exp_f32_e32 v44, v44
	s_nop 0
	v_add_f32_e32 v44, 1.0, v44
	v_rcp_f32_e32 v57, v44
	s_nop 0
	v_pk_mul_f32 v[76:77], v[42:43], v[56:57]
	v_pk_fma_f32 v[42:43], v[2:3], v[72:73], v[18:19]
	v_lshlrev_b32_e32 v72, 16, v45
	v_pk_fma_f32 v[42:43], v[6:7], v[54:55], v[42:43]
	v_and_b32_e32 v73, 0xffff0000, v45
	v_pk_fma_f32 v[42:43], v[10:11], v[88:89], v[42:43]
	s_nop 0
	v_pk_fma_f32 v[42:43], v[14:15], v[58:59], v[42:43]
	s_nop 0
	v_mul_f32_e32 v44, 0xbfb8aa3b, v42
	v_exp_f32_e32 v44, v44
	s_nop 0
	v_add_f32_e32 v44, 1.0, v44
	v_rcp_f32_e32 v56, v44
	v_mul_f32_e32 v44, 0xbfb8aa3b, v43
	v_exp_f32_e32 v44, v44
	s_nop 0
	v_add_f32_e32 v44, 1.0, v44
	v_rcp_f32_e32 v57, v44
	s_nop 0
	v_pk_mul_f32 v[94:95], v[42:43], v[56:57]
	v_pk_fma_f32 v[42:43], v[4:5], v[78:79], v[20:21]
	v_lshlrev_b32_e32 v56, 16, v49
	v_pk_fma_f32 v[42:43], v[8:9], v[74:75], v[42:43]
	v_and_b32_e32 v57, 0xffff0000, v49
	v_pk_fma_f32 v[42:43], v[12:13], v[52:53], v[42:43]
	s_nop 0
	v_pk_fma_f32 v[42:43], v[16:17], v[72:73], v[42:43]
	s_nop 0
; #define LAS __attribute__((address_space(3)))
; __device__ __forceinline__ unsigned pk2(float lo, float hi) { const f32x2 v = {lo, hi}; return __builtin_bit_cast(unsigned, __builtin_convertvector(v, hwbf16x2)); }
; __device__ __forceinline__ float fsigmoid(float x) { return __builtin_amdgcn_rcpf(1.0f + __expf(-x)); }
; __device__ __forceinline__ void unpack8(const v4u q, float (&d)[8]) { d[0] = bflo(q.x); d[1] = bfhi(q.x); d[2] = bflo(q.y); d[3] = bfhi(q.y); d[4] = bflo(q.z); d[5] = bfhi(q.z); d[6] = bflo(q.w); d[7] = bfhi(q.w); }
; template <bool TR, bool SCALE>
; __device__ __forceinline__ void conv_task(const Params& p, const bf16* proj, size_t trow0, int tl0, int run, int xcol, LAS bf16* dst, int d0, const LAS float* sc) {
;     ...
;     for (int i = 0; i < 8; i += 2) {
;         float r3[8], r4[8], o0[8], o1[8];
;         unpack8(*(const v4u*)(src + (size_t)i * PROJ_LD), r3); unpack8(*(const v4u*)(src + (size_t)(i + 1) * PROJ_LD), r4);
; #pragma unroll
;         for (int j = 0; j < 8; ++j) { const float a0 = bb[j] + w[0][j] * r0[j] + w[1][j] * r1[j] + w[2][j] * r2[j] + w[3][j] * r3[j];
;             const float a1 = bb[j] + w[0][j] * r1[j] + w[1][j] * r2[j] + w[2][j] * r3[j] + w[3][j] * r4[j];
;             o0[j] = a0 * fsigmoid(a0); o1[j] = a1 * fsigmoid(a1); }
;         if constexpr (TR) {
;             float s0 = 1.f, s1 = 1.f; if constexpr (SCALE) { s0 = sc[l0 + i]; s1 = sc[l0 + i + 1]; }
; #pragma unroll
;             for (int j = 0; j < 8; ++j) *(LAS unsigned*)(dst + (d0 + j) * SPT + l0 + i) = pk2(o0[j] * s0, o1[j] * s1);
;         } else {
;             *(LAS v4u*)(dst + (l0 + i) * SPT + d0) = (v4u){pk2(o0[0], o0[1]), pk2(o0[2], o0[3]), pk2(o0[4], o0[5]), pk2(o0[6], o0[7])};
;             *(LAS v4u*)(dst + (l0 + i + 1) * SPT + d0) = (v4u){pk2(o1[0], o1[1]), pk2(o1[2], o1[3]), pk2(o1[4], o1[5]), pk2(o1[6], o1[7])};
;         }
; #pragma unroll
;         for (int j = 0; j < 8; ++j) { r0[j] = r2[j]; r1[j] = r3[j]; r2[j] = r4[j]; }
	v_mul_f32_e32 v44, 0xbfb8aa3b, v42
	v_mul_f32_e32 v45, 0xbfb8aa3b, v43
	v_exp_f32_e32 v44, v44
	v_exp_f32_e32 v45, v45
	v_add_f32_e32 v44, 1.0, v44
	v_add_f32_e32 v45, 1.0, v45
	v_rcp_f32_e32 v44, v44
	v_rcp_f32_e32 v45, v45
	s_nop 0
	v_pk_mul_f32 v[78:79], v[42:43], v[44:45]
	v_pk_fma_f32 v[42:43], v[4:5], v[74:75], v[20:21]
	s_nop 0
	v_pk_fma_f32 v[42:43], v[8:9], v[52:53], v[42:43]
	s_nop 0
	v_pk_fma_f32 v[42:43], v[12:13], v[72:73], v[42:43]
	s_nop 0
	v_pk_fma_f32 v[42:43], v[16:17], v[56:57], v[42:43]
	s_nop 0
	v_mul_f32_e32 v44, 0xbfb8aa3b, v42
	v_mul_f32_e32 v45, 0xbfb8aa3b, v43
	v_exp_f32_e32 v44, v44
	v_exp_f32_e32 v45, v45
	v_add_f32_e32 v44, 1.0, v44
	v_add_f32_e32 v45, 1.0, v45
	v_rcp_f32_e32 v44, v44
	v_rcp_f32_e32 v45, v45
	s_nop 0
	v_pk_mul_f32 v[48:49], v[42:43], v[44:45]
	v_cvt_pk_bf16_f32 v42, v92, v93
	v_cvt_pk_bf16_f32 v43, v70, v71
	v_cvt_pk_bf16_f32 v44, v76, v77
	v_cvt_pk_bf16_f32 v45, v78, v79
	ds_write_b128 v90, v[42:45] offset:544
	v_cvt_pk_bf16_f32 v42, v68, v69
	v_cvt_pk_bf16_f32 v43, v46, v47
	v_cvt_pk_bf16_f32 v44, v94, v95
	v_cvt_pk_bf16_f32 v45, v48, v49
	ds_write_b128 v90, v[42:45] offset:816
	v_add_co_u32_e32 v42, vcc, s82, v62
	s_nop 1
	v_addc_co_u32_e32 v43, vcc, 0, v63, vcc
	global_load_dwordx4 v[42:45], v[42:43], off offset:2048
	v_add_co_u32_e32 v46, vcc, s83, v62
	s_nop 1
	v_addc_co_u32_e32 v47, vcc, 0, v63, vcc
	global_load_dwordx4 v[46:49], v[46:47], off offset:1536
	s_waitcnt vmcnt(1)
	v_lshlrev_b32_e32 v68, 16, v42
	v_and_b32_e32 v69, 0xffff0000, v42
	v_pk_fma_f32 v[64:65], v[34:35], v[68:69], v[64:65]
	s_waitcnt vmcnt(0)
	v_lshlrev_b32_e32 v74, 16, v46
	v_mul_f32_e32 v42, 0xbfb8aa3b, v64
	v_exp_f32_e32 v42, v42
	v_and_b32_e32 v75, 0xffff0000, v46
	v_lshlrev_b32_e32 v76, 16, v47
	v_and_b32_e32 v77, 0xffff0000, v47
	v_add_f32_e32 v42, 1.0, v42
	v_rcp_f32_e32 v70, v42
	v_mul_f32_e32 v42, 0xbfb8aa3b, v65
	v_exp_f32_e32 v42, v42
	s_nop 0
	v_add_f32_e32 v42, 1.0, v42
	v_rcp_f32_e32 v71, v42
	s_nop 0
	v_pk_mul_f32 v[78:79], v[64:65], v[70:71]
	v_pk_fma_f32 v[64:65], v[22:23], v[86:87], v[38:39]
	s_nop 0
	v_pk_fma_f32 v[64:65], v[26:27], v[66:67], v[64:65]
	s_nop 0
	v_pk_fma_f32 v[64:65], v[30:31], v[68:69], v[64:65]
	s_nop 0
	v_pk_fma_f32 v[64:65], v[34:35], v[74:75], v[64:65]
	s_nop 0
	v_mul_f32_e32 v42, 0xbfb8aa3b, v64
	v_exp_f32_e32 v42, v42
	s_nop 0
	v_add_f32_e32 v42, 1.0, v42
	v_rcp_f32_e32 v70, v42
	v_mul_f32_e32 v42, 0xbfb8aa3b, v65
	v_exp_f32_e32 v42, v42
	s_nop 0
	v_add_f32_e32 v42, 1.0, v42
	v_rcp_f32_e32 v71, v42
	s_nop 0
	v_pk_mul_f32 v[86:87], v[64:65], v[70:71]
	v_lshlrev_b32_e32 v70, 16, v43
	v_and_b32_e32 v71, 0xffff0000, v43
	v_pk_fma_f32 v[42:43], v[24:25], v[50:51], v[40:41]
	v_lshlrev_b32_e32 v64, 16, v44
	v_pk_fma_f32 v[42:43], v[28:29], v[80:81], v[42:43]
	v_and_b32_e32 v65, 0xffff0000, v44
	v_pk_fma_f32 v[42:43], v[32:33], v[60:61], v[42:43]
	s_nop 0
	v_pk_fma_f32 v[42:43], v[36:37], v[70:71], v[42:43]
	s_nop 0
	v_mul_f32_e32 v46, 0xbfb8aa3b, v42
	v_exp_f32_e32 v46, v46
	s_nop 0
	v_add_f32_e32 v46, 1.0, v46
	v_rcp_f32_e32 v50, v46
	v_mul_f32_e32 v46, 0xbfb8aa3b, v43
	v_exp_f32_e32 v46, v46
	s_nop 0
	v_add_f32_e32 v46, 1.0, v46
	v_rcp_f32_e32 v51, v46
	s_nop 0
	v_pk_mul_f32 v[92:93], v[42:43], v[50:51]
	v_pk_fma_f32 v[42:43], v[24:25], v[80:81], v[40:41]
	s_nop 0
	v_pk_fma_f32 v[42:43], v[28:29], v[60:61], v[42:43]
	s_nop 0
	v_pk_fma_f32 v[42:43], v[32:33], v[70:71], v[42:43]
	s_nop 0
	v_pk_fma_f32 v[42:43], v[36:37], v[76:77], v[42:43]
	s_nop 0
	v_mul_f32_e32 v46, 0xbfb8aa3b, v42
	v_mul_f32_e32 v47, 0xbfb8aa3b, v43
	v_exp_f32_e32 v46, v46
	v_exp_f32_e32 v47, v47
	v_add_f32_e32 v46, 1.0, v46
	v_add_f32_e32 v47, 1.0, v47
	v_rcp_f32_e32 v46, v46
	v_rcp_f32_e32 v47, v47
	s_nop 0
	v_pk_mul_f32 v[46:47], v[42:43], v[46:47]
	v_pk_fma_f32 v[42:43], v[2:3], v[54:55], v[18:19]
	v_lshlrev_b32_e32 v54, 16, v48
	v_pk_fma_f32 v[42:43], v[6:7], v[88:89], v[42:43]
	v_and_b32_e32 v55, 0xffff0000, v48
	v_pk_fma_f32 v[42:43], v[10:11], v[58:59], v[42:43]
	s_nop 0
	v_pk_fma_f32 v[42:43], v[14:15], v[64:65], v[42:43]
	s_nop 0
	v_mul_f32_e32 v44, 0xbfb8aa3b, v42
	v_exp_f32_e32 v44, v44
	s_nop 0
	v_add_f32_e32 v44, 1.0, v44
	v_rcp_f32_e32 v50, v44
	v_mul_f32_e32 v44, 0xbfb8aa3b, v43
	v_exp_f32_e32 v44, v44
	s_nop 0
	v_add_f32_e32 v44, 1.0, v44
	v_rcp_f32_e32 v51, v44
	s_nop 0
	v_pk_mul_f32 v[80:81], v[42:43], v[50:51]
	v_pk_fma_f32 v[42:43], v[2:3], v[88:89], v[18:19]
	s_nop 0
	v_pk_fma_f32 v[42:43], v[6:7], v[58:59], v[42:43]
	s_nop 0
	v_pk_fma_f32 v[42:43], v[10:11], v[64:65], v[42:43]
	s_nop 0
	v_pk_fma_f32 v[42:43], v[14:15], v[54:55], v[42:43]
	s_nop 0
	v_mul_f32_e32 v44, 0xbfb8aa3b, v42
	v_exp_f32_e32 v44, v44
	s_nop 0
	v_add_f32_e32 v44, 1.0, v44
	v_rcp_f32_e32 v50, v44
	v_mul_f32_e32 v44, 0xbfb8aa3b, v43
	v_exp_f32_e32 v44, v44
	s_nop 0
	v_add_f32_e32 v44, 1.0, v44
	v_rcp_f32_e32 v51, v44
	s_nop 0
	v_pk_mul_f32 v[88:89], v[42:43], v[50:51]
	v_pk_fma_f32 v[42:43], v[4:5], v[52:53], v[20:21]
	v_lshlrev_b32_e32 v50, 16, v45
	v_pk_fma_f32 v[42:43], v[8:9], v[72:73], v[42:43]
	v_and_b32_e32 v51, 0xffff0000, v45
	v_pk_fma_f32 v[42:43], v[12:13], v[56:57], v[42:43]
	v_lshlrev_b32_e32 v52, 16, v49
	v_pk_fma_f32 v[42:43], v[16:17], v[50:51], v[42:43]
	v_and_b32_e32 v53, 0xffff0000, v49
	v_mul_f32_e32 v44, 0xbfb8aa3b, v42
	v_mul_f32_e32 v45, 0xbfb8aa3b, v43
	v_exp_f32_e32 v44, v44
	v_exp_f32_e32 v45, v45
	v_add_f32_e32 v44, 1.0, v44
	v_add_f32_e32 v45, 1.0, v45
	v_rcp_f32_e32 v44, v44
	v_rcp_f32_e32 v45, v45
	s_nop 0
	v_pk_mul_f32 v[94:95], v[42:43], v[44:45]
	v_pk_fma_f32 v[42:43], v[4:5], v[72:73], v[20:21]
	s_nop 0
	v_pk_fma_f32 v[42:43], v[8:9], v[56:57], v[42:43]
	s_nop 0
	v_pk_fma_f32 v[42:43], v[12:13], v[50:51], v[42:43]
	s_nop 0
	v_pk_fma_f32 v[42:43], v[16:17], v[52:53], v[42:43]
	s_nop 0
	v_mul_f32_e32 v44, 0xbfb8aa3b, v42
	v_mul_f32_e32 v45, 0xbfb8aa3b, v43
	v_exp_f32_e32 v44, v44
	v_exp_f32_e32 v45, v45
	v_add_f32_e32 v44, 1.0, v44
	v_add_f32_e32 v45, 1.0, v45
	v_rcp_f32_e32 v44, v44
	v_rcp_f32_e32 v45, v45
	s_nop 0
	v_pk_mul_f32 v[48:49], v[42:43], v[44:45]
	v_cvt_pk_bf16_f32 v42, v78, v79
	v_cvt_pk_bf16_f32 v43, v92, v93
	v_cvt_pk_bf16_f32 v44, v80, v81
	v_cvt_pk_bf16_f32 v45, v94, v95
	ds_write_b128 v90, v[42:45] offset:1088
	v_cvt_pk_bf16_f32 v42, v86, v87
	v_cvt_pk_bf16_f32 v43, v46, v47
	v_cvt_pk_bf16_f32 v44, v88, v89
	v_cvt_pk_bf16_f32 v45, v48, v49
	ds_write_b128 v90, v[42:45] offset:1360
	v_add_co_u32_e32 v42, vcc, s92, v62
	s_nop 1
	v_addc_co_u32_e32 v43, vcc, 0, v63, vcc
	global_load_dwordx4 v[46:49], v[42:43], off offset:1024
	v_add_co_u32_e32 v42, vcc, s93, v62
	s_waitcnt vmcnt(0)
; #define LAS __attribute__((address_space(3)))
; __device__ __forceinline__ unsigned pk2(float lo, float hi) { const f32x2 v = {lo, hi}; return __builtin_bit_cast(unsigned, __builtin_convertvector(v, hwbf16x2)); }
; __device__ __forceinline__ float fsigmoid(float x) { return __builtin_amdgcn_rcpf(1.0f + __expf(-x)); }
; __device__ __forceinline__ void unpack8(const v4u q, float (&d)[8]) { d[0] = bflo(q.x); d[1] = bfhi(q.x); d[2] = bflo(q.y); d[3] = bfhi(q.y); d[4] = bflo(q.z); d[5] = bfhi(q.z); d[6] = bflo(q.w); d[7] = bfhi(q.w); }
; template <bool TR, bool SCALE>
; __device__ __forceinline__ void conv_task(const Params& p, const bf16* proj, size_t trow0, int tl0, int run, int xcol, LAS bf16* dst, int d0, const LAS float* sc) {
;     ...
;     for (int i = 0; i < 8; i += 2) {
;         float r3[8], r4[8], o0[8], o1[8];
;         unpack8(*(const v4u*)(src + (size_t)i * PROJ_LD), r3); unpack8(*(const v4u*)(src + (size_t)(i + 1) * PROJ_LD), r4);
; #pragma unroll
;         for (int j = 0; j < 8; ++j) { const float a0 = bb[j] + w[0][j] * r0[j] + w[1][j] * r1[j] + w[2][j] * r2[j] + w[3][j] * r3[j];
;             const float a1 = bb[j] + w[0][j] * r1[j] + w[1][j] * r2[j] + w[2][j] * r3[j] + w[3][j] * r4[j];
;             o0[j] = a0 * fsigmoid(a0); o1[j] = a1 * fsigmoid(a1); }
;         if constexpr (TR) {
;             float s0 = 1.f, s1 = 1.f; if constexpr (SCALE) { s0 = sc[l0 + i]; s1 = sc[l0 + i + 1]; }
; #pragma unroll
;             for (int j = 0; j < 8; ++j) *(LAS unsigned*)(dst + (d0 + j) * SPT + l0 + i) = pk2(o0[j] * s0, o1[j] * s1);
;         } else {
;             *(LAS v4u*)(dst + (l0 + i) * SPT + d0) = (v4u){pk2(o0[0], o0[1]), pk2(o0[2], o0[3]), pk2(o0[4], o0[5]), pk2(o0[6], o0[7])};
;             *(LAS v4u*)(dst + (l0 + i + 1) * SPT + d0) = (v4u){pk2(o1[0], o1[1]), pk2(o1[2], o1[3]), pk2(o1[4], o1[5]), pk2(o1[6], o1[7])};
;         }
; #pragma unroll
;         for (int j = 0; j < 8; ++j) { r0[j] = r2[j]; r1[j] = r3[j]; r2[j] = r4[j]; }
	v_lshlrev_b32_e32 v72, 16, v46
	v_addc_co_u32_e32 v43, vcc, 0, v63, vcc
	global_load_dwordx4 v[42:45], v[42:43], off offset:512
	v_pk_fma_f32 v[62:63], v[22:23], v[66:67], v[38:39]
	v_and_b32_e32 v73, 0xffff0000, v46
	v_pk_fma_f32 v[62:63], v[26:27], v[68:69], v[62:63]
	v_pk_fma_f32 v[22:23], v[22:23], v[68:69], v[38:39]
	v_pk_fma_f32 v[62:63], v[30:31], v[74:75], v[62:63]
	v_pk_fma_f32 v[22:23], v[26:27], v[74:75], v[22:23]
	v_pk_fma_f32 v[62:63], v[34:35], v[72:73], v[62:63]
	v_pk_fma_f32 v[22:23], v[30:31], v[72:73], v[22:23]
	v_mul_f32_e32 v46, 0xbfb8aa3b, v62
	v_exp_f32_e32 v46, v46
	v_pk_fma_f32 v[30:31], v[24:25], v[60:61], v[40:41]
	v_pk_fma_f32 v[24:25], v[24:25], v[70:71], v[40:41]
	v_pk_fma_f32 v[30:31], v[28:29], v[70:71], v[30:31]
	v_add_f32_e32 v46, 1.0, v46
	v_rcp_f32_e32 v66, v46
	v_mul_f32_e32 v46, 0xbfb8aa3b, v63
	v_exp_f32_e32 v46, v46
	v_pk_fma_f32 v[30:31], v[32:33], v[76:77], v[30:31]
	v_pk_fma_f32 v[24:25], v[28:29], v[76:77], v[24:25]
	v_pk_fma_f32 v[28:29], v[2:3], v[58:59], v[18:19]
	v_add_f32_e32 v46, 1.0, v46
	v_rcp_f32_e32 v67, v46
	v_pk_fma_f32 v[28:29], v[6:7], v[64:65], v[28:29]
	v_pk_fma_f32 v[2:3], v[2:3], v[64:65], v[18:19]
	v_pk_fma_f32 v[28:29], v[10:11], v[54:55], v[28:29]
	v_pk_mul_f32 v[62:63], v[62:63], v[66:67]
	v_pk_fma_f32 v[2:3], v[6:7], v[54:55], v[2:3]
	s_waitcnt vmcnt(0)
	v_lshlrev_b32_e32 v66, 16, v42
	v_and_b32_e32 v67, 0xffff0000, v42
	v_pk_fma_f32 v[22:23], v[34:35], v[66:67], v[22:23]
	s_nop 0
	v_mul_f32_e32 v26, 0xbfb8aa3b, v22
	v_mul_f32_e32 v27, 0xbfb8aa3b, v23
	v_exp_f32_e32 v26, v26
	v_exp_f32_e32 v27, v27
	v_add_f32_e32 v26, 1.0, v26
	v_add_f32_e32 v27, 1.0, v27
	v_rcp_f32_e32 v26, v26
	v_rcp_f32_e32 v27, v27
	s_nop 0
	v_pk_mul_f32 v[22:23], v[22:23], v[26:27]
	v_lshlrev_b32_e32 v26, 16, v47
	v_and_b32_e32 v27, 0xffff0000, v47
	v_pk_fma_f32 v[30:31], v[36:37], v[26:27], v[30:31]
	v_pk_fma_f32 v[24:25], v[32:33], v[26:27], v[24:25]
	v_mul_f32_e32 v34, 0xbfb8aa3b, v30
	v_mul_f32_e32 v35, 0xbfb8aa3b, v31
	v_exp_f32_e32 v34, v34
	v_exp_f32_e32 v35, v35
	v_add_f32_e32 v34, 1.0, v34
	v_add_f32_e32 v35, 1.0, v35
	v_rcp_f32_e32 v34, v34
	v_rcp_f32_e32 v35, v35
	s_nop 0
	v_pk_mul_f32 v[30:31], v[30:31], v[34:35]
	v_lshlrev_b32_e32 v34, 16, v43
	v_and_b32_e32 v35, 0xffff0000, v43
	v_pk_fma_f32 v[24:25], v[36:37], v[34:35], v[24:25]
	s_nop 0
	v_mul_f32_e32 v26, 0xbfb8aa3b, v24
	v_mul_f32_e32 v27, 0xbfb8aa3b, v25
	v_exp_f32_e32 v26, v26
	v_exp_f32_e32 v27, v27
	v_add_f32_e32 v26, 1.0, v26
	v_add_f32_e32 v27, 1.0, v27
	v_rcp_f32_e32 v26, v26
	v_rcp_f32_e32 v27, v27
	s_nop 0
	v_pk_mul_f32 v[24:25], v[24:25], v[26:27]
	v_lshlrev_b32_e32 v26, 16, v48
	v_and_b32_e32 v27, 0xffff0000, v48
	v_pk_fma_f32 v[28:29], v[14:15], v[26:27], v[28:29]
	v_pk_fma_f32 v[2:3], v[10:11], v[26:27], v[2:3]
	v_mul_f32_e32 v32, 0xbfb8aa3b, v28
	v_mul_f32_e32 v33, 0xbfb8aa3b, v29
	v_exp_f32_e32 v32, v32
	v_exp_f32_e32 v33, v33
	v_pk_fma_f32 v[10:11], v[4:5], v[56:57], v[20:21]
	v_pk_fma_f32 v[4:5], v[4:5], v[50:51], v[20:21]
	v_add_f32_e32 v32, 1.0, v32
	v_add_f32_e32 v33, 1.0, v33
	v_rcp_f32_e32 v32, v32
	v_rcp_f32_e32 v33, v33
	v_pk_fma_f32 v[10:11], v[8:9], v[50:51], v[10:11]
	v_pk_fma_f32 v[4:5], v[8:9], v[52:53], v[4:5]
	v_pk_fma_f32 v[10:11], v[12:13], v[52:53], v[10:11]
	v_pk_mul_f32 v[28:29], v[28:29], v[32:33]
	v_lshlrev_b32_e32 v32, 16, v44
	v_and_b32_e32 v33, 0xffff0000, v44
	v_pk_fma_f32 v[2:3], v[14:15], v[32:33], v[2:3]
	s_nop 0
	v_mul_f32_e32 v6, 0xbfb8aa3b, v2
	v_mul_f32_e32 v7, 0xbfb8aa3b, v3
	v_exp_f32_e32 v6, v6
	v_exp_f32_e32 v7, v7
	v_add_f32_e32 v6, 1.0, v6
	v_add_f32_e32 v7, 1.0, v7
	v_rcp_f32_e32 v6, v6
	v_rcp_f32_e32 v7, v7
	s_nop 0
	v_pk_mul_f32 v[6:7], v[2:3], v[6:7]
	v_lshlrev_b32_e32 v2, 16, v49
	v_and_b32_e32 v3, 0xffff0000, v49
	v_pk_fma_f32 v[10:11], v[16:17], v[2:3], v[10:11]
	v_pk_fma_f32 v[2:3], v[12:13], v[2:3], v[4:5]
	v_mul_f32_e32 v14, 0xbfb8aa3b, v10
	v_mul_f32_e32 v15, 0xbfb8aa3b, v11
	v_exp_f32_e32 v14, v14
	v_exp_f32_e32 v15, v15
	v_add_f32_e32 v14, 1.0, v14
	v_add_f32_e32 v15, 1.0, v15
	v_rcp_f32_e32 v14, v14
	v_rcp_f32_e32 v15, v15
	s_nop 0
	v_pk_mul_f32 v[10:11], v[10:11], v[14:15]
	v_lshlrev_b32_e32 v14, 16, v45
	v_and_b32_e32 v15, 0xffff0000, v45
	v_pk_fma_f32 v[2:3], v[16:17], v[14:15], v[2:3]
	s_nop 0
	v_mul_f32_e32 v4, 0xbfb8aa3b, v2
	v_mul_f32_e32 v5, 0xbfb8aa3b, v3
	v_exp_f32_e32 v4, v4
	v_exp_f32_e32 v5, v5
	v_add_f32_e32 v4, 1.0, v4
	v_add_f32_e32 v5, 1.0, v5
	v_rcp_f32_e32 v4, v4
	v_rcp_f32_e32 v5, v5
	s_nop 0
	v_pk_mul_f32 v[8:9], v[2:3], v[4:5]
	v_cvt_pk_bf16_f32 v2, v62, v63
	v_cvt_pk_bf16_f32 v3, v30, v31
	v_cvt_pk_bf16_f32 v4, v28, v29
	v_cvt_pk_bf16_f32 v5, v10, v11
	ds_write_b128 v90, v[2:5] offset:1632
	v_cvt_pk_bf16_f32 v2, v22, v23
	v_cvt_pk_bf16_f32 v3, v24, v25
	v_cvt_pk_bf16_f32 v4, v6, v7
	v_cvt_pk_bf16_f32 v5, v8, v9
	ds_write_b128 v90, v[2:5] offset:1904

; #define LAS __attribute__((address_space(3)))
; __device__ __forceinline__ unsigned pk2(float lo, float hi) { const f32x2 v = {lo, hi}; return __builtin_bit_cast(unsigned, __builtin_convertvector(v, hwbf16x2)); }
; __device__ __forceinline__ float fsigmoid(float x) { return __builtin_amdgcn_rcpf(1.0f + __expf(-x)); }
; __device__ __forceinline__ void unpack8(const v4u q, float (&d)[8]) { d[0] = bflo(q.x); d[1] = bfhi(q.x); d[2] = bflo(q.y); d[3] = bfhi(q.y); d[4] = bflo(q.z); d[5] = bfhi(q.z); d[6] = bflo(q.w); d[7] = bfhi(q.w); }
; template <bool TR, bool SCALE>
; __device__ __forceinline__ void conv_task(const Params& p, const bf16* proj, size_t trow0, int tl0, int run, int xcol, LAS bf16* dst, int d0, const LAS float* sc) {
;     ...
;     const int l0 = run * 8; const bf16* src = proj + (trow0 + l0) * PROJ_LD + COL_XBC + xcol;
;     float r0[8], r1[8], r2[8];
;     { const int pos = tl0 + l0; v4u q0 = (v4u){0u, 0u, 0u, 0u}, q1 = q0, q2 = q0;
;       if (pos - 3 >= 0) q0 = *(const v4u*)(src - 3 * PROJ_LD);
;       if (pos - 2 >= 0) q1 = *(const v4u*)(src - 2 * PROJ_LD);
;       if (pos - 1 >= 0) q2 = *(const v4u*)(src - 1 * PROJ_LD);
;       unpack8(q0, r0); unpack8(q1, r1); unpack8(q2, r2); }
; #pragma unroll
;     for (int i = 0; i < 8; i += 2) {
;         float r3[8], r4[8], o0[8], o1[8];
;         unpack8(*(const v4u*)(src + (size_t)i * PROJ_LD), r3); unpack8(*(const v4u*)(src + (size_t)(i + 1) * PROJ_LD), r4);
; #pragma unroll
;         for (int j = 0; j < 8; ++j) { const float a0 = bb[j] + w[0][j] * r0[j] + w[1][j] * r1[j] + w[2][j] * r2[j] + w[3][j] * r3[j];
;             const float a1 = bb[j] + w[0][j] * r1[j] + w[1][j] * r2[j] + w[2][j] * r3[j] + w[3][j] * r4[j];
;             o0[j] = a0 * fsigmoid(a0); o1[j] = a1 * fsigmoid(a1); }
;         if constexpr (TR) {
;             float s0 = 1.f, s1 = 1.f; if constexpr (SCALE) { s0 = sc[l0 + i]; s1 = sc[l0 + i + 1]; }
; #pragma unroll
;             for (int j = 0; j < 8; ++j) *(LAS unsigned*)(dst + (d0 + j) * SPT + l0 + i) = pk2(o0[j] * s0, o1[j] * s1);
.LBB0_454:
	s_or_b64 exec, exec, s[12:13]
	v_add_co_u32_e32 v58, vcc, s78, v80
	global_load_dwordx4 v[54:57], v[80:81], off
	s_nop 0
	v_addc_co_u32_e32 v59, vcc, 0, v81, vcc
	global_load_dwordx4 v[58:61], v[58:59], off offset:3584
	v_add_co_u32_e32 v248, vcc, s79, v80
	s_nop 1
	v_addc_co_u32_e32 v249, vcc, 0, v81, vcc
	global_load_dword v246, v[248:249], off offset:3072
	v_add_co_u32_e32 v248, vcc, s81, v80
	s_nop 1
	v_addc_co_u32_e32 v249, vcc, 0, v81, vcc
	global_load_dword v246, v[248:249], off offset:2560
	v_add_co_u32_e32 v248, vcc, s82, v80
	s_nop 1
	v_addc_co_u32_e32 v249, vcc, 0, v81, vcc
	global_load_dword v246, v[248:249], off offset:2048
	v_add_co_u32_e32 v248, vcc, s83, v80
	s_nop 1
	v_addc_co_u32_e32 v249, vcc, 0, v81, vcc
	global_load_dword v246, v[248:249], off offset:1536
	v_add_co_u32_e32 v248, vcc, s92, v80
	s_nop 1
	v_addc_co_u32_e32 v249, vcc, 0, v81, vcc
	global_load_dword v246, v[248:249], off offset:1024
	v_add_co_u32_e32 v248, vcc, s93, v80
	s_nop 1
	v_addc_co_u32_e32 v249, vcc, 0, v81, vcc
	global_load_dword v246, v[248:249], off offset:512
	s_waitcnt vmcnt(2)
	v_lshlrev_b32_e32 v63, 16, v46
	v_lshlrev_b32_e32 v62, 16, v42
	v_lshlrev_b32_e32 v64, 16, v50
	v_mov_b32_e32 v66, v63
	v_mov_b32_e32 v67, v64
	v_pk_fma_f32 v[62:63], v[22:23], v[62:63], v[38:39] op_sel_hi:[0,1,0]
	v_pk_fma_f32 v[62:63], v[26:27], v[66:67], v[62:63] op_sel_hi:[0,1,1]
	v_and_b32_e32 v73, 0xffff0000, v50
	v_mov_b32_e32 v118, v73
	v_lshlrev_b32_e32 v122, 16, v51
	v_mov_b32_e32 v75, v122
	v_mov_b32_e32 v86, v25
	v_mov_b32_e32 v88, v41
	v_mov_b32_e32 v90, v29
	v_mov_b32_e32 v92, v33
	v_mov_b32_e32 v94, v37
	v_lshlrev_b32_e32 v130, 16, v52
	v_mov_b32_e32 v108, v3
	v_mov_b32_e32 v110, v19
	v_mov_b32_e32 v112, v7
	v_mov_b32_e32 v114, v11
	v_mov_b32_e32 v116, v15
	v_lshlrev_b32_e32 v140, 16, v53
	v_mov_b32_e32 v98, v5
	v_mov_b32_e32 v100, v21
	v_mov_b32_e32 v102, v9
	v_mov_b32_e32 v104, v13
	v_mov_b32_e32 v106, v17
	v_mad_u64_u32 v[96:97], s[12:13], v71, s80, v[84:85]
	s_waitcnt vmcnt(1)
	v_lshlrev_b32_e32 v65, 16, v54
	v_mov_b32_e32 v68, v65
	v_pk_fma_f32 v[62:63], v[30:31], v[64:65], v[62:63] op_sel_hi:[0,1,1]
	s_waitcnt vmcnt(0)
	v_lshlrev_b32_e32 v69, 16, v58
	v_pk_fma_f32 v[62:63], v[34:35], v[68:69], v[62:63] op_sel_hi:[0,1,1]
	v_mul_f32_e32 v66, 0xbfb8aa3b, v62
	v_mul_f32_e32 v67, 0xbfb8aa3b, v63
	v_exp_f32_e32 v66, v66
	v_exp_f32_e32 v67, v67
	v_and_b32_e32 v119, 0xffff0000, v54
	v_and_b32_e32 v121, 0xffff0000, v58
	v_add_f32_e32 v66, 1.0, v66
	v_add_f32_e32 v67, 1.0, v67
	v_rcp_f32_e32 v66, v66
	v_rcp_f32_e32 v67, v67
	v_mov_b32_e32 v120, v119
	v_lshlrev_b32_e32 v123, 16, v55
	v_lshlrev_b32_e32 v125, 16, v59
	v_pk_mul_f32 v[62:63], v[62:63], v[66:67]
	v_and_b32_e32 v67, 0xffff0000, v46
	v_and_b32_e32 v66, 0xffff0000, v42
	v_mov_b32_e32 v72, v67
	v_pk_fma_f32 v[66:67], v[22:23], v[66:67], v[38:39] op_sel:[1,0,1]
	v_mov_b32_e32 v124, v123
	v_pk_fma_f32 v[66:67], v[26:27], v[72:73], v[66:67] op_sel:[1,0,0]
	v_and_b32_e32 v46, 0xffff0000, v43
	v_pk_fma_f32 v[66:67], v[30:31], v[118:119], v[66:67] op_sel:[1,0,0]
	v_and_b32_e32 v127, 0xffff0000, v55
	v_pk_fma_f32 v[66:67], v[34:35], v[120:121], v[66:67] op_sel:[1,0,0]
	v_and_b32_e32 v129, 0xffff0000, v59
	v_mul_f32_e32 v42, 0xbfb8aa3b, v66
	v_exp_f32_e32 v42, v42
	v_mov_b32_e32 v128, v127
	v_lshlrev_b32_e32 v131, 16, v56
	v_lshlrev_b32_e32 v133, 16, v60
	v_add_f32_e32 v42, 1.0, v42
	v_rcp_f32_e32 v72, v42
	v_mul_f32_e32 v42, 0xbfb8aa3b, v67
	v_exp_f32_e32 v42, v42
	v_mov_b32_e32 v132, v131
	v_and_b32_e32 v55, 0xffff0000, v52
	v_and_b32_e32 v135, 0xffff0000, v56
	v_add_f32_e32 v42, 1.0, v42
	v_rcp_f32_e32 v73, v42
	v_mov_b32_e32 v134, v55
	v_and_b32_e32 v137, 0xffff0000, v60
	v_mov_b32_e32 v136, v135
	v_pk_mul_f32 v[66:67], v[66:67], v[72:73]
	v_lshlrev_b32_e32 v72, 16, v43
	v_lshlrev_b32_e32 v73, 16, v47
	v_mov_b32_e32 v74, v73
	v_pk_fma_f32 v[72:73], v[24:25], v[72:73], v[40:41] op_sel_hi:[0,1,0]
	v_pk_fma_f32 v[72:73], v[28:29], v[74:75], v[72:73] op_sel_hi:[0,1,1]
	v_pk_fma_f32 v[72:73], v[32:33], v[122:123], v[72:73] op_sel_hi:[0,1,1]
	v_pk_fma_f32 v[72:73], v[36:37], v[124:125], v[72:73] op_sel_hi:[0,1,1]
	v_mul_f32_e32 v42, 0xbfb8aa3b, v72
	v_exp_f32_e32 v42, v42
	v_and_b32_e32 v47, 0xffff0000, v47
	v_and_b32_e32 v43, 0xffff0000, v51
	v_mov_b32_e32 v126, v43
	v_add_f32_e32 v42, 1.0, v42
	v_rcp_f32_e32 v74, v42
	v_mul_f32_e32 v42, 0xbfb8aa3b, v73
	v_exp_f32_e32 v42, v42
	v_mov_b32_e32 v51, v130
	v_mov_b32_e32 v59, v140
	v_lshlrev_b32_e32 v141, 16, v57
	v_add_f32_e32 v42, 1.0, v42
	v_rcp_f32_e32 v75, v42
	v_mov_b32_e32 v42, v47
	v_pk_fma_f32 v[46:47], v[86:87], v[46:47], v[88:89] op_sel_hi:[0,1,0]
	v_pk_fma_f32 v[42:43], v[90:91], v[42:43], v[46:47] op_sel_hi:[0,1,1]
	v_pk_fma_f32 v[42:43], v[92:93], v[126:127], v[42:43] op_sel_hi:[0,1,1]
	v_pk_fma_f32 v[42:43], v[94:95], v[128:129], v[42:43] op_sel_hi:[0,1,1]
	v_mul_f32_e32 v46, 0xbfb8aa3b, v42
	v_mul_f32_e32 v47, 0xbfb8aa3b, v43
	v_exp_f32_e32 v46, v46
	v_exp_f32_e32 v47, v47
	v_lshlrev_b32_e32 v143, 16, v61
	v_mov_b32_e32 v142, v141
	v_add_f32_e32 v46, 1.0, v46
	v_add_f32_e32 v47, 1.0, v47
	v_rcp_f32_e32 v46, v46
	v_rcp_f32_e32 v47, v47
	v_and_b32_e32 v149, 0xffff0000, v57
	v_and_b32_e32 v151, 0xffff0000, v61
	v_mov_b32_e32 v150, v149
	v_pk_mul_f32 v[42:43], v[42:43], v[46:47]
	v_lshlrev_b32_e32 v47, 16, v48
	v_lshlrev_b32_e32 v46, 16, v44
	v_mov_b32_e32 v50, v47
	v_pk_fma_f32 v[46:47], v[2:3], v[46:47], v[18:19] op_sel_hi:[0,1,0]
	v_pk_fma_f32 v[46:47], v[6:7], v[50:51], v[46:47] op_sel_hi:[0,1,1]
	v_pk_fma_f32 v[46:47], v[10:11], v[130:131], v[46:47] op_sel_hi:[0,1,1]
	v_pk_fma_f32 v[46:47], v[14:15], v[132:133], v[46:47] op_sel_hi:[0,1,1]
; #define LAS __attribute__((address_space(3)))
; __device__ __forceinline__ unsigned pk2(float lo, float hi) { const f32x2 v = {lo, hi}; return __builtin_bit_cast(unsigned, __builtin_convertvector(v, hwbf16x2)); }
; __device__ __forceinline__ float fsigmoid(float x) { return __builtin_amdgcn_rcpf(1.0f + __expf(-x)); }
; __device__ __forceinline__ void unpack8(const v4u q, float (&d)[8]) { d[0] = bflo(q.x); d[1] = bfhi(q.x); d[2] = bflo(q.y); d[3] = bfhi(q.y); d[4] = bflo(q.z); d[5] = bfhi(q.z); d[6] = bflo(q.w); d[7] = bfhi(q.w); }
; template <bool TR, bool SCALE>
; __device__ __forceinline__ void conv_task(const Params& p, const bf16* proj, size_t trow0, int tl0, int run, int xcol, LAS bf16* dst, int d0, const LAS float* sc) {
;     ...
;     for (int i = 0; i < 8; i += 2) {
;         float r3[8], r4[8], o0[8], o1[8];
;         unpack8(*(const v4u*)(src + (size_t)i * PROJ_LD), r3); unpack8(*(const v4u*)(src + (size_t)(i + 1) * PROJ_LD), r4);
; #pragma unroll
;         for (int j = 0; j < 8; ++j) { const float a0 = bb[j] + w[0][j] * r0[j] + w[1][j] * r1[j] + w[2][j] * r2[j] + w[3][j] * r3[j];
;             const float a1 = bb[j] + w[0][j] * r1[j] + w[1][j] * r2[j] + w[2][j] * r3[j] + w[3][j] * r4[j];
;             o0[j] = a0 * fsigmoid(a0); o1[j] = a1 * fsigmoid(a1); }
;         if constexpr (TR) {
;             float s0 = 1.f, s1 = 1.f; if constexpr (SCALE) { s0 = sc[l0 + i]; s1 = sc[l0 + i + 1]; }
; #pragma unroll
;             for (int j = 0; j < 8; ++j) *(LAS unsigned*)(dst + (d0 + j) * SPT + l0 + i) = pk2(o0[j] * s0, o1[j] * s1);
;         } else {
;             *(LAS v4u*)(dst + (l0 + i) * SPT + d0) = (v4u){pk2(o0[0], o0[1]), pk2(o0[2], o0[3]), pk2(o0[4], o0[5]), pk2(o0[6], o0[7])};
;             *(LAS v4u*)(dst + (l0 + i + 1) * SPT + d0) = (v4u){pk2(o1[0], o1[1]), pk2(o1[2], o1[3]), pk2(o1[4], o1[5]), pk2(o1[6], o1[7])};
;         }
; #pragma unroll
;         for (int j = 0; j < 8; ++j) { r0[j] = r2[j]; r1[j] = r3[j]; r2[j] = r4[j]; }
	v_mul_f32_e32 v50, 0xbfb8aa3b, v46
	v_mul_f32_e32 v51, 0xbfb8aa3b, v47
	v_exp_f32_e32 v50, v50
	v_exp_f32_e32 v51, v51
	v_pk_mul_f32 v[72:73], v[72:73], v[74:75]
	v_cvt_pk_bf16_f32 v70, v62, v63
	v_add_f32_e32 v50, 1.0, v50
	v_add_f32_e32 v51, 1.0, v51
	v_rcp_f32_e32 v50, v50
	v_rcp_f32_e32 v51, v51
	v_cvt_pk_bf16_f32 v62, v72, v73
	v_cvt_pk_bf16_f32 v66, v66, v67
	v_pk_mul_f32 v[46:47], v[46:47], v[50:51]
	v_and_b32_e32 v51, 0xffff0000, v48
	v_and_b32_e32 v50, 0xffff0000, v44
	v_mov_b32_e32 v54, v51
	v_pk_fma_f32 v[50:51], v[108:109], v[50:51], v[110:111] op_sel_hi:[0,1,0]
	v_pk_fma_f32 v[50:51], v[112:113], v[54:55], v[50:51] op_sel_hi:[0,1,1]
	v_pk_fma_f32 v[50:51], v[114:115], v[134:135], v[50:51] op_sel_hi:[0,1,1]
	v_pk_fma_f32 v[50:51], v[116:117], v[136:137], v[50:51] op_sel_hi:[0,1,1]
	v_mul_f32_e32 v3, 0xbfb8aa3b, v50
	v_exp_f32_e32 v3, v3
	v_and_b32_e32 v48, 0xffff0000, v45
	v_add_f32_e32 v3, 1.0, v3
	v_rcp_f32_e32 v54, v3
	v_mul_f32_e32 v3, 0xbfb8aa3b, v51
	v_exp_f32_e32 v3, v3
	s_nop 0
	v_add_f32_e32 v3, 1.0, v3
	v_rcp_f32_e32 v55, v3
	s_nop 0
	v_pk_mul_f32 v[50:51], v[50:51], v[54:55]
	v_lshlrev_b32_e32 v54, 16, v45
	v_lshlrev_b32_e32 v55, 16, v49
	v_mov_b32_e32 v58, v55
	v_pk_fma_f32 v[54:55], v[4:5], v[54:55], v[20:21] op_sel_hi:[0,1,0]
	v_pk_fma_f32 v[54:55], v[8:9], v[58:59], v[54:55] op_sel_hi:[0,1,1]
	v_pk_fma_f32 v[54:55], v[12:13], v[140:141], v[54:55] op_sel_hi:[0,1,1]
	v_pk_fma_f32 v[54:55], v[16:17], v[142:143], v[54:55] op_sel_hi:[0,1,1]
	v_mul_f32_e32 v3, 0xbfb8aa3b, v54
	v_exp_f32_e32 v3, v3
	v_and_b32_e32 v49, 0xffff0000, v49
	v_and_b32_e32 v45, 0xffff0000, v53
	v_mov_b32_e32 v44, v49
	v_add_f32_e32 v3, 1.0, v3
	v_rcp_f32_e32 v58, v3
	v_mul_f32_e32 v3, 0xbfb8aa3b, v55
	v_exp_f32_e32 v3, v3
	v_pk_fma_f32 v[48:49], v[98:99], v[48:49], v[100:101] op_sel_hi:[0,1,0]
	v_mov_b32_e32 v148, v45
	v_pk_fma_f32 v[44:45], v[102:103], v[44:45], v[48:49] op_sel_hi:[0,1,1]
	v_pk_fma_f32 v[44:45], v[104:105], v[148:149], v[44:45] op_sel_hi:[0,1,1]
	v_add_f32_e32 v3, 1.0, v3
	v_pk_fma_f32 v[44:45], v[106:107], v[150:151], v[44:45] op_sel_hi:[0,1,1]
	v_rcp_f32_e32 v59, v3
	v_mul_f32_e32 v3, 0xbfb8aa3b, v44
	v_exp_f32_e32 v3, v3
	v_cvt_pk_bf16_f32 v50, v50, v51
	v_pk_mul_f32 v[74:75], v[54:55], v[58:59]
	v_cvt_pk_bf16_f32 v58, v42, v43
	v_add_f32_e32 v3, 1.0, v3
	v_rcp_f32_e32 v48, v3
	v_mul_f32_e32 v3, 0xbfb8aa3b, v45
	v_exp_f32_e32 v3, v3
	v_cvt_pk_bf16_f32 v54, v46, v47
	v_cvt_pk_bf16_f32 v46, v74, v75
	v_add_f32_e32 v3, 1.0, v3
	v_rcp_f32_e32 v49, v3
	s_nop 0
	v_pk_mul_f32 v[44:45], v[44:45], v[48:49]
	s_nop 0
	v_cvt_pk_bf16_f32 v42, v44, v45
	v_add_co_u32_e32 v44, vcc, s79, v80
	s_nop 1
	v_addc_co_u32_e32 v45, vcc, 0, v81, vcc
	global_load_dwordx4 v[72:75], v[44:45], off offset:3072
	v_add_co_u32_e32 v44, vcc, s81, v80
	s_waitcnt vmcnt(0)
	v_lshlrev_b32_e32 v146, 16, v72
	v_addc_co_u32_e32 v45, vcc, 0, v81, vcc
	global_load_dwordx4 v[76:79], v[44:45], off offset:2560
	v_pk_fma_f32 v[44:45], v[22:23], v[64:65], v[38:39] op_sel_hi:[0,1,0]
	v_pk_fma_f32 v[44:45], v[26:27], v[68:69], v[44:45] op_sel_hi:[0,1,1]
	v_and_b32_e32 v60, 0xffff0000, v72
	v_lshlrev_b32_e32 v144, 16, v73
	v_and_b32_e32 v64, 0xffff0000, v73
	v_lshlrev_b32_e32 v56, 16, v74
	s_waitcnt vmcnt(0)
	v_lshlrev_b32_e32 v147, 16, v76
	v_pk_mov_b32 v[152:153], v[68:69], v[146:147] op_sel:[1,0]
	v_and_b32_e32 v61, 0xffff0000, v76
	v_pk_fma_f32 v[44:45], v[30:31], v[152:153], v[44:45] op_sel_hi:[0,1,1]
	v_pk_fma_f32 v[44:45], v[34:35], v[146:147], v[44:45] op_sel_hi:[0,1,1]
	v_mul_f32_e32 v3, 0xbfb8aa3b, v44
	v_exp_f32_e32 v3, v3
	v_pk_mov_b32 v[154:155], v[120:121], v[60:61] op_sel:[1,0]
	v_lshlrev_b32_e32 v145, 16, v77
	v_and_b32_e32 v65, 0xffff0000, v77
	v_add_f32_e32 v3, 1.0, v3
	v_rcp_f32_e32 v48, v3
	v_mul_f32_e32 v3, 0xbfb8aa3b, v45
	v_exp_f32_e32 v3, v3
	v_lshlrev_b32_e32 v57, 16, v78
	v_pk_mov_b32 v[68:69], v[132:133], v[56:57] op_sel:[1,0]
	v_add_f32_e32 v3, 1.0, v3
	v_rcp_f32_e32 v49, v3
	s_nop 0
	v_pk_mul_f32 v[156:157], v[44:45], v[48:49]
	v_pk_fma_f32 v[44:45], v[22:23], v[118:119], v[38:39] op_sel:[1,0,1]
	v_cvt_pk_bf16_f32 v71, v156, v157
	v_pk_fma_f32 v[44:45], v[26:27], v[120:121], v[44:45] op_sel:[1,0,0]
	s_nop 0
	v_pk_fma_f32 v[44:45], v[30:31], v[154:155], v[44:45] op_sel:[1,0,0]
	s_nop 0
	v_pk_fma_f32 v[44:45], v[34:35], v[60:61], v[44:45] op_sel:[1,0,0]
	s_nop 0
	v_mul_f32_e32 v3, 0xbfb8aa3b, v44
	v_exp_f32_e32 v3, v3
	s_nop 0
	v_add_f32_e32 v3, 1.0, v3
	v_rcp_f32_e32 v48, v3
	v_mul_f32_e32 v3, 0xbfb8aa3b, v45
	v_exp_f32_e32 v3, v3
	s_nop 0
	v_add_f32_e32 v3, 1.0, v3
	v_rcp_f32_e32 v49, v3
	s_nop 0
	v_pk_mul_f32 v[158:159], v[44:45], v[48:49]
	v_pk_fma_f32 v[44:45], v[24:25], v[122:123], v[40:41] op_sel_hi:[0,1,0]
	v_pk_fma_f32 v[44:45], v[28:29], v[124:125], v[44:45] op_sel_hi:[0,1,1]
	v_pk_mov_b32 v[122:123], v[124:125], v[144:145] op_sel:[1,0]
	v_pk_mov_b32 v[124:125], v[128:129], v[64:65] op_sel:[1,0]
	v_pk_fma_f32 v[44:45], v[32:33], v[122:123], v[44:45] op_sel_hi:[0,1,1]
	v_pk_fma_f32 v[44:45], v[36:37], v[144:145], v[44:45] op_sel_hi:[0,1,1]
	v_mul_f32_e32 v3, 0xbfb8aa3b, v44
	v_exp_f32_e32 v3, v3
	v_pk_fma_f32 v[122:123], v[24:25], v[122:123], v[40:41] op_sel_hi:[0,1,0]
	v_pk_fma_f32 v[122:123], v[28:29], v[144:145], v[122:123] op_sel_hi:[0,1,1]
	v_cvt_pk_bf16_f32 v67, v158, v159
	v_add_f32_e32 v3, 1.0, v3
	v_rcp_f32_e32 v48, v3
	v_mul_f32_e32 v3, 0xbfb8aa3b, v45
	v_exp_f32_e32 v3, v3
	s_nop 0
	v_add_f32_e32 v3, 1.0, v3
	v_rcp_f32_e32 v49, v3
	s_nop 0
	v_pk_mul_f32 v[160:161], v[44:45], v[48:49]
	v_pk_fma_f32 v[44:45], v[86:87], v[126:127], v[88:89] op_sel_hi:[0,1,0]
	v_pk_fma_f32 v[44:45], v[90:91], v[128:129], v[44:45] op_sel_hi:[0,1,1]
; #define LAS __attribute__((address_space(3)))
; __device__ __forceinline__ unsigned pk2(float lo, float hi) { const f32x2 v = {lo, hi}; return __builtin_bit_cast(unsigned, __builtin_convertvector(v, hwbf16x2)); }
; __device__ __forceinline__ float fsigmoid(float x) { return __builtin_amdgcn_rcpf(1.0f + __expf(-x)); }
; __device__ __forceinline__ void unpack8(const v4u q, float (&d)[8]) { d[0] = bflo(q.x); d[1] = bfhi(q.x); d[2] = bflo(q.y); d[3] = bfhi(q.y); d[4] = bflo(q.z); d[5] = bfhi(q.z); d[6] = bflo(q.w); d[7] = bfhi(q.w); }
; template <bool TR, bool SCALE>
; __device__ __forceinline__ void conv_task(const Params& p, const bf16* proj, size_t trow0, int tl0, int run, int xcol, LAS bf16* dst, int d0, const LAS float* sc) {
;     ...
;     for (int i = 0; i < 8; i += 2) {
;         float r3[8], r4[8], o0[8], o1[8];
;         unpack8(*(const v4u*)(src + (size_t)i * PROJ_LD), r3); unpack8(*(const v4u*)(src + (size_t)(i + 1) * PROJ_LD), r4);
; #pragma unroll
;         for (int j = 0; j < 8; ++j) { const float a0 = bb[j] + w[0][j] * r0[j] + w[1][j] * r1[j] + w[2][j] * r2[j] + w[3][j] * r3[j];
;             const float a1 = bb[j] + w[0][j] * r1[j] + w[1][j] * r2[j] + w[2][j] * r3[j] + w[3][j] * r4[j];
;             o0[j] = a0 * fsigmoid(a0); o1[j] = a1 * fsigmoid(a1); }
;         if constexpr (TR) {
;             float s0 = 1.f, s1 = 1.f; if constexpr (SCALE) { s0 = sc[l0 + i]; s1 = sc[l0 + i + 1]; }
; #pragma unroll
;             for (int j = 0; j < 8; ++j) *(LAS unsigned*)(dst + (d0 + j) * SPT + l0 + i) = pk2(o0[j] * s0, o1[j] * s1);
;         } else {
;             *(LAS v4u*)(dst + (l0 + i) * SPT + d0) = (v4u){pk2(o0[0], o0[1]), pk2(o0[2], o0[3]), pk2(o0[4], o0[5]), pk2(o0[6], o0[7])};
;             *(LAS v4u*)(dst + (l0 + i + 1) * SPT + d0) = (v4u){pk2(o1[0], o1[1]), pk2(o1[2], o1[3]), pk2(o1[4], o1[5]), pk2(o1[6], o1[7])};
;         }
; #pragma unroll
;         for (int j = 0; j < 8; ++j) { r0[j] = r2[j]; r1[j] = r3[j]; r2[j] = r4[j]; }
	v_pk_fma_f32 v[44:45], v[92:93], v[124:125], v[44:45] op_sel_hi:[0,1,1]
	v_pk_fma_f32 v[44:45], v[94:95], v[64:65], v[44:45] op_sel_hi:[0,1,1]
	v_mul_f32_e32 v3, 0xbfb8aa3b, v44
	v_exp_f32_e32 v3, v3
	v_cvt_pk_bf16_f32 v63, v160, v161
	v_add_f32_e32 v3, 1.0, v3
	v_rcp_f32_e32 v48, v3
	v_mul_f32_e32 v3, 0xbfb8aa3b, v45
	v_exp_f32_e32 v3, v3
	s_nop 0
	v_add_f32_e32 v3, 1.0, v3
	v_rcp_f32_e32 v49, v3
	s_nop 0
	v_pk_mul_f32 v[72:73], v[44:45], v[48:49]
	v_pk_fma_f32 v[44:45], v[2:3], v[130:131], v[18:19] op_sel_hi:[0,1,0]
	v_pk_fma_f32 v[44:45], v[6:7], v[132:133], v[44:45] op_sel_hi:[0,1,1]
	v_pk_fma_f32 v[44:45], v[10:11], v[68:69], v[44:45] op_sel_hi:[0,1,1]
	v_pk_fma_f32 v[44:45], v[14:15], v[56:57], v[44:45] op_sel_hi:[0,1,1]
	v_mul_f32_e32 v3, 0xbfb8aa3b, v44
	v_exp_f32_e32 v3, v3
	v_cvt_pk_bf16_f32 v59, v72, v73
	v_add_co_u32_e32 v72, vcc, s82, v80
	v_add_f32_e32 v3, 1.0, v3
	v_rcp_f32_e32 v48, v3
	v_mul_f32_e32 v3, 0xbfb8aa3b, v45
	v_exp_f32_e32 v3, v3
	v_addc_co_u32_e32 v73, vcc, 0, v81, vcc
	v_add_f32_e32 v3, 1.0, v3
	v_rcp_f32_e32 v49, v3
	s_nop 0
	v_pk_mul_f32 v[76:77], v[44:45], v[48:49]
	v_and_b32_e32 v45, 0xffff0000, v78
	v_and_b32_e32 v44, 0xffff0000, v74
	v_pk_fma_f32 v[48:49], v[108:109], v[134:135], v[110:111] op_sel_hi:[0,1,0]
	v_pk_fma_f32 v[48:49], v[112:113], v[136:137], v[48:49] op_sel_hi:[0,1,1]
	v_pk_mov_b32 v[118:119], v[136:137], v[44:45] op_sel:[1,0]
	v_cvt_pk_bf16_f32 v55, v76, v77
	v_pk_fma_f32 v[48:49], v[114:115], v[118:119], v[48:49] op_sel_hi:[0,1,1]
	v_pk_fma_f32 v[48:49], v[116:117], v[44:45], v[48:49] op_sel_hi:[0,1,1]
	v_mul_f32_e32 v3, 0xbfb8aa3b, v48
	v_exp_f32_e32 v3, v3
	v_add_co_u32_e32 v76, vcc, s83, v80
	v_add_f32_e32 v3, 1.0, v3
	v_rcp_f32_e32 v52, v3
	v_mul_f32_e32 v3, 0xbfb8aa3b, v49
	v_exp_f32_e32 v3, v3
	v_addc_co_u32_e32 v77, vcc, 0, v81, vcc
	v_add_f32_e32 v3, 1.0, v3
	v_rcp_f32_e32 v53, v3
	s_nop 0
	v_pk_mul_f32 v[126:127], v[48:49], v[52:53]
	v_lshlrev_b32_e32 v53, 16, v79
	v_lshlrev_b32_e32 v52, 16, v75
	v_pk_fma_f32 v[48:49], v[4:5], v[140:141], v[20:21] op_sel_hi:[0,1,0]
	v_pk_fma_f32 v[48:49], v[8:9], v[142:143], v[48:49] op_sel_hi:[0,1,1]
	v_pk_mov_b32 v[120:121], v[142:143], v[52:53] op_sel:[1,0]
	v_cvt_pk_bf16_f32 v51, v126, v127
	v_pk_fma_f32 v[48:49], v[12:13], v[120:121], v[48:49] op_sel_hi:[0,1,1]
	v_pk_fma_f32 v[48:49], v[16:17], v[52:53], v[48:49] op_sel_hi:[0,1,1]
	v_mul_f32_e32 v3, 0xbfb8aa3b, v48
	v_exp_f32_e32 v3, v3
	v_pk_fma_f32 v[126:127], v[22:23], v[152:153], v[38:39] op_sel_hi:[0,1,0]
	v_pk_fma_f32 v[126:127], v[26:27], v[146:147], v[126:127] op_sel_hi:[0,1,1]
	v_add_f32_e32 v3, 1.0, v3
	v_rcp_f32_e32 v128, v3
	v_mul_f32_e32 v3, 0xbfb8aa3b, v49
	v_exp_f32_e32 v3, v3
	s_nop 0
	v_add_f32_e32 v3, 1.0, v3
	v_rcp_f32_e32 v129, v3
	s_nop 0
	v_pk_mul_f32 v[128:129], v[48:49], v[128:129]
	v_and_b32_e32 v49, 0xffff0000, v79
	v_and_b32_e32 v48, 0xffff0000, v75
	v_pk_fma_f32 v[74:75], v[98:99], v[148:149], v[100:101] op_sel_hi:[0,1,0]
	v_pk_fma_f32 v[74:75], v[102:103], v[150:151], v[74:75] op_sel_hi:[0,1,1]
	v_pk_mov_b32 v[134:135], v[150:151], v[48:49] op_sel:[1,0]
	v_cvt_pk_bf16_f32 v47, v128, v129
	v_pk_fma_f32 v[74:75], v[104:105], v[134:135], v[74:75] op_sel_hi:[0,1,1]
	v_pk_fma_f32 v[74:75], v[106:107], v[48:49], v[74:75] op_sel_hi:[0,1,1]
	v_mul_f32_e32 v3, 0xbfb8aa3b, v74
	v_exp_f32_e32 v3, v3
	s_nop 0
	v_add_f32_e32 v3, 1.0, v3
	v_rcp_f32_e32 v78, v3
	v_mul_f32_e32 v3, 0xbfb8aa3b, v75
	v_exp_f32_e32 v3, v3
	s_nop 0
	v_add_f32_e32 v3, 1.0, v3
	v_rcp_f32_e32 v79, v3
	s_nop 0
	v_pk_mul_f32 v[74:75], v[74:75], v[78:79]
	s_nop 0
	v_cvt_pk_bf16_f32 v43, v74, v75
	global_load_dwordx4 v[72:75], v[72:73], off offset:2048
	s_nop 0
	global_load_dwordx4 v[76:79], v[76:77], off offset:1536
	s_waitcnt vmcnt(1)
	v_lshlrev_b32_e32 v148, 16, v72
	v_and_b32_e32 v142, 0xffff0000, v72
	s_waitcnt vmcnt(0)
	v_lshlrev_b32_e32 v149, 16, v76
	v_pk_mov_b32 v[150:151], v[146:147], v[148:149] op_sel:[1,0]
	v_and_b32_e32 v143, 0xffff0000, v76
	v_pk_fma_f32 v[126:127], v[30:31], v[150:151], v[126:127] op_sel_hi:[0,1,1]
	v_pk_fma_f32 v[126:127], v[34:35], v[148:149], v[126:127] op_sel_hi:[0,1,1]
	v_mul_f32_e32 v3, 0xbfb8aa3b, v126
	v_exp_f32_e32 v3, v3
	v_pk_mov_b32 v[152:153], v[60:61], v[142:143] op_sel:[1,0]
	v_lshlrev_b32_e32 v141, 16, v77
	v_lshlrev_b32_e32 v140, 16, v73
	v_add_f32_e32 v3, 1.0, v3
	v_rcp_f32_e32 v128, v3
	v_mul_f32_e32 v3, 0xbfb8aa3b, v127
	v_exp_f32_e32 v3, v3
	v_pk_mov_b32 v[144:145], v[144:145], v[140:141] op_sel:[1,0]
	v_and_b32_e32 v137, 0xffff0000, v77
	v_pk_fma_f32 v[122:123], v[32:33], v[144:145], v[122:123] op_sel_hi:[0,1,1]
	v_add_f32_e32 v3, 1.0, v3
	v_rcp_f32_e32 v129, v3
	v_pk_fma_f32 v[122:123], v[36:37], v[140:141], v[122:123] op_sel_hi:[0,1,1]
	v_and_b32_e32 v136, 0xffff0000, v73
	v_pk_fma_f32 v[72:73], v[86:87], v[124:125], v[88:89] op_sel_hi:[0,1,0]
	v_pk_mul_f32 v[156:157], v[126:127], v[128:129]
	v_pk_fma_f32 v[126:127], v[22:23], v[154:155], v[38:39] op_sel:[1,0,1]
	v_pk_fma_f32 v[72:73], v[90:91], v[64:65], v[72:73] op_sel_hi:[0,1,1]
	v_pk_fma_f32 v[126:127], v[26:27], v[60:61], v[126:127] op_sel:[1,0,0]
	v_pk_mov_b32 v[146:147], v[64:65], v[136:137] op_sel:[1,0]
	v_pk_fma_f32 v[60:61], v[30:31], v[152:153], v[126:127] op_sel:[1,0,0]
	v_pk_fma_f32 v[64:65], v[92:93], v[146:147], v[72:73] op_sel_hi:[0,1,1]
	v_pk_fma_f32 v[60:61], v[34:35], v[142:143], v[60:61] op_sel:[1,0,0]
	v_pk_fma_f32 v[64:65], v[94:95], v[136:137], v[64:65] op_sel_hi:[0,1,1]
	v_mul_f32_e32 v3, 0xbfb8aa3b, v60
	v_exp_f32_e32 v3, v3
	v_lshlrev_b32_e32 v131, 16, v78
	v_lshlrev_b32_e32 v130, 16, v74
	v_pk_mov_b32 v[132:133], v[56:57], v[130:131] op_sel:[1,0]
	v_add_f32_e32 v3, 1.0, v3
; #define LAS __attribute__((address_space(3)))
; __device__ __forceinline__ unsigned pk2(float lo, float hi) { const f32x2 v = {lo, hi}; return __builtin_bit_cast(unsigned, __builtin_convertvector(v, hwbf16x2)); }
; __device__ __forceinline__ float fsigmoid(float x) { return __builtin_amdgcn_rcpf(1.0f + __expf(-x)); }
; __device__ __forceinline__ void unpack8(const v4u q, float (&d)[8]) { d[0] = bflo(q.x); d[1] = bfhi(q.x); d[2] = bflo(q.y); d[3] = bfhi(q.y); d[4] = bflo(q.z); d[5] = bfhi(q.z); d[6] = bflo(q.w); d[7] = bfhi(q.w); }
; template <bool TR, bool SCALE>
; __device__ __forceinline__ void conv_task(const Params& p, const bf16* proj, size_t trow0, int tl0, int run, int xcol, LAS bf16* dst, int d0, const LAS float* sc) {
;     ...
;     for (int i = 0; i < 8; i += 2) {
;         float r3[8], r4[8], o0[8], o1[8];
;         unpack8(*(const v4u*)(src + (size_t)i * PROJ_LD), r3); unpack8(*(const v4u*)(src + (size_t)(i + 1) * PROJ_LD), r4);
; #pragma unroll
;         for (int j = 0; j < 8; ++j) { const float a0 = bb[j] + w[0][j] * r0[j] + w[1][j] * r1[j] + w[2][j] * r2[j] + w[3][j] * r3[j];
;             const float a1 = bb[j] + w[0][j] * r1[j] + w[1][j] * r2[j] + w[2][j] * r3[j] + w[3][j] * r4[j];
;             o0[j] = a0 * fsigmoid(a0); o1[j] = a1 * fsigmoid(a1); }
;         if constexpr (TR) {
;             float s0 = 1.f, s1 = 1.f; if constexpr (SCALE) { s0 = sc[l0 + i]; s1 = sc[l0 + i + 1]; }
; #pragma unroll
;             for (int j = 0; j < 8; ++j) *(LAS unsigned*)(dst + (d0 + j) * SPT + l0 + i) = pk2(o0[j] * s0, o1[j] * s1);
;         } else {
;             *(LAS v4u*)(dst + (l0 + i) * SPT + d0) = (v4u){pk2(o0[0], o0[1]), pk2(o0[2], o0[3]), pk2(o0[4], o0[5]), pk2(o0[6], o0[7])};
;             *(LAS v4u*)(dst + (l0 + i + 1) * SPT + d0) = (v4u){pk2(o1[0], o1[1]), pk2(o1[2], o1[3]), pk2(o1[4], o1[5]), pk2(o1[6], o1[7])};
;         }
; #pragma unroll
;         for (int j = 0; j < 8; ++j) { r0[j] = r2[j]; r1[j] = r3[j]; r2[j] = r4[j]; }
	v_rcp_f32_e32 v126, v3
	v_mul_f32_e32 v3, 0xbfb8aa3b, v61
	v_exp_f32_e32 v3, v3
	v_pk_fma_f32 v[150:151], v[22:23], v[150:151], v[38:39] op_sel_hi:[0,1,0]
	v_pk_fma_f32 v[150:151], v[26:27], v[148:149], v[150:151] op_sel_hi:[0,1,1]
	v_pk_fma_f32 v[22:23], v[22:23], v[152:153], v[38:39] op_sel:[1,0,1]
	v_add_f32_e32 v3, 1.0, v3
	v_rcp_f32_e32 v127, v3
	v_mul_f32_e32 v3, 0xbfb8aa3b, v122
	v_exp_f32_e32 v3, v3
	v_pk_fma_f32 v[22:23], v[26:27], v[142:143], v[22:23] op_sel:[1,0,0]
	v_pk_mul_f32 v[60:61], v[60:61], v[126:127]
	v_pk_fma_f32 v[24:25], v[24:25], v[144:145], v[40:41] op_sel_hi:[0,1,0]
	v_add_f32_e32 v3, 1.0, v3
	v_rcp_f32_e32 v126, v3
	v_mul_f32_e32 v3, 0xbfb8aa3b, v123
	v_exp_f32_e32 v3, v3
	v_pk_fma_f32 v[24:25], v[28:29], v[140:141], v[24:25] op_sel_hi:[0,1,1]
	v_add_f32_e32 v3, 1.0, v3
	v_rcp_f32_e32 v127, v3
	v_mul_f32_e32 v3, 0xbfb8aa3b, v64
	v_exp_f32_e32 v3, v3
	v_pk_mul_f32 v[154:155], v[122:123], v[126:127]
	v_and_b32_e32 v127, 0xffff0000, v78
	v_add_f32_e32 v3, 1.0, v3
	v_rcp_f32_e32 v72, v3
	v_mul_f32_e32 v3, 0xbfb8aa3b, v65
	v_exp_f32_e32 v3, v3
	v_and_b32_e32 v126, 0xffff0000, v74
	v_pk_mov_b32 v[128:129], v[44:45], v[126:127] op_sel:[1,0]
	v_lshlrev_b32_e32 v123, 16, v79
	v_add_f32_e32 v3, 1.0, v3
	v_rcp_f32_e32 v73, v3
	v_lshlrev_b32_e32 v122, 16, v75
	v_pk_mov_b32 v[124:125], v[52:53], v[122:123] op_sel:[1,0]
	v_pk_mul_f32 v[76:77], v[64:65], v[72:73]
	v_pk_fma_f32 v[64:65], v[2:3], v[68:69], v[18:19] op_sel_hi:[0,1,0]
	v_pk_fma_f32 v[64:65], v[6:7], v[56:57], v[64:65] op_sel_hi:[0,1,1]
	v_pk_fma_f32 v[56:57], v[10:11], v[132:133], v[64:65] op_sel_hi:[0,1,1]
	v_pk_fma_f32 v[56:57], v[14:15], v[130:131], v[56:57] op_sel_hi:[0,1,1]
	v_mul_f32_e32 v3, 0xbfb8aa3b, v56
	v_exp_f32_e32 v3, v3
	v_cvt_pk_bf16_f32 v68, v60, v61
	v_cvt_pk_bf16_f32 v60, v76, v77
	v_cvt_pk_bf16_f32 v72, v156, v157
	v_add_f32_e32 v3, 1.0, v3
	v_rcp_f32_e32 v64, v3
	v_mul_f32_e32 v3, 0xbfb8aa3b, v57
	v_exp_f32_e32 v3, v3
	s_nop 0
	v_add_f32_e32 v3, 1.0, v3
	v_rcp_f32_e32 v65, v3
	s_nop 0
	v_pk_mul_f32 v[56:57], v[56:57], v[64:65]
	v_pk_fma_f32 v[64:65], v[108:109], v[118:119], v[110:111] op_sel_hi:[0,1,0]
	v_pk_fma_f32 v[64:65], v[112:113], v[44:45], v[64:65] op_sel_hi:[0,1,1]
	v_pk_fma_f32 v[44:45], v[114:115], v[128:129], v[64:65] op_sel_hi:[0,1,1]
	v_pk_fma_f32 v[44:45], v[116:117], v[126:127], v[44:45] op_sel_hi:[0,1,1]
	v_mul_f32_e32 v3, 0xbfb8aa3b, v44
	v_exp_f32_e32 v3, v3
	v_and_b32_e32 v119, 0xffff0000, v79
	v_and_b32_e32 v118, 0xffff0000, v75
	v_cvt_pk_bf16_f32 v56, v56, v57
	v_add_f32_e32 v3, 1.0, v3
	v_rcp_f32_e32 v64, v3
	v_mul_f32_e32 v3, 0xbfb8aa3b, v45
	v_exp_f32_e32 v3, v3
	s_nop 0
	v_add_f32_e32 v3, 1.0, v3
	v_rcp_f32_e32 v65, v3
	s_nop 0
	v_pk_mul_f32 v[44:45], v[44:45], v[64:65]
	v_pk_fma_f32 v[64:65], v[4:5], v[120:121], v[20:21] op_sel_hi:[0,1,0]
	v_pk_fma_f32 v[64:65], v[8:9], v[52:53], v[64:65] op_sel_hi:[0,1,1]
	v_pk_fma_f32 v[52:53], v[12:13], v[124:125], v[64:65] op_sel_hi:[0,1,1]
	v_pk_fma_f32 v[52:53], v[16:17], v[122:123], v[52:53] op_sel_hi:[0,1,1]
	v_mul_f32_e32 v3, 0xbfb8aa3b, v52
	v_exp_f32_e32 v3, v3
	v_pk_mov_b32 v[120:121], v[48:49], v[118:119] op_sel:[1,0]
	v_add_f32_e32 v3, 1.0, v3
	v_rcp_f32_e32 v64, v3
	v_mul_f32_e32 v3, 0xbfb8aa3b, v53
	v_exp_f32_e32 v3, v3
	s_nop 0
	v_add_f32_e32 v3, 1.0, v3
	v_rcp_f32_e32 v65, v3
	s_nop 0
	v_pk_mul_f32 v[158:159], v[52:53], v[64:65]
	v_pk_fma_f32 v[52:53], v[98:99], v[134:135], v[100:101] op_sel_hi:[0,1,0]
	v_pk_fma_f32 v[52:53], v[102:103], v[48:49], v[52:53] op_sel_hi:[0,1,1]
	v_pk_fma_f32 v[48:49], v[104:105], v[120:121], v[52:53] op_sel_hi:[0,1,1]
	v_pk_fma_f32 v[48:49], v[106:107], v[118:119], v[48:49] op_sel_hi:[0,1,1]
	v_mul_f32_e32 v3, 0xbfb8aa3b, v48
	v_exp_f32_e32 v3, v3
	v_cvt_pk_bf16_f32 v64, v154, v155
	v_add_f32_e32 v3, 1.0, v3
	v_rcp_f32_e32 v52, v3
	v_mul_f32_e32 v3, 0xbfb8aa3b, v49
	v_exp_f32_e32 v3, v3
	s_nop 0
	v_add_f32_e32 v3, 1.0, v3
	v_rcp_f32_e32 v53, v3
	s_nop 0
	v_pk_mul_f32 v[74:75], v[48:49], v[52:53]
	v_cvt_pk_bf16_f32 v52, v44, v45
	v_cvt_pk_bf16_f32 v44, v74, v75
	v_add_co_u32_e32 v74, vcc, s92, v80
	v_cvt_pk_bf16_f32 v48, v158, v159
	s_nop 0
	v_addc_co_u32_e32 v75, vcc, 0, v81, vcc
	v_add_co_u32_e32 v78, vcc, s93, v80
	global_load_dwordx4 v[74:77], v[74:75], off offset:1024
	s_nop 0
	v_addc_co_u32_e32 v79, vcc, 0, v81, vcc
	global_load_dwordx4 v[78:81], v[78:79], off offset:512
	s_waitcnt vmcnt(1)
	v_lshlrev_b32_e32 v134, 16, v74
	s_waitcnt vmcnt(0)
; #define LAS __attribute__((address_space(3)))
; __device__ __forceinline__ unsigned pk2(float lo, float hi) { const f32x2 v = {lo, hi}; return __builtin_bit_cast(unsigned, __builtin_convertvector(v, hwbf16x2)); }
; __device__ __forceinline__ float fsigmoid(float x) { return __builtin_amdgcn_rcpf(1.0f + __expf(-x)); }
; __device__ __forceinline__ void unpack8(const v4u q, float (&d)[8]) { d[0] = bflo(q.x); d[1] = bfhi(q.x); d[2] = bflo(q.y); d[3] = bfhi(q.y); d[4] = bflo(q.z); d[5] = bfhi(q.z); d[6] = bflo(q.w); d[7] = bfhi(q.w); }
; template <bool TR, bool SCALE>
; __device__ __forceinline__ void conv_task(const Params& p, const bf16* proj, size_t trow0, int tl0, int run, int xcol, LAS bf16* dst, int d0, const LAS float* sc) {
;     ...
;     for (int i = 0; i < 8; i += 2) {
;         float r3[8], r4[8], o0[8], o1[8];
;         unpack8(*(const v4u*)(src + (size_t)i * PROJ_LD), r3); unpack8(*(const v4u*)(src + (size_t)(i + 1) * PROJ_LD), r4);
; #pragma unroll
;         for (int j = 0; j < 8; ++j) { const float a0 = bb[j] + w[0][j] * r0[j] + w[1][j] * r1[j] + w[2][j] * r2[j] + w[3][j] * r3[j];
;             const float a1 = bb[j] + w[0][j] * r1[j] + w[1][j] * r2[j] + w[2][j] * r3[j] + w[3][j] * r4[j];
;             o0[j] = a0 * fsigmoid(a0); o1[j] = a1 * fsigmoid(a1); }
;         if constexpr (TR) {
;             float s0 = 1.f, s1 = 1.f; if constexpr (SCALE) { s0 = sc[l0 + i]; s1 = sc[l0 + i + 1]; }
; #pragma unroll
;             for (int j = 0; j < 8; ++j) *(LAS unsigned*)(dst + (d0 + j) * SPT + l0 + i) = pk2(o0[j] * s0, o1[j] * s1);
	v_lshlrev_b32_e32 v135, 16, v78
	v_pk_mov_b32 v[148:149], v[148:149], v[134:135] op_sel:[1,0]
	s_nop 0
	v_pk_fma_f32 v[148:149], v[30:31], v[148:149], v[150:151] op_sel_hi:[0,1,1]
	v_pk_fma_f32 v[134:135], v[34:35], v[134:135], v[148:149] op_sel_hi:[0,1,1]
	v_mul_f32_e32 v3, 0xbfb8aa3b, v134
	v_exp_f32_e32 v3, v3
	s_nop 0
	v_add_f32_e32 v3, 1.0, v3
	v_rcp_f32_e32 v148, v3
	v_mul_f32_e32 v3, 0xbfb8aa3b, v135
	v_exp_f32_e32 v3, v3
	s_nop 0
	v_add_f32_e32 v3, 1.0, v3
	v_rcp_f32_e32 v149, v3
	s_nop 0
	v_pk_mul_f32 v[134:135], v[134:135], v[148:149]
	v_and_b32_e32 v149, 0xffff0000, v78
	v_and_b32_e32 v148, 0xffff0000, v74
	v_pk_mov_b32 v[26:27], v[142:143], v[148:149] op_sel:[1,0]
	v_cvt_pk_bf16_f32 v73, v134, v135
	v_pk_fma_f32 v[22:23], v[30:31], v[26:27], v[22:23] op_sel:[1,0,0]
	ds_write_b128 v96, v[70:73]
	v_pk_fma_f32 v[22:23], v[34:35], v[148:149], v[22:23] op_sel:[1,0,0]
	s_nop 0
	v_mul_f32_e32 v3, 0xbfb8aa3b, v22
	v_exp_f32_e32 v3, v3
	s_nop 0
	v_add_f32_e32 v3, 1.0, v3
	v_rcp_f32_e32 v26, v3
	v_mul_f32_e32 v3, 0xbfb8aa3b, v23
	v_exp_f32_e32 v3, v3
	s_nop 0
	v_add_f32_e32 v3, 1.0, v3
	v_rcp_f32_e32 v27, v3
	s_nop 0
	v_pk_mul_f32 v[22:23], v[22:23], v[26:27]
	v_lshlrev_b32_e32 v26, 16, v75
	v_lshlrev_b32_e32 v27, 16, v79
	v_pk_mov_b32 v[28:29], v[140:141], v[26:27] op_sel:[1,0]
	v_cvt_pk_bf16_f32 v69, v22, v23
	v_pk_fma_f32 v[24:25], v[32:33], v[28:29], v[24:25] op_sel_hi:[0,1,1]
	v_pk_fma_f32 v[24:25], v[36:37], v[26:27], v[24:25] op_sel_hi:[0,1,1]
	v_mul_f32_e32 v3, 0xbfb8aa3b, v24
	v_exp_f32_e32 v3, v3
	v_pk_fma_f32 v[28:29], v[86:87], v[146:147], v[88:89] op_sel_hi:[0,1,0]
	v_pk_fma_f32 v[28:29], v[90:91], v[136:137], v[28:29] op_sel_hi:[0,1,1]
	ds_write_b128 v96, v[66:69] offset:272
	v_add_f32_e32 v3, 1.0, v3
	v_rcp_f32_e32 v26, v3
	v_mul_f32_e32 v3, 0xbfb8aa3b, v25
	v_exp_f32_e32 v3, v3
	s_nop 0
	v_add_f32_e32 v3, 1.0, v3
	v_rcp_f32_e32 v27, v3
	s_nop 0
	v_pk_mul_f32 v[24:25], v[24:25], v[26:27]
	v_and_b32_e32 v27, 0xffff0000, v79
	v_and_b32_e32 v26, 0xffff0000, v75
	v_pk_mov_b32 v[30:31], v[136:137], v[26:27] op_sel:[1,0]
	v_cvt_pk_bf16_f32 v65, v24, v25
	v_pk_fma_f32 v[28:29], v[92:93], v[30:31], v[28:29] op_sel_hi:[0,1,1]
	v_pk_fma_f32 v[26:27], v[94:95], v[26:27], v[28:29] op_sel_hi:[0,1,1]
	v_mul_f32_e32 v3, 0xbfb8aa3b, v26
	v_exp_f32_e32 v3, v3
	ds_write_b128 v96, v[62:65] offset:544
	v_add_f32_e32 v3, 1.0, v3
	v_rcp_f32_e32 v28, v3
	v_mul_f32_e32 v3, 0xbfb8aa3b, v27
	v_exp_f32_e32 v3, v3
	s_nop 0
	v_add_f32_e32 v3, 1.0, v3
	v_rcp_f32_e32 v29, v3
	v_pk_fma_f32 v[2:3], v[2:3], v[132:133], v[18:19] op_sel_hi:[0,1,0]
	v_pk_fma_f32 v[2:3], v[6:7], v[130:131], v[2:3] op_sel_hi:[0,1,1]
	v_pk_mul_f32 v[26:27], v[26:27], v[28:29]
	v_lshlrev_b32_e32 v28, 16, v76
	v_lshlrev_b32_e32 v29, 16, v80
	v_pk_mov_b32 v[6:7], v[130:131], v[28:29] op_sel:[1,0]
	v_cvt_pk_bf16_f32 v61, v26, v27
	v_pk_fma_f32 v[2:3], v[10:11], v[6:7], v[2:3] op_sel_hi:[0,1,1]
	v_pk_fma_f32 v[2:3], v[14:15], v[28:29], v[2:3] op_sel_hi:[0,1,1]
	v_mul_f32_e32 v5, 0xbfb8aa3b, v2
	v_exp_f32_e32 v5, v5
	v_pk_fma_f32 v[10:11], v[108:109], v[128:129], v[110:111] op_sel_hi:[0,1,0]
	v_pk_fma_f32 v[10:11], v[112:113], v[126:127], v[10:11] op_sel_hi:[0,1,1]
	ds_write_b128 v96, v[58:61] offset:816
	v_add_f32_e32 v5, 1.0, v5
	v_rcp_f32_e32 v6, v5
	v_mul_f32_e32 v5, 0xbfb8aa3b, v3
	v_exp_f32_e32 v5, v5
	s_nop 0
	v_add_f32_e32 v5, 1.0, v5
	v_rcp_f32_e32 v7, v5
	s_nop 0
	v_pk_mul_f32 v[2:3], v[2:3], v[6:7]
	v_and_b32_e32 v7, 0xffff0000, v80
	v_and_b32_e32 v6, 0xffff0000, v76
	v_pk_mov_b32 v[14:15], v[126:127], v[6:7] op_sel:[1,0]
	v_cvt_pk_bf16_f32 v57, v2, v3
	v_pk_fma_f32 v[10:11], v[114:115], v[14:15], v[10:11] op_sel_hi:[0,1,1]
	v_pk_fma_f32 v[6:7], v[116:117], v[6:7], v[10:11] op_sel_hi:[0,1,1]
	v_mul_f32_e32 v5, 0xbfb8aa3b, v6
	v_exp_f32_e32 v5, v5
	ds_write_b128 v96, v[54:57] offset:1088
	v_add_f32_e32 v5, 1.0, v5
	v_rcp_f32_e32 v10, v5
	v_mul_f32_e32 v5, 0xbfb8aa3b, v7
	v_exp_f32_e32 v5, v5
	s_nop 0
	v_add_f32_e32 v5, 1.0, v5
	v_rcp_f32_e32 v11, v5
	v_pk_fma_f32 v[4:5], v[4:5], v[124:125], v[20:21] op_sel_hi:[0,1,0]
	v_pk_fma_f32 v[4:5], v[8:9], v[122:123], v[4:5] op_sel_hi:[0,1,1]
	v_pk_mul_f32 v[6:7], v[6:7], v[10:11]
	v_lshlrev_b32_e32 v10, 16, v77
	v_lshlrev_b32_e32 v11, 16, v81
	v_pk_mov_b32 v[8:9], v[122:123], v[10:11] op_sel:[1,0]
	v_cvt_pk_bf16_f32 v53, v6, v7
	v_pk_fma_f32 v[4:5], v[12:13], v[8:9], v[4:5] op_sel_hi:[0,1,1]
	v_pk_fma_f32 v[4:5], v[16:17], v[10:11], v[4:5] op_sel_hi:[0,1,1]
	v_mul_f32_e32 v8, 0xbfb8aa3b, v4
	v_mul_f32_e32 v9, 0xbfb8aa3b, v5
	v_exp_f32_e32 v8, v8
	v_exp_f32_e32 v9, v9
	v_pk_fma_f32 v[10:11], v[98:99], v[120:121], v[100:101] op_sel_hi:[0,1,0]
	v_pk_fma_f32 v[10:11], v[102:103], v[118:119], v[10:11] op_sel_hi:[0,1,1]
	v_add_f32_e32 v8, 1.0, v8
	v_add_f32_e32 v9, 1.0, v9
	v_rcp_f32_e32 v8, v8
	v_rcp_f32_e32 v9, v9
	ds_write_b128 v96, v[50:53] offset:1360
	v_pk_mul_f32 v[4:5], v[4:5], v[8:9]
	v_and_b32_e32 v9, 0xffff0000, v81
	v_and_b32_e32 v8, 0xffff0000, v77
	v_pk_mov_b32 v[12:13], v[118:119], v[8:9] op_sel:[1,0]
	v_cvt_pk_bf16_f32 v49, v4, v5
	v_pk_fma_f32 v[10:11], v[104:105], v[12:13], v[10:11] op_sel_hi:[0,1,1]
	v_pk_fma_f32 v[8:9], v[106:107], v[8:9], v[10:11] op_sel_hi:[0,1,1]
	v_mul_f32_e32 v10, 0xbfb8aa3b, v8
	v_mul_f32_e32 v11, 0xbfb8aa3b, v9
	v_exp_f32_e32 v10, v10
	v_exp_f32_e32 v11, v11
	ds_write_b128 v96, v[46:49] offset:1632
	v_add_f32_e32 v10, 1.0, v10
	v_add_f32_e32 v11, 1.0, v11
	v_rcp_f32_e32 v10, v10
	v_rcp_f32_e32 v11, v11
	s_nop 0
	v_pk_mul_f32 v[8:9], v[8:9], v[10:11]
	s_nop 0
	v_cvt_pk_bf16_f32 v45, v8, v9
	ds_write_b128 v96, v[42:45] offset:1904

; #define LAS __attribute__((address_space(3)))
; __device__ __forceinline__ unsigned pk2(float lo, float hi) { const f32x2 v = {lo, hi}; return __builtin_bit_cast(unsigned, __builtin_convertvector(v, hwbf16x2)); }
; __device__ __forceinline__ float fsigmoid(float x) { return __builtin_amdgcn_rcpf(1.0f + __expf(-x)); }
; __device__ __forceinline__ void unpack8(const v4u q, float (&d)[8]) { d[0] = bflo(q.x); d[1] = bfhi(q.x); d[2] = bflo(q.y); d[3] = bfhi(q.y); d[4] = bflo(q.z); d[5] = bfhi(q.z); d[6] = bflo(q.w); d[7] = bfhi(q.w); }
; template <bool TR, bool SCALE>
; __device__ __forceinline__ void conv_task(const Params& p, const bf16* proj, size_t trow0, int tl0, int run, int xcol, LAS bf16* dst, int d0, const LAS float* sc) {
;     ...
;     const int l0 = run * 8; const bf16* src = proj + (trow0 + l0) * PROJ_LD + COL_XBC + xcol;
;     float r0[8], r1[8], r2[8];
;     { const int pos = tl0 + l0; v4u q0 = (v4u){0u, 0u, 0u, 0u}, q1 = q0, q2 = q0;
;       if (pos - 3 >= 0) q0 = *(const v4u*)(src - 3 * PROJ_LD);
;       if (pos - 2 >= 0) q1 = *(const v4u*)(src - 2 * PROJ_LD);
;       if (pos - 1 >= 0) q2 = *(const v4u*)(src - 1 * PROJ_LD);
;       unpack8(q0, r0); unpack8(q1, r1); unpack8(q2, r2); }
; #pragma unroll
;     for (int i = 0; i < 8; i += 2) {
;         float r3[8], r4[8], o0[8], o1[8];
;         unpack8(*(const v4u*)(src + (size_t)i * PROJ_LD), r3); unpack8(*(const v4u*)(src + (size_t)(i + 1) * PROJ_LD), r4);
; #pragma unroll
;         for (int j = 0; j < 8; ++j) { const float a0 = bb[j] + w[0][j] * r0[j] + w[1][j] * r1[j] + w[2][j] * r2[j] + w[3][j] * r3[j];
;             const float a1 = bb[j] + w[0][j] * r1[j] + w[1][j] * r2[j] + w[2][j] * r3[j] + w[3][j] * r4[j];
;             o0[j] = a0 * fsigmoid(a0); o1[j] = a1 * fsigmoid(a1); }
;         if constexpr (TR) {
;             float s0 = 1.f, s1 = 1.f; if constexpr (SCALE) { s0 = sc[l0 + i]; s1 = sc[l0 + i + 1]; }
; #pragma unroll
;             for (int j = 0; j < 8; ++j) *(LAS unsigned*)(dst + (d0 + j) * SPT + l0 + i) = pk2(o0[j] * s0, o1[j] * s1);
.LBB0_462:
	s_or_b64 exec, exec, s[12:13]
	global_load_dwordx4 v[58:61], v[62:63], off
	v_add_co_u32_e32 v54, vcc, 0x1000, v62
	s_waitcnt vmcnt(1)
	v_lshlrev_b32_e32 v64, 16, v46
	v_addc_co_u32_e32 v55, vcc, 0, v63, vcc
	global_load_dwordx4 v[54:57], v[54:55], off offset:3584
	v_add_co_u32_e32 v248, vcc, s79, v62
	s_nop 1
	v_addc_co_u32_e32 v249, vcc, 0, v63, vcc
	global_load_dword v246, v[248:249], off offset:3072
	v_add_co_u32_e32 v248, vcc, s81, v62
	s_nop 1
	v_addc_co_u32_e32 v249, vcc, 0, v63, vcc
	global_load_dword v246, v[248:249], off offset:2560
	v_add_co_u32_e32 v248, vcc, s82, v62
	s_nop 1
	v_addc_co_u32_e32 v249, vcc, 0, v63, vcc
	global_load_dword v246, v[248:249], off offset:2048
	v_add_co_u32_e32 v248, vcc, s83, v62
	s_nop 1
	v_addc_co_u32_e32 v249, vcc, 0, v63, vcc
	global_load_dword v246, v[248:249], off offset:1536
	v_add_co_u32_e32 v248, vcc, s92, v62
	s_nop 1
	v_addc_co_u32_e32 v249, vcc, 0, v63, vcc
	global_load_dword v246, v[248:249], off offset:1024
	v_add_co_u32_e32 v248, vcc, s93, v62
	s_nop 1
	v_addc_co_u32_e32 v249, vcc, 0, v63, vcc
	global_load_dword v246, v[248:249], off offset:512
	v_and_b32_e32 v65, 0xffff0000, v46
	v_lshlrev_b32_e32 v70, 16, v42
	v_and_b32_e32 v71, 0xffff0000, v42
	v_pk_fma_f32 v[64:65], v[22:23], v[64:65], v[38:39]
	v_lshlrev_b32_e32 v66, 16, v50
	v_and_b32_e32 v67, 0xffff0000, v50
	v_pk_fma_f32 v[64:65], v[26:27], v[70:71], v[64:65]
	v_pk_fma_f32 v[70:71], v[22:23], v[70:71], v[38:39]
	v_pk_fma_f32 v[64:65], v[30:31], v[66:67], v[64:65]
	v_pk_fma_f32 v[70:71], v[26:27], v[66:67], v[70:71]
	v_lshlrev_b32_e32 v46, 16, v47
	v_and_b32_e32 v47, 0xffff0000, v47
	v_pk_fma_f32 v[46:47], v[24:25], v[46:47], v[40:41]
	v_lshlrev_b32_e32 v74, 16, v44
	v_and_b32_e32 v75, 0xffff0000, v44
	v_lshlrev_b32_e32 v76, 16, v52
	v_and_b32_e32 v77, 0xffff0000, v52
	v_lshlrev_b32_e32 v78, 16, v53
	v_and_b32_e32 v79, 0xffff0000, v53
	s_waitcnt vmcnt(1)
	v_lshlrev_b32_e32 v68, 16, v58
	v_and_b32_e32 v69, 0xffff0000, v58
	v_pk_fma_f32 v[64:65], v[34:35], v[68:69], v[64:65]
	v_pk_fma_f32 v[70:71], v[30:31], v[68:69], v[70:71]
	v_mul_f32_e32 v42, 0xbfb8aa3b, v64
	v_exp_f32_e32 v42, v42
	v_lshlrev_b32_e32 v58, 16, v59
	v_and_b32_e32 v59, 0xffff0000, v59
	s_waitcnt vmcnt(0)
	v_lshlrev_b32_e32 v52, 16, v57
	v_add_f32_e32 v42, 1.0, v42
	v_rcp_f32_e32 v72, v42
	v_mul_f32_e32 v42, 0xbfb8aa3b, v65
	v_exp_f32_e32 v42, v42
	v_and_b32_e32 v53, 0xffff0000, v57
	v_add_f32_e32 v42, 1.0, v42
	v_rcp_f32_e32 v73, v42
	s_nop 0
	v_pk_mul_f32 v[80:81], v[64:65], v[72:73]
	v_lshlrev_b32_e32 v64, 16, v54
	v_and_b32_e32 v65, 0xffff0000, v54
	v_pk_fma_f32 v[70:71], v[34:35], v[64:65], v[70:71]
	s_nop 0
	v_mul_f32_e32 v42, 0xbfb8aa3b, v70
	v_exp_f32_e32 v42, v42
	s_nop 0
	v_add_f32_e32 v42, 1.0, v42
	v_rcp_f32_e32 v72, v42
	v_mul_f32_e32 v42, 0xbfb8aa3b, v71
	v_exp_f32_e32 v42, v42
	s_nop 0
	v_add_f32_e32 v42, 1.0, v42
	v_rcp_f32_e32 v73, v42
	v_lshlrev_b32_e32 v42, 16, v43
	v_and_b32_e32 v43, 0xffff0000, v43
	v_pk_fma_f32 v[46:47], v[28:29], v[42:43], v[46:47]
	v_pk_mul_f32 v[86:87], v[70:71], v[72:73]
	v_lshlrev_b32_e32 v70, 16, v51
	v_and_b32_e32 v71, 0xffff0000, v51
	v_pk_fma_f32 v[46:47], v[32:33], v[70:71], v[46:47]
	v_pk_fma_f32 v[42:43], v[24:25], v[42:43], v[40:41]
	v_pk_fma_f32 v[46:47], v[36:37], v[58:59], v[46:47]
	v_pk_fma_f32 v[42:43], v[28:29], v[70:71], v[42:43]
	v_mul_f32_e32 v50, 0xbfb8aa3b, v46
	v_mul_f32_e32 v51, 0xbfb8aa3b, v47
	v_exp_f32_e32 v50, v50
	v_exp_f32_e32 v51, v51
	v_pk_fma_f32 v[42:43], v[32:33], v[58:59], v[42:43]
	v_lshlrev_b32_e32 v72, 16, v60
	v_add_f32_e32 v50, 1.0, v50
	v_add_f32_e32 v51, 1.0, v51
	v_rcp_f32_e32 v50, v50
	v_rcp_f32_e32 v51, v51
	v_and_b32_e32 v73, 0xffff0000, v60
	v_pk_mul_f32 v[46:47], v[46:47], v[50:51]
	v_lshlrev_b32_e32 v50, 16, v55
	v_and_b32_e32 v51, 0xffff0000, v55
	v_pk_fma_f32 v[42:43], v[36:37], v[50:51], v[42:43]
	s_nop 0
	v_mul_f32_e32 v54, 0xbfb8aa3b, v42
	v_mul_f32_e32 v55, 0xbfb8aa3b, v43
	v_exp_f32_e32 v54, v54
	v_exp_f32_e32 v55, v55
	v_add_f32_e32 v54, 1.0, v54
	v_add_f32_e32 v55, 1.0, v55
	v_rcp_f32_e32 v54, v54
	v_rcp_f32_e32 v55, v55
	s_nop 0
	v_pk_mul_f32 v[92:93], v[42:43], v[54:55]
	v_lshlrev_b32_e32 v42, 16, v48
	v_and_b32_e32 v43, 0xffff0000, v48
	v_pk_fma_f32 v[42:43], v[2:3], v[42:43], v[18:19]
	s_nop 0
	v_pk_fma_f32 v[42:43], v[6:7], v[74:75], v[42:43]
	s_nop 0
	v_pk_fma_f32 v[42:43], v[10:11], v[76:77], v[42:43]
	s_nop 0
	v_pk_fma_f32 v[42:43], v[14:15], v[72:73], v[42:43]
	s_nop 0
	v_mul_f32_e32 v44, 0xbfb8aa3b, v42
	v_exp_f32_e32 v44, v44
	s_nop 0
	v_add_f32_e32 v44, 1.0, v44
	v_rcp_f32_e32 v54, v44
	v_mul_f32_e32 v44, 0xbfb8aa3b, v43
	v_exp_f32_e32 v44, v44
	s_nop 0
	v_add_f32_e32 v44, 1.0, v44
	v_rcp_f32_e32 v55, v44
	s_nop 0
	v_pk_mul_f32 v[90:91], v[42:43], v[54:55]
	v_pk_fma_f32 v[42:43], v[2:3], v[74:75], v[18:19]
	v_lshlrev_b32_e32 v54, 16, v56
	v_pk_fma_f32 v[42:43], v[6:7], v[76:77], v[42:43]
	v_and_b32_e32 v55, 0xffff0000, v56
	v_pk_fma_f32 v[42:43], v[10:11], v[72:73], v[42:43]
	s_nop 0
	v_pk_fma_f32 v[42:43], v[14:15], v[54:55], v[42:43]
	s_nop 0
	v_mul_f32_e32 v44, 0xbfb8aa3b, v42
	v_exp_f32_e32 v44, v44
	s_nop 0
	v_add_f32_e32 v44, 1.0, v44
	v_rcp_f32_e32 v74, v44
	v_mul_f32_e32 v44, 0xbfb8aa3b, v43
	v_exp_f32_e32 v44, v44
	s_nop 0
	v_add_f32_e32 v44, 1.0, v44
	v_rcp_f32_e32 v75, v44
	v_lshlrev_b32_e32 v44, 16, v45
	v_and_b32_e32 v45, 0xffff0000, v45
	v_pk_mul_f32 v[94:95], v[42:43], v[74:75]
	v_lshlrev_b32_e32 v42, 16, v49
	v_and_b32_e32 v43, 0xffff0000, v49
	v_pk_fma_f32 v[42:43], v[4:5], v[42:43], v[20:21]
	v_lshlrev_b32_e32 v74, 16, v61
	v_pk_fma_f32 v[42:43], v[8:9], v[44:45], v[42:43]
	v_and_b32_e32 v75, 0xffff0000, v61
; #define LAS __attribute__((address_space(3)))
; __device__ __forceinline__ unsigned pk2(float lo, float hi) { const f32x2 v = {lo, hi}; return __builtin_bit_cast(unsigned, __builtin_convertvector(v, hwbf16x2)); }
; __device__ __forceinline__ float fsigmoid(float x) { return __builtin_amdgcn_rcpf(1.0f + __expf(-x)); }
; __device__ __forceinline__ void unpack8(const v4u q, float (&d)[8]) { d[0] = bflo(q.x); d[1] = bfhi(q.x); d[2] = bflo(q.y); d[3] = bfhi(q.y); d[4] = bflo(q.z); d[5] = bfhi(q.z); d[6] = bflo(q.w); d[7] = bfhi(q.w); }
; template <bool TR, bool SCALE>
; __device__ __forceinline__ void conv_task(const Params& p, const bf16* proj, size_t trow0, int tl0, int run, int xcol, LAS bf16* dst, int d0, const LAS float* sc) {
;     ...
;     for (int i = 0; i < 8; i += 2) {
;         float r3[8], r4[8], o0[8], o1[8];
;         unpack8(*(const v4u*)(src + (size_t)i * PROJ_LD), r3); unpack8(*(const v4u*)(src + (size_t)(i + 1) * PROJ_LD), r4);
; #pragma unroll
;         for (int j = 0; j < 8; ++j) { const float a0 = bb[j] + w[0][j] * r0[j] + w[1][j] * r1[j] + w[2][j] * r2[j] + w[3][j] * r3[j];
;             const float a1 = bb[j] + w[0][j] * r1[j] + w[1][j] * r2[j] + w[2][j] * r3[j] + w[3][j] * r4[j];
;             o0[j] = a0 * fsigmoid(a0); o1[j] = a1 * fsigmoid(a1); }
;         if constexpr (TR) {
;             float s0 = 1.f, s1 = 1.f; if constexpr (SCALE) { s0 = sc[l0 + i]; s1 = sc[l0 + i + 1]; }
; #pragma unroll
;             for (int j = 0; j < 8; ++j) *(LAS unsigned*)(dst + (d0 + j) * SPT + l0 + i) = pk2(o0[j] * s0, o1[j] * s1);
;         } else {
;             *(LAS v4u*)(dst + (l0 + i) * SPT + d0) = (v4u){pk2(o0[0], o0[1]), pk2(o0[2], o0[3]), pk2(o0[4], o0[5]), pk2(o0[6], o0[7])};
;             *(LAS v4u*)(dst + (l0 + i + 1) * SPT + d0) = (v4u){pk2(o1[0], o1[1]), pk2(o1[2], o1[3]), pk2(o1[4], o1[5]), pk2(o1[6], o1[7])};
;         }
; #pragma unroll
;         for (int j = 0; j < 8; ++j) { r0[j] = r2[j]; r1[j] = r3[j]; r2[j] = r4[j]; }
	v_pk_fma_f32 v[42:43], v[12:13], v[78:79], v[42:43]
	s_nop 0
	v_pk_fma_f32 v[42:43], v[16:17], v[74:75], v[42:43]
	s_nop 0
	v_mul_f32_e32 v48, 0xbfb8aa3b, v42
	v_mul_f32_e32 v49, 0xbfb8aa3b, v43
	v_exp_f32_e32 v48, v48
	v_exp_f32_e32 v49, v49
	v_add_f32_e32 v48, 1.0, v48
	v_add_f32_e32 v49, 1.0, v49
	v_rcp_f32_e32 v48, v48
	v_rcp_f32_e32 v49, v49
	s_nop 0
	v_pk_mul_f32 v[48:49], v[42:43], v[48:49]
	v_pk_fma_f32 v[42:43], v[4:5], v[44:45], v[20:21]
	s_nop 0
	v_pk_fma_f32 v[42:43], v[8:9], v[78:79], v[42:43]
	s_nop 0
	v_pk_fma_f32 v[42:43], v[12:13], v[74:75], v[42:43]
	s_nop 0
	v_pk_fma_f32 v[42:43], v[16:17], v[52:53], v[42:43]
	s_nop 0
	v_mul_f32_e32 v44, 0xbfb8aa3b, v42
	v_mul_f32_e32 v45, 0xbfb8aa3b, v43
	v_exp_f32_e32 v44, v44
	v_exp_f32_e32 v45, v45
	v_add_f32_e32 v44, 1.0, v44
	v_add_f32_e32 v45, 1.0, v45
	v_rcp_f32_e32 v44, v44
	v_rcp_f32_e32 v45, v45
	s_nop 0
	v_pk_mul_f32 v[56:57], v[42:43], v[44:45]
	v_cvt_pk_bf16_f32 v42, v80, v81
	v_cvt_pk_bf16_f32 v43, v46, v47
	v_cvt_pk_bf16_f32 v44, v90, v91
	v_cvt_pk_bf16_f32 v45, v48, v49
	v_lshl_add_u32 v90, v88, 1, v85
	ds_write_b128 v90, v[42:45] offset:34560
	v_cvt_pk_bf16_f32 v42, v86, v87
	v_cvt_pk_bf16_f32 v43, v92, v93
	v_cvt_pk_bf16_f32 v44, v94, v95
	v_cvt_pk_bf16_f32 v45, v56, v57
	ds_write_b128 v90, v[42:45] offset:34832
	v_add_co_u32_e32 v42, vcc, s79, v62
	v_pk_fma_f32 v[56:57], v[22:23], v[66:67], v[38:39]
	s_nop 0
	v_addc_co_u32_e32 v43, vcc, 0, v63, vcc
	global_load_dwordx4 v[42:45], v[42:43], off offset:3072
	v_add_co_u32_e32 v46, vcc, s81, v62
	v_pk_fma_f32 v[56:57], v[26:27], v[68:69], v[56:57]
	s_nop 0
	v_addc_co_u32_e32 v47, vcc, 0, v63, vcc
	global_load_dwordx4 v[46:49], v[46:47], off offset:2560
	v_pk_fma_f32 v[56:57], v[30:31], v[64:65], v[56:57]
	s_waitcnt vmcnt(1)
	v_lshlrev_b32_e32 v86, 16, v42
	v_and_b32_e32 v87, 0xffff0000, v42
	v_pk_fma_f32 v[56:57], v[34:35], v[86:87], v[56:57]
	v_lshlrev_b32_e32 v80, 16, v43
	v_mul_f32_e32 v42, 0xbfb8aa3b, v56
	v_exp_f32_e32 v42, v42
	s_waitcnt vmcnt(0)
	v_lshlrev_b32_e32 v66, 16, v46
	v_and_b32_e32 v67, 0xffff0000, v46
	v_and_b32_e32 v81, 0xffff0000, v43
	v_add_f32_e32 v42, 1.0, v42
	v_rcp_f32_e32 v60, v42
	v_mul_f32_e32 v42, 0xbfb8aa3b, v57
	v_exp_f32_e32 v42, v42
	v_lshlrev_b32_e32 v88, 16, v44
	v_and_b32_e32 v89, 0xffff0000, v44
	v_add_f32_e32 v42, 1.0, v42
	v_rcp_f32_e32 v61, v42
	s_nop 0
	v_pk_mul_f32 v[92:93], v[56:57], v[60:61]
	v_pk_fma_f32 v[56:57], v[22:23], v[68:69], v[38:39]
	s_nop 0
	v_pk_fma_f32 v[56:57], v[26:27], v[64:65], v[56:57]
	v_pk_fma_f32 v[64:65], v[22:23], v[64:65], v[38:39]
	v_pk_fma_f32 v[56:57], v[30:31], v[86:87], v[56:57]
	v_pk_fma_f32 v[64:65], v[26:27], v[86:87], v[64:65]
	v_pk_fma_f32 v[56:57], v[34:35], v[66:67], v[56:57]
	v_pk_fma_f32 v[64:65], v[30:31], v[66:67], v[64:65]
	v_mul_f32_e32 v42, 0xbfb8aa3b, v56
	v_exp_f32_e32 v42, v42
	s_nop 0
	v_add_f32_e32 v42, 1.0, v42
	v_rcp_f32_e32 v60, v42
	v_mul_f32_e32 v42, 0xbfb8aa3b, v57
	v_exp_f32_e32 v42, v42
	s_nop 0
	v_add_f32_e32 v42, 1.0, v42
	v_rcp_f32_e32 v61, v42
	v_pk_fma_f32 v[42:43], v[24:25], v[70:71], v[40:41]
	v_pk_mul_f32 v[68:69], v[56:57], v[60:61]
	v_pk_fma_f32 v[42:43], v[28:29], v[58:59], v[42:43]
	v_lshlrev_b32_e32 v60, 16, v47
	v_pk_fma_f32 v[42:43], v[32:33], v[50:51], v[42:43]
	v_and_b32_e32 v61, 0xffff0000, v47
	v_pk_fma_f32 v[42:43], v[36:37], v[80:81], v[42:43]
	s_nop 0
	v_mul_f32_e32 v46, 0xbfb8aa3b, v42
	v_exp_f32_e32 v46, v46
	s_nop 0
	v_add_f32_e32 v46, 1.0, v46
	v_rcp_f32_e32 v56, v46
	v_mul_f32_e32 v46, 0xbfb8aa3b, v43
	v_exp_f32_e32 v46, v46
	s_nop 0
	v_add_f32_e32 v46, 1.0, v46
	v_rcp_f32_e32 v57, v46
	s_nop 0
	v_pk_mul_f32 v[70:71], v[42:43], v[56:57]
	v_pk_fma_f32 v[42:43], v[24:25], v[58:59], v[40:41]
	v_lshlrev_b32_e32 v58, 16, v48
	v_pk_fma_f32 v[42:43], v[28:29], v[50:51], v[42:43]
	v_and_b32_e32 v59, 0xffff0000, v48
	v_pk_fma_f32 v[42:43], v[32:33], v[80:81], v[42:43]
	s_nop 0
	v_pk_fma_f32 v[42:43], v[36:37], v[60:61], v[42:43]
	s_nop 0
	v_mul_f32_e32 v46, 0xbfb8aa3b, v42
	v_mul_f32_e32 v47, 0xbfb8aa3b, v43
	v_exp_f32_e32 v46, v46
	v_exp_f32_e32 v47, v47
	v_add_f32_e32 v46, 1.0, v46
	v_add_f32_e32 v47, 1.0, v47
	v_rcp_f32_e32 v46, v46
	v_rcp_f32_e32 v47, v47
	s_nop 0
	v_pk_mul_f32 v[46:47], v[42:43], v[46:47]
	v_pk_fma_f32 v[42:43], v[2:3], v[76:77], v[18:19]
	s_nop 0
	v_pk_fma_f32 v[42:43], v[6:7], v[72:73], v[42:43]
	s_nop 0
	v_pk_fma_f32 v[42:43], v[10:11], v[54:55], v[42:43]
	s_nop 0
	v_pk_fma_f32 v[42:43], v[14:15], v[88:89], v[42:43]
	s_nop 0
	v_mul_f32_e32 v44, 0xbfb8aa3b, v42
	v_exp_f32_e32 v44, v44
	s_nop 0
	v_add_f32_e32 v44, 1.0, v44
	v_rcp_f32_e32 v56, v44
	v_mul_f32_e32 v44, 0xbfb8aa3b, v43
	v_exp_f32_e32 v44, v44
	s_nop 0
	v_add_f32_e32 v44, 1.0, v44
	v_rcp_f32_e32 v57, v44
	s_nop 0
	v_pk_mul_f32 v[76:77], v[42:43], v[56:57]
	v_pk_fma_f32 v[42:43], v[2:3], v[72:73], v[18:19]
	v_lshlrev_b32_e32 v72, 16, v45
	v_pk_fma_f32 v[42:43], v[6:7], v[54:55], v[42:43]
	v_and_b32_e32 v73, 0xffff0000, v45
	v_pk_fma_f32 v[42:43], v[10:11], v[88:89], v[42:43]
	s_nop 0
	v_pk_fma_f32 v[42:43], v[14:15], v[58:59], v[42:43]
	s_nop 0
	v_mul_f32_e32 v44, 0xbfb8aa3b, v42
	v_exp_f32_e32 v44, v44
	s_nop 0
	v_add_f32_e32 v44, 1.0, v44
	v_rcp_f32_e32 v56, v44
	v_mul_f32_e32 v44, 0xbfb8aa3b, v43
	v_exp_f32_e32 v44, v44
	s_nop 0
	v_add_f32_e32 v44, 1.0, v44
	v_rcp_f32_e32 v57, v44
	s_nop 0
	v_pk_mul_f32 v[94:95], v[42:43], v[56:57]
	v_pk_fma_f32 v[42:43], v[4:5], v[78:79], v[20:21]
	v_lshlrev_b32_e32 v56, 16, v49
	v_pk_fma_f32 v[42:43], v[8:9], v[74:75], v[42:43]
	v_and_b32_e32 v57, 0xffff0000, v49
	v_pk_fma_f32 v[42:43], v[12:13], v[52:53], v[42:43]
	s_nop 0
	v_pk_fma_f32 v[42:43], v[16:17], v[72:73], v[42:43]
; #define LAS __attribute__((address_space(3)))
; __device__ __forceinline__ unsigned pk2(float lo, float hi) { const f32x2 v = {lo, hi}; return __builtin_bit_cast(unsigned, __builtin_convertvector(v, hwbf16x2)); }
; __device__ __forceinline__ float fsigmoid(float x) { return __builtin_amdgcn_rcpf(1.0f + __expf(-x)); }
; __device__ __forceinline__ void unpack8(const v4u q, float (&d)[8]) { d[0] = bflo(q.x); d[1] = bfhi(q.x); d[2] = bflo(q.y); d[3] = bfhi(q.y); d[4] = bflo(q.z); d[5] = bfhi(q.z); d[6] = bflo(q.w); d[7] = bfhi(q.w); }
; template <bool TR, bool SCALE>
; __device__ __forceinline__ void conv_task(const Params& p, const bf16* proj, size_t trow0, int tl0, int run, int xcol, LAS bf16* dst, int d0, const LAS float* sc) {
;     ...
;     for (int i = 0; i < 8; i += 2) {
;         float r3[8], r4[8], o0[8], o1[8];
;         unpack8(*(const v4u*)(src + (size_t)i * PROJ_LD), r3); unpack8(*(const v4u*)(src + (size_t)(i + 1) * PROJ_LD), r4);
; #pragma unroll
;         for (int j = 0; j < 8; ++j) { const float a0 = bb[j] + w[0][j] * r0[j] + w[1][j] * r1[j] + w[2][j] * r2[j] + w[3][j] * r3[j];
;             const float a1 = bb[j] + w[0][j] * r1[j] + w[1][j] * r2[j] + w[2][j] * r3[j] + w[3][j] * r4[j];
;             o0[j] = a0 * fsigmoid(a0); o1[j] = a1 * fsigmoid(a1); }
;         if constexpr (TR) {
;             float s0 = 1.f, s1 = 1.f; if constexpr (SCALE) { s0 = sc[l0 + i]; s1 = sc[l0 + i + 1]; }
; #pragma unroll
;             for (int j = 0; j < 8; ++j) *(LAS unsigned*)(dst + (d0 + j) * SPT + l0 + i) = pk2(o0[j] * s0, o1[j] * s1);
;         } else {
;             *(LAS v4u*)(dst + (l0 + i) * SPT + d0) = (v4u){pk2(o0[0], o0[1]), pk2(o0[2], o0[3]), pk2(o0[4], o0[5]), pk2(o0[6], o0[7])};
;             *(LAS v4u*)(dst + (l0 + i + 1) * SPT + d0) = (v4u){pk2(o1[0], o1[1]), pk2(o1[2], o1[3]), pk2(o1[4], o1[5]), pk2(o1[6], o1[7])};
;         }
; #pragma unroll
;         for (int j = 0; j < 8; ++j) { r0[j] = r2[j]; r1[j] = r3[j]; r2[j] = r4[j]; }
	s_nop 0
	v_mul_f32_e32 v44, 0xbfb8aa3b, v42
	v_mul_f32_e32 v45, 0xbfb8aa3b, v43
	v_exp_f32_e32 v44, v44
	v_exp_f32_e32 v45, v45
	v_add_f32_e32 v44, 1.0, v44
	v_add_f32_e32 v45, 1.0, v45
	v_rcp_f32_e32 v44, v44
	v_rcp_f32_e32 v45, v45
	s_nop 0
	v_pk_mul_f32 v[78:79], v[42:43], v[44:45]
	v_pk_fma_f32 v[42:43], v[4:5], v[74:75], v[20:21]
	s_nop 0
	v_pk_fma_f32 v[42:43], v[8:9], v[52:53], v[42:43]
	s_nop 0
	v_pk_fma_f32 v[42:43], v[12:13], v[72:73], v[42:43]
	s_nop 0
	v_pk_fma_f32 v[42:43], v[16:17], v[56:57], v[42:43]
	s_nop 0
	v_mul_f32_e32 v44, 0xbfb8aa3b, v42
	v_mul_f32_e32 v45, 0xbfb8aa3b, v43
	v_exp_f32_e32 v44, v44
	v_exp_f32_e32 v45, v45
	v_add_f32_e32 v44, 1.0, v44
	v_add_f32_e32 v45, 1.0, v45
	v_rcp_f32_e32 v44, v44
	v_rcp_f32_e32 v45, v45
	s_nop 0
	v_pk_mul_f32 v[48:49], v[42:43], v[44:45]
	v_cvt_pk_bf16_f32 v42, v92, v93
	v_cvt_pk_bf16_f32 v43, v70, v71
	v_cvt_pk_bf16_f32 v44, v76, v77
	v_cvt_pk_bf16_f32 v45, v78, v79
	ds_write_b128 v90, v[42:45] offset:35104
	v_cvt_pk_bf16_f32 v42, v68, v69
	v_cvt_pk_bf16_f32 v43, v46, v47
	v_cvt_pk_bf16_f32 v44, v94, v95
	v_cvt_pk_bf16_f32 v45, v48, v49
	ds_write_b128 v90, v[42:45] offset:35376
	v_add_co_u32_e32 v42, vcc, s82, v62
	s_nop 1
	v_addc_co_u32_e32 v43, vcc, 0, v63, vcc
	global_load_dwordx4 v[42:45], v[42:43], off offset:2048
	v_add_co_u32_e32 v46, vcc, s83, v62
	s_nop 1
	v_addc_co_u32_e32 v47, vcc, 0, v63, vcc
	global_load_dwordx4 v[46:49], v[46:47], off offset:1536
	s_waitcnt vmcnt(1)
	v_lshlrev_b32_e32 v68, 16, v42
	v_and_b32_e32 v69, 0xffff0000, v42
	v_pk_fma_f32 v[64:65], v[34:35], v[68:69], v[64:65]
	s_waitcnt vmcnt(0)
	v_lshlrev_b32_e32 v74, 16, v46
	v_mul_f32_e32 v42, 0xbfb8aa3b, v64
	v_exp_f32_e32 v42, v42
	v_and_b32_e32 v75, 0xffff0000, v46
	v_lshlrev_b32_e32 v76, 16, v47
	v_and_b32_e32 v77, 0xffff0000, v47
	v_add_f32_e32 v42, 1.0, v42
	v_rcp_f32_e32 v70, v42
	v_mul_f32_e32 v42, 0xbfb8aa3b, v65
	v_exp_f32_e32 v42, v42
	s_nop 0
	v_add_f32_e32 v42, 1.0, v42
	v_rcp_f32_e32 v71, v42
	s_nop 0
	v_pk_mul_f32 v[78:79], v[64:65], v[70:71]
	v_pk_fma_f32 v[64:65], v[22:23], v[86:87], v[38:39]
	s_nop 0
	v_pk_fma_f32 v[64:65], v[26:27], v[66:67], v[64:65]
	s_nop 0
	v_pk_fma_f32 v[64:65], v[30:31], v[68:69], v[64:65]
	s_nop 0
	v_pk_fma_f32 v[64:65], v[34:35], v[74:75], v[64:65]
	s_nop 0
	v_mul_f32_e32 v42, 0xbfb8aa3b, v64
	v_exp_f32_e32 v42, v42
	s_nop 0
	v_add_f32_e32 v42, 1.0, v42
	v_rcp_f32_e32 v70, v42
	v_mul_f32_e32 v42, 0xbfb8aa3b, v65
	v_exp_f32_e32 v42, v42
	s_nop 0
	v_add_f32_e32 v42, 1.0, v42
	v_rcp_f32_e32 v71, v42
	s_nop 0
	v_pk_mul_f32 v[86:87], v[64:65], v[70:71]
	v_lshlrev_b32_e32 v70, 16, v43
	v_and_b32_e32 v71, 0xffff0000, v43
	v_pk_fma_f32 v[42:43], v[24:25], v[50:51], v[40:41]
	v_lshlrev_b32_e32 v64, 16, v44
	v_pk_fma_f32 v[42:43], v[28:29], v[80:81], v[42:43]
	v_and_b32_e32 v65, 0xffff0000, v44
	v_pk_fma_f32 v[42:43], v[32:33], v[60:61], v[42:43]
	s_nop 0
	v_pk_fma_f32 v[42:43], v[36:37], v[70:71], v[42:43]
	s_nop 0
	v_mul_f32_e32 v46, 0xbfb8aa3b, v42
	v_exp_f32_e32 v46, v46
	s_nop 0
	v_add_f32_e32 v46, 1.0, v46
	v_rcp_f32_e32 v50, v46
	v_mul_f32_e32 v46, 0xbfb8aa3b, v43
	v_exp_f32_e32 v46, v46
	s_nop 0
	v_add_f32_e32 v46, 1.0, v46
	v_rcp_f32_e32 v51, v46
	s_nop 0
	v_pk_mul_f32 v[92:93], v[42:43], v[50:51]
	v_pk_fma_f32 v[42:43], v[24:25], v[80:81], v[40:41]
	s_nop 0
	v_pk_fma_f32 v[42:43], v[28:29], v[60:61], v[42:43]
	s_nop 0
	v_pk_fma_f32 v[42:43], v[32:33], v[70:71], v[42:43]
	s_nop 0
	v_pk_fma_f32 v[42:43], v[36:37], v[76:77], v[42:43]
	s_nop 0
	v_mul_f32_e32 v46, 0xbfb8aa3b, v42
	v_mul_f32_e32 v47, 0xbfb8aa3b, v43
	v_exp_f32_e32 v46, v46
	v_exp_f32_e32 v47, v47
	v_add_f32_e32 v46, 1.0, v46
	v_add_f32_e32 v47, 1.0, v47
	v_rcp_f32_e32 v46, v46
	v_rcp_f32_e32 v47, v47
	s_nop 0
	v_pk_mul_f32 v[46:47], v[42:43], v[46:47]
	v_pk_fma_f32 v[42:43], v[2:3], v[54:55], v[18:19]
	v_lshlrev_b32_e32 v54, 16, v48
	v_pk_fma_f32 v[42:43], v[6:7], v[88:89], v[42:43]
	v_and_b32_e32 v55, 0xffff0000, v48
	v_pk_fma_f32 v[42:43], v[10:11], v[58:59], v[42:43]
	s_nop 0
	v_pk_fma_f32 v[42:43], v[14:15], v[64:65], v[42:43]
	s_nop 0
	v_mul_f32_e32 v44, 0xbfb8aa3b, v42
	v_exp_f32_e32 v44, v44
	s_nop 0
	v_add_f32_e32 v44, 1.0, v44
	v_rcp_f32_e32 v50, v44
	v_mul_f32_e32 v44, 0xbfb8aa3b, v43
	v_exp_f32_e32 v44, v44
	s_nop 0
	v_add_f32_e32 v44, 1.0, v44
	v_rcp_f32_e32 v51, v44
	s_nop 0
	v_pk_mul_f32 v[80:81], v[42:43], v[50:51]
	v_pk_fma_f32 v[42:43], v[2:3], v[88:89], v[18:19]
	s_nop 0
	v_pk_fma_f32 v[42:43], v[6:7], v[58:59], v[42:43]
	s_nop 0
	v_pk_fma_f32 v[42:43], v[10:11], v[64:65], v[42:43]
	s_nop 0
	v_pk_fma_f32 v[42:43], v[14:15], v[54:55], v[42:43]
	s_nop 0
	v_mul_f32_e32 v44, 0xbfb8aa3b, v42
	v_exp_f32_e32 v44, v44
	s_nop 0
	v_add_f32_e32 v44, 1.0, v44
	v_rcp_f32_e32 v50, v44
	v_mul_f32_e32 v44, 0xbfb8aa3b, v43
	v_exp_f32_e32 v44, v44
	s_nop 0
	v_add_f32_e32 v44, 1.0, v44
	v_rcp_f32_e32 v51, v44
	s_nop 0
	v_pk_mul_f32 v[88:89], v[42:43], v[50:51]
	v_pk_fma_f32 v[42:43], v[4:5], v[52:53], v[20:21]
	v_lshlrev_b32_e32 v50, 16, v45
	v_pk_fma_f32 v[42:43], v[8:9], v[72:73], v[42:43]
	v_and_b32_e32 v51, 0xffff0000, v45
	v_pk_fma_f32 v[42:43], v[12:13], v[56:57], v[42:43]
	v_lshlrev_b32_e32 v52, 16, v49
	v_pk_fma_f32 v[42:43], v[16:17], v[50:51], v[42:43]
	v_and_b32_e32 v53, 0xffff0000, v49
	v_mul_f32_e32 v44, 0xbfb8aa3b, v42
	v_mul_f32_e32 v45, 0xbfb8aa3b, v43
	v_exp_f32_e32 v44, v44
	v_exp_f32_e32 v45, v45
	v_add_f32_e32 v44, 1.0, v44
	v_add_f32_e32 v45, 1.0, v45
	v_rcp_f32_e32 v44, v44
	v_rcp_f32_e32 v45, v45
	s_nop 0
	v_pk_mul_f32 v[94:95], v[42:43], v[44:45]
	v_pk_fma_f32 v[42:43], v[4:5], v[72:73], v[20:21]
	s_nop 0
	v_pk_fma_f32 v[42:43], v[8:9], v[56:57], v[42:43]
	s_nop 0
	v_pk_fma_f32 v[42:43], v[12:13], v[50:51], v[42:43]
	s_nop 0
	v_pk_fma_f32 v[42:43], v[16:17], v[52:53], v[42:43]
	s_nop 0
	v_mul_f32_e32 v44, 0xbfb8aa3b, v42
	v_mul_f32_e32 v45, 0xbfb8aa3b, v43
	v_exp_f32_e32 v44, v44
	v_exp_f32_e32 v45, v45
	v_add_f32_e32 v44, 1.0, v44
	v_add_f32_e32 v45, 1.0, v45
	v_rcp_f32_e32 v44, v44
	v_rcp_f32_e32 v45, v45
	s_nop 0
	v_pk_mul_f32 v[48:49], v[42:43], v[44:45]
	v_cvt_pk_bf16_f32 v42, v78, v79
	v_cvt_pk_bf16_f32 v43, v92, v93
	v_cvt_pk_bf16_f32 v44, v80, v81
	v_cvt_pk_bf16_f32 v45, v94, v95
	ds_write_b128 v90, v[42:45] offset:35648
	v_cvt_pk_bf16_f32 v42, v86, v87
	v_cvt_pk_bf16_f32 v43, v46, v47
	v_cvt_pk_bf16_f32 v44, v88, v89
	v_cvt_pk_bf16_f32 v45, v48, v49
	ds_write_b128 v90, v[42:45] offset:35920
	v_add_co_u32_e32 v42, vcc, s92, v62
	s_nop 1
	v_addc_co_u32_e32 v43, vcc, 0, v63, vcc
	global_load_dwordx4 v[46:49], v[42:43], off offset:1024
	v_add_co_u32_e32 v42, vcc, s93, v62
	s_waitcnt vmcnt(0)
; #define LAS __attribute__((address_space(3)))
; __device__ __forceinline__ unsigned pk2(float lo, float hi) { const f32x2 v = {lo, hi}; return __builtin_bit_cast(unsigned, __builtin_convertvector(v, hwbf16x2)); }
; __device__ __forceinline__ float fsigmoid(float x) { return __builtin_amdgcn_rcpf(1.0f + __expf(-x)); }
; __device__ __forceinline__ void unpack8(const v4u q, float (&d)[8]) { d[0] = bflo(q.x); d[1] = bfhi(q.x); d[2] = bflo(q.y); d[3] = bfhi(q.y); d[4] = bflo(q.z); d[5] = bfhi(q.z); d[6] = bflo(q.w); d[7] = bfhi(q.w); }
; template <bool TR, bool SCALE>
; __device__ __forceinline__ void conv_task(const Params& p, const bf16* proj, size_t trow0, int tl0, int run, int xcol, LAS bf16* dst, int d0, const LAS float* sc) {
;     ...
;     for (int i = 0; i < 8; i += 2) {
;         float r3[8], r4[8], o0[8], o1[8];
;         unpack8(*(const v4u*)(src + (size_t)i * PROJ_LD), r3); unpack8(*(const v4u*)(src + (size_t)(i + 1) * PROJ_LD), r4);
; #pragma unroll
;         for (int j = 0; j < 8; ++j) { const float a0 = bb[j] + w[0][j] * r0[j] + w[1][j] * r1[j] + w[2][j] * r2[j] + w[3][j] * r3[j];
;             const float a1 = bb[j] + w[0][j] * r1[j] + w[1][j] * r2[j] + w[2][j] * r3[j] + w[3][j] * r4[j];
;             o0[j] = a0 * fsigmoid(a0); o1[j] = a1 * fsigmoid(a1); }
;         if constexpr (TR) {
;             float s0 = 1.f, s1 = 1.f; if constexpr (SCALE) { s0 = sc[l0 + i]; s1 = sc[l0 + i + 1]; }
; #pragma unroll
;             for (int j = 0; j < 8; ++j) *(LAS unsigned*)(dst + (d0 + j) * SPT + l0 + i) = pk2(o0[j] * s0, o1[j] * s1);
;         } else {
;             *(LAS v4u*)(dst + (l0 + i) * SPT + d0) = (v4u){pk2(o0[0], o0[1]), pk2(o0[2], o0[3]), pk2(o0[4], o0[5]), pk2(o0[6], o0[7])};
;             *(LAS v4u*)(dst + (l0 + i + 1) * SPT + d0) = (v4u){pk2(o1[0], o1[1]), pk2(o1[2], o1[3]), pk2(o1[4], o1[5]), pk2(o1[6], o1[7])};
;         }
; #pragma unroll
;         for (int j = 0; j < 8; ++j) { r0[j] = r2[j]; r1[j] = r3[j]; r2[j] = r4[j]; }
	v_lshlrev_b32_e32 v72, 16, v46
	v_addc_co_u32_e32 v43, vcc, 0, v63, vcc
	global_load_dwordx4 v[42:45], v[42:43], off offset:512
	v_pk_fma_f32 v[62:63], v[22:23], v[66:67], v[38:39]
	v_and_b32_e32 v73, 0xffff0000, v46
	v_pk_fma_f32 v[62:63], v[26:27], v[68:69], v[62:63]
	v_pk_fma_f32 v[22:23], v[22:23], v[68:69], v[38:39]
	v_pk_fma_f32 v[62:63], v[30:31], v[74:75], v[62:63]
	v_pk_fma_f32 v[22:23], v[26:27], v[74:75], v[22:23]
	v_pk_fma_f32 v[62:63], v[34:35], v[72:73], v[62:63]
	v_pk_fma_f32 v[22:23], v[30:31], v[72:73], v[22:23]
	v_mul_f32_e32 v46, 0xbfb8aa3b, v62
	v_exp_f32_e32 v46, v46
	v_pk_fma_f32 v[30:31], v[24:25], v[60:61], v[40:41]
	v_pk_fma_f32 v[24:25], v[24:25], v[70:71], v[40:41]
	v_pk_fma_f32 v[30:31], v[28:29], v[70:71], v[30:31]
	v_add_f32_e32 v46, 1.0, v46
	v_rcp_f32_e32 v66, v46
	v_mul_f32_e32 v46, 0xbfb8aa3b, v63
	v_exp_f32_e32 v46, v46
	v_pk_fma_f32 v[30:31], v[32:33], v[76:77], v[30:31]
	v_pk_fma_f32 v[24:25], v[28:29], v[76:77], v[24:25]
	v_pk_fma_f32 v[28:29], v[2:3], v[58:59], v[18:19]
	v_add_f32_e32 v46, 1.0, v46
	v_rcp_f32_e32 v67, v46
	v_pk_fma_f32 v[28:29], v[6:7], v[64:65], v[28:29]
	v_pk_fma_f32 v[2:3], v[2:3], v[64:65], v[18:19]
	v_pk_fma_f32 v[28:29], v[10:11], v[54:55], v[28:29]
	v_pk_mul_f32 v[62:63], v[62:63], v[66:67]
	v_pk_fma_f32 v[2:3], v[6:7], v[54:55], v[2:3]
	s_waitcnt vmcnt(0)
	v_lshlrev_b32_e32 v66, 16, v42
	v_and_b32_e32 v67, 0xffff0000, v42
	v_pk_fma_f32 v[22:23], v[34:35], v[66:67], v[22:23]
	s_nop 0
	v_mul_f32_e32 v26, 0xbfb8aa3b, v22
	v_mul_f32_e32 v27, 0xbfb8aa3b, v23
	v_exp_f32_e32 v26, v26
	v_exp_f32_e32 v27, v27
	v_add_f32_e32 v26, 1.0, v26
	v_add_f32_e32 v27, 1.0, v27
	v_rcp_f32_e32 v26, v26
	v_rcp_f32_e32 v27, v27
	s_nop 0
	v_pk_mul_f32 v[22:23], v[22:23], v[26:27]
	v_lshlrev_b32_e32 v26, 16, v47
	v_and_b32_e32 v27, 0xffff0000, v47
	v_pk_fma_f32 v[30:31], v[36:37], v[26:27], v[30:31]
	v_pk_fma_f32 v[24:25], v[32:33], v[26:27], v[24:25]
	v_mul_f32_e32 v34, 0xbfb8aa3b, v30
	v_mul_f32_e32 v35, 0xbfb8aa3b, v31
	v_exp_f32_e32 v34, v34
	v_exp_f32_e32 v35, v35
	v_add_f32_e32 v34, 1.0, v34
	v_add_f32_e32 v35, 1.0, v35
	v_rcp_f32_e32 v34, v34
	v_rcp_f32_e32 v35, v35
	s_nop 0
	v_pk_mul_f32 v[30:31], v[30:31], v[34:35]
	v_lshlrev_b32_e32 v34, 16, v43
	v_and_b32_e32 v35, 0xffff0000, v43
	v_pk_fma_f32 v[24:25], v[36:37], v[34:35], v[24:25]
	s_nop 0
	v_mul_f32_e32 v26, 0xbfb8aa3b, v24
	v_mul_f32_e32 v27, 0xbfb8aa3b, v25
	v_exp_f32_e32 v26, v26
	v_exp_f32_e32 v27, v27
	v_add_f32_e32 v26, 1.0, v26
	v_add_f32_e32 v27, 1.0, v27
	v_rcp_f32_e32 v26, v26
	v_rcp_f32_e32 v27, v27
	s_nop 0
	v_pk_mul_f32 v[24:25], v[24:25], v[26:27]
	v_lshlrev_b32_e32 v26, 16, v48
	v_and_b32_e32 v27, 0xffff0000, v48
	v_pk_fma_f32 v[28:29], v[14:15], v[26:27], v[28:29]
	v_pk_fma_f32 v[2:3], v[10:11], v[26:27], v[2:3]
	v_mul_f32_e32 v32, 0xbfb8aa3b, v28
	v_mul_f32_e32 v33, 0xbfb8aa3b, v29
	v_exp_f32_e32 v32, v32
	v_exp_f32_e32 v33, v33
	v_pk_fma_f32 v[10:11], v[4:5], v[56:57], v[20:21]
	v_pk_fma_f32 v[4:5], v[4:5], v[50:51], v[20:21]
	v_add_f32_e32 v32, 1.0, v32
	v_add_f32_e32 v33, 1.0, v33
	v_rcp_f32_e32 v32, v32
	v_rcp_f32_e32 v33, v33
	v_pk_fma_f32 v[10:11], v[8:9], v[50:51], v[10:11]
	v_pk_fma_f32 v[4:5], v[8:9], v[52:53], v[4:5]
	v_pk_fma_f32 v[10:11], v[12:13], v[52:53], v[10:11]
	v_pk_mul_f32 v[28:29], v[28:29], v[32:33]
	v_lshlrev_b32_e32 v32, 16, v44
	v_and_b32_e32 v33, 0xffff0000, v44
	v_pk_fma_f32 v[2:3], v[14:15], v[32:33], v[2:3]
	s_nop 0
	v_mul_f32_e32 v6, 0xbfb8aa3b, v2
	v_mul_f32_e32 v7, 0xbfb8aa3b, v3
	v_exp_f32_e32 v6, v6
	v_exp_f32_e32 v7, v7
	v_add_f32_e32 v6, 1.0, v6
	v_add_f32_e32 v7, 1.0, v7
	v_rcp_f32_e32 v6, v6
	v_rcp_f32_e32 v7, v7
	s_nop 0
	v_pk_mul_f32 v[6:7], v[2:3], v[6:7]
	v_lshlrev_b32_e32 v2, 16, v49
	v_and_b32_e32 v3, 0xffff0000, v49
	v_pk_fma_f32 v[10:11], v[16:17], v[2:3], v[10:11]
	v_pk_fma_f32 v[2:3], v[12:13], v[2:3], v[4:5]
	v_mul_f32_e32 v14, 0xbfb8aa3b, v10
	v_mul_f32_e32 v15, 0xbfb8aa3b, v11
	v_exp_f32_e32 v14, v14
	v_exp_f32_e32 v15, v15
	v_add_f32_e32 v14, 1.0, v14
	v_add_f32_e32 v15, 1.0, v15
	v_rcp_f32_e32 v14, v14
	v_rcp_f32_e32 v15, v15
	s_nop 0
	v_pk_mul_f32 v[10:11], v[10:11], v[14:15]
	v_lshlrev_b32_e32 v14, 16, v45
	v_and_b32_e32 v15, 0xffff0000, v45
	v_pk_fma_f32 v[2:3], v[16:17], v[14:15], v[2:3]
	s_nop 0
	v_mul_f32_e32 v4, 0xbfb8aa3b, v2
	v_mul_f32_e32 v5, 0xbfb8aa3b, v3
	v_exp_f32_e32 v4, v4
	v_exp_f32_e32 v5, v5
	v_add_f32_e32 v4, 1.0, v4
	v_add_f32_e32 v5, 1.0, v5
	v_rcp_f32_e32 v4, v4
	v_rcp_f32_e32 v5, v5
	s_nop 0
	v_pk_mul_f32 v[8:9], v[2:3], v[4:5]
	v_cvt_pk_bf16_f32 v2, v62, v63
	v_cvt_pk_bf16_f32 v3, v30, v31
	v_cvt_pk_bf16_f32 v4, v28, v29
	v_cvt_pk_bf16_f32 v5, v10, v11
	ds_write_b128 v90, v[2:5] offset:36192
	v_cvt_pk_bf16_f32 v2, v22, v23
	v_cvt_pk_bf16_f32 v3, v24, v25
	v_cvt_pk_bf16_f32 v4, v6, v7
	v_cvt_pk_bf16_f32 v5, v8, v9
	ds_write_b128 v90, v[2:5] offset:36464
	s_or_b64 exec, exec, s[10:11]

; #define LAS __attribute__((address_space(3)))
; __device__ __forceinline__ unsigned pk2(float lo, float hi) { const f32x2 v = {lo, hi}; return __builtin_bit_cast(unsigned, __builtin_convertvector(v, hwbf16x2)); }
; __device__ __forceinline__ float fsigmoid(float x) { return __builtin_amdgcn_rcpf(1.0f + __expf(-x)); }
; __device__ __forceinline__ void unpack8(const v4u q, float (&d)[8]) { d[0] = bflo(q.x); d[1] = bfhi(q.x); d[2] = bflo(q.y); d[3] = bfhi(q.y); d[4] = bflo(q.z); d[5] = bfhi(q.z); d[6] = bflo(q.w); d[7] = bfhi(q.w); }
; template <bool TR, bool SCALE>
; __device__ __forceinline__ void conv_task(const Params& p, const bf16* proj, size_t trow0, int tl0, int run, int xcol, LAS bf16* dst, int d0, const LAS float* sc) {
;     ...
;     const int l0 = run * 8; const bf16* src = proj + (trow0 + l0) * PROJ_LD + COL_XBC + xcol;
;     float r0[8], r1[8], r2[8];
;     { const int pos = tl0 + l0; v4u q0 = (v4u){0u, 0u, 0u, 0u}, q1 = q0, q2 = q0;
;       if (pos - 3 >= 0) q0 = *(const v4u*)(src - 3 * PROJ_LD);
;       if (pos - 2 >= 0) q1 = *(const v4u*)(src - 2 * PROJ_LD);
;       if (pos - 1 >= 0) q2 = *(const v4u*)(src - 1 * PROJ_LD);
;       unpack8(q0, r0); unpack8(q1, r1); unpack8(q2, r2); }
; #pragma unroll
;     for (int i = 0; i < 8; i += 2) {
;         float r3[8], r4[8], o0[8], o1[8];
;         unpack8(*(const v4u*)(src + (size_t)i * PROJ_LD), r3); unpack8(*(const v4u*)(src + (size_t)(i + 1) * PROJ_LD), r4);
; #pragma unroll
;         for (int j = 0; j < 8; ++j) { const float a0 = bb[j] + w[0][j] * r0[j] + w[1][j] * r1[j] + w[2][j] * r2[j] + w[3][j] * r3[j];
;             const float a1 = bb[j] + w[0][j] * r1[j] + w[1][j] * r2[j] + w[2][j] * r3[j] + w[3][j] * r4[j];
;             o0[j] = a0 * fsigmoid(a0); o1[j] = a1 * fsigmoid(a1); }
;         if constexpr (TR) {
;             float s0 = 1.f, s1 = 1.f; if constexpr (SCALE) { s0 = sc[l0 + i]; s1 = sc[l0 + i + 1]; }
; #pragma unroll
;             for (int j = 0; j < 8; ++j) *(LAS unsigned*)(dst + (d0 + j) * SPT + l0 + i) = pk2(o0[j] * s0, o1[j] * s1);
; __device__ __forceinline__ void phase_ssd_out(const Params& p, LAS unsigned char* lds, int G, int lane, int wave) {
;     ...
;         { int tz_ = threadIdx.x; asm volatile("" : "+v"(tz_)); const int cg = tz_ >> 4, run = tz_ & 15; conv_task<true, false>(p, proj, trow0, tl0, run, (h0 + 4) * 64 + cg * 8, XT, cg * 8, nullptr); }
.LBB0_493:
	s_or_b64 exec, exec, s[6:7]
	v_add_co_u32_e32 v58, vcc, s78, v80
	v_lshlrev_b32_e32 v71, 1, v54
	global_load_dwordx4 v[54:57], v[80:81], off
	v_addc_co_u32_e32 v59, vcc, 0, v81, vcc
	global_load_dwordx4 v[58:61], v[58:59], off offset:3584
	v_add_co_u32_e32 v248, vcc, s79, v80
	s_nop 1
	v_addc_co_u32_e32 v249, vcc, 0, v81, vcc
	global_load_dword v246, v[248:249], off offset:3072
	v_add_co_u32_e32 v248, vcc, s81, v80
	s_nop 1
	v_addc_co_u32_e32 v249, vcc, 0, v81, vcc
	global_load_dword v246, v[248:249], off offset:2560
	v_add_co_u32_e32 v248, vcc, s82, v80
	s_nop 1
	v_addc_co_u32_e32 v249, vcc, 0, v81, vcc
	global_load_dword v246, v[248:249], off offset:2048
	v_add_co_u32_e32 v248, vcc, s83, v80
	s_nop 1
	v_addc_co_u32_e32 v249, vcc, 0, v81, vcc
	global_load_dword v246, v[248:249], off offset:1536
	v_add_co_u32_e32 v248, vcc, s92, v80
	s_nop 1
	v_addc_co_u32_e32 v249, vcc, 0, v81, vcc
	global_load_dword v246, v[248:249], off offset:1024
	v_add_co_u32_e32 v248, vcc, s93, v80
	s_nop 1
	v_addc_co_u32_e32 v249, vcc, 0, v81, vcc
	global_load_dword v246, v[248:249], off offset:512
	s_waitcnt vmcnt(2)
	v_lshlrev_b32_e32 v63, 16, v42
	v_lshlrev_b32_e32 v62, 16, v46
	v_lshlrev_b32_e32 v64, 16, v50
	v_mov_b32_e32 v66, v63
	v_mov_b32_e32 v67, v64
	v_pk_fma_f32 v[62:63], v[22:23], v[62:63], v[38:39] op_sel_hi:[0,1,0]
	v_pk_fma_f32 v[62:63], v[26:27], v[66:67], v[62:63] op_sel_hi:[0,1,1]
	v_and_b32_e32 v73, 0xffff0000, v50
	v_mov_b32_e32 v112, v73
	v_lshlrev_b32_e32 v116, 16, v51
	v_mov_b32_e32 v75, v116
	v_mov_b32_e32 v82, v25
	v_mov_b32_e32 v84, v41
	v_mov_b32_e32 v86, v29
	v_mov_b32_e32 v88, v33
	v_mov_b32_e32 v90, v37
	v_lshlrev_b32_e32 v124, 16, v52
	v_mov_b32_e32 v102, v3
	v_mov_b32_e32 v104, v19
	v_mov_b32_e32 v106, v7
	v_mov_b32_e32 v108, v11
	v_mov_b32_e32 v110, v15
	v_lshlrev_b32_e32 v132, 16, v53
	v_mov_b32_e32 v92, v5
	v_mov_b32_e32 v94, v21
	v_mov_b32_e32 v96, v9
	v_mov_b32_e32 v98, v13
	v_mov_b32_e32 v100, v17
	v_mul_lo_u32 v1, v1, s80
	v_add3_u32 v1, s77, v71, v1
	s_waitcnt vmcnt(1)
	v_lshlrev_b32_e32 v65, 16, v54
	v_mov_b32_e32 v68, v65
	v_pk_fma_f32 v[62:63], v[30:31], v[64:65], v[62:63] op_sel_hi:[0,1,1]
	s_waitcnt vmcnt(0)
	v_lshlrev_b32_e32 v69, 16, v58
	v_pk_fma_f32 v[62:63], v[34:35], v[68:69], v[62:63] op_sel_hi:[0,1,1]
	v_mul_f32_e32 v66, 0xbfb8aa3b, v62
	v_mul_f32_e32 v67, 0xbfb8aa3b, v63
	v_exp_f32_e32 v66, v66
	v_exp_f32_e32 v67, v67
	v_and_b32_e32 v113, 0xffff0000, v54
	v_and_b32_e32 v115, 0xffff0000, v58
	v_add_f32_e32 v66, 1.0, v66
	v_add_f32_e32 v67, 1.0, v67
	v_rcp_f32_e32 v66, v66
	v_rcp_f32_e32 v67, v67
	v_mov_b32_e32 v114, v113
	v_lshlrev_b32_e32 v117, 16, v55
	v_lshlrev_b32_e32 v119, 16, v59
	v_pk_mul_f32 v[62:63], v[62:63], v[66:67]
	v_and_b32_e32 v67, 0xffff0000, v42
	v_and_b32_e32 v66, 0xffff0000, v46
	v_mov_b32_e32 v72, v67
	v_pk_fma_f32 v[66:67], v[22:23], v[66:67], v[38:39] op_sel:[1,0,1]
	v_mov_b32_e32 v118, v117
	v_pk_fma_f32 v[66:67], v[26:27], v[72:73], v[66:67] op_sel:[1,0,0]
	v_and_b32_e32 v121, 0xffff0000, v55
	v_pk_fma_f32 v[66:67], v[30:31], v[112:113], v[66:67] op_sel:[1,0,0]
	v_and_b32_e32 v123, 0xffff0000, v59
	v_pk_fma_f32 v[66:67], v[34:35], v[114:115], v[66:67] op_sel:[1,0,0]
	v_mov_b32_e32 v122, v121
	v_mul_f32_e32 v42, 0xbfb8aa3b, v66
	v_exp_f32_e32 v42, v42
	v_lshlrev_b32_e32 v125, 16, v56
	v_lshlrev_b32_e32 v127, 16, v60
	v_mov_b32_e32 v126, v125
	v_add_f32_e32 v42, 1.0, v42
	v_rcp_f32_e32 v72, v42
	v_mul_f32_e32 v42, 0xbfb8aa3b, v67
	v_exp_f32_e32 v42, v42
	v_and_b32_e32 v55, 0xffff0000, v52
	v_and_b32_e32 v129, 0xffff0000, v56
	v_mov_b32_e32 v128, v55
	v_add_f32_e32 v42, 1.0, v42
	v_rcp_f32_e32 v73, v42
	v_and_b32_e32 v131, 0xffff0000, v60
	v_mov_b32_e32 v130, v129
	v_mov_b32_e32 v59, v132
	v_pk_mul_f32 v[66:67], v[66:67], v[72:73]
	v_lshlrev_b32_e32 v72, 16, v47
	v_lshlrev_b32_e32 v73, 16, v43
	v_mov_b32_e32 v74, v73
	v_pk_fma_f32 v[72:73], v[24:25], v[72:73], v[40:41] op_sel_hi:[0,1,0]
	v_pk_fma_f32 v[72:73], v[28:29], v[74:75], v[72:73] op_sel_hi:[0,1,1]
	v_pk_fma_f32 v[72:73], v[32:33], v[116:117], v[72:73] op_sel_hi:[0,1,1]
	v_pk_fma_f32 v[72:73], v[36:37], v[118:119], v[72:73] op_sel_hi:[0,1,1]
	v_mul_f32_e32 v42, 0xbfb8aa3b, v72
	v_exp_f32_e32 v42, v42
	v_and_b32_e32 v43, 0xffff0000, v43
	v_mov_b32_e32 v46, v43
	v_lshlrev_b32_e32 v133, 16, v57
	v_add_f32_e32 v42, 1.0, v42
	v_rcp_f32_e32 v74, v42
	v_mul_f32_e32 v42, 0xbfb8aa3b, v73
	v_exp_f32_e32 v42, v42
	v_lshlrev_b32_e32 v135, 16, v61
	v_mov_b32_e32 v134, v133
	v_and_b32_e32 v137, 0xffff0000, v57
	v_add_f32_e32 v42, 1.0, v42
	v_rcp_f32_e32 v75, v42
	v_and_b32_e32 v42, 0xffff0000, v47
	v_and_b32_e32 v47, 0xffff0000, v51
	v_pk_fma_f32 v[42:43], v[82:83], v[42:43], v[84:85] op_sel_hi:[0,1,0]
	v_mov_b32_e32 v120, v47
	v_pk_fma_f32 v[42:43], v[86:87], v[46:47], v[42:43] op_sel_hi:[0,1,1]
	v_pk_fma_f32 v[42:43], v[88:89], v[120:121], v[42:43] op_sel_hi:[0,1,1]
	v_pk_fma_f32 v[42:43], v[90:91], v[122:123], v[42:43] op_sel_hi:[0,1,1]
	v_mul_f32_e32 v46, 0xbfb8aa3b, v42
	v_mul_f32_e32 v47, 0xbfb8aa3b, v43
	v_exp_f32_e32 v46, v46
	v_exp_f32_e32 v47, v47
	v_mov_b32_e32 v51, v124
	v_and_b32_e32 v61, 0xffff0000, v61
	v_add_f32_e32 v46, 1.0, v46
	v_add_f32_e32 v47, 1.0, v47
	v_rcp_f32_e32 v46, v46
	v_rcp_f32_e32 v47, v47
	v_mov_b32_e32 v60, v137
	v_pk_mul_f32 v[72:73], v[72:73], v[74:75]
	v_cvt_pk_bf16_f32 v70, v62, v63
	v_pk_mul_f32 v[42:43], v[42:43], v[46:47]
	v_lshlrev_b32_e32 v47, 16, v44
	v_lshlrev_b32_e32 v46, 16, v48
	v_mov_b32_e32 v50, v47
	v_pk_fma_f32 v[46:47], v[2:3], v[46:47], v[18:19] op_sel_hi:[0,1,0]
	v_pk_fma_f32 v[46:47], v[6:7], v[50:51], v[46:47] op_sel_hi:[0,1,1]
	v_pk_fma_f32 v[46:47], v[10:11], v[124:125], v[46:47] op_sel_hi:[0,1,1]
; #define LAS __attribute__((address_space(3)))
; __device__ __forceinline__ unsigned pk2(float lo, float hi) { const f32x2 v = {lo, hi}; return __builtin_bit_cast(unsigned, __builtin_convertvector(v, hwbf16x2)); }
; __device__ __forceinline__ float fsigmoid(float x) { return __builtin_amdgcn_rcpf(1.0f + __expf(-x)); }
; __device__ __forceinline__ void unpack8(const v4u q, float (&d)[8]) { d[0] = bflo(q.x); d[1] = bfhi(q.x); d[2] = bflo(q.y); d[3] = bfhi(q.y); d[4] = bflo(q.z); d[5] = bfhi(q.z); d[6] = bflo(q.w); d[7] = bfhi(q.w); }
; template <bool TR, bool SCALE>
; __device__ __forceinline__ void conv_task(const Params& p, const bf16* proj, size_t trow0, int tl0, int run, int xcol, LAS bf16* dst, int d0, const LAS float* sc) {
;     ...
;     for (int i = 0; i < 8; i += 2) {
;         float r3[8], r4[8], o0[8], o1[8];
;         unpack8(*(const v4u*)(src + (size_t)i * PROJ_LD), r3); unpack8(*(const v4u*)(src + (size_t)(i + 1) * PROJ_LD), r4);
; #pragma unroll
;         for (int j = 0; j < 8; ++j) { const float a0 = bb[j] + w[0][j] * r0[j] + w[1][j] * r1[j] + w[2][j] * r2[j] + w[3][j] * r3[j];
;             const float a1 = bb[j] + w[0][j] * r1[j] + w[1][j] * r2[j] + w[2][j] * r3[j] + w[3][j] * r4[j];
;             o0[j] = a0 * fsigmoid(a0); o1[j] = a1 * fsigmoid(a1); }
;         if constexpr (TR) {
;             float s0 = 1.f, s1 = 1.f; if constexpr (SCALE) { s0 = sc[l0 + i]; s1 = sc[l0 + i + 1]; }
; #pragma unroll
;             for (int j = 0; j < 8; ++j) *(LAS unsigned*)(dst + (d0 + j) * SPT + l0 + i) = pk2(o0[j] * s0, o1[j] * s1);
;         } else {
;             *(LAS v4u*)(dst + (l0 + i) * SPT + d0) = (v4u){pk2(o0[0], o0[1]), pk2(o0[2], o0[3]), pk2(o0[4], o0[5]), pk2(o0[6], o0[7])};
;             *(LAS v4u*)(dst + (l0 + i + 1) * SPT + d0) = (v4u){pk2(o1[0], o1[1]), pk2(o1[2], o1[3]), pk2(o1[4], o1[5]), pk2(o1[6], o1[7])};
;         }
; #pragma unroll
;         for (int j = 0; j < 8; ++j) { r0[j] = r2[j]; r1[j] = r3[j]; r2[j] = r4[j]; }
	v_pk_fma_f32 v[46:47], v[14:15], v[126:127], v[46:47] op_sel_hi:[0,1,1]
	v_mul_f32_e32 v50, 0xbfb8aa3b, v46
	v_mul_f32_e32 v51, 0xbfb8aa3b, v47
	v_exp_f32_e32 v50, v50
	v_exp_f32_e32 v51, v51
	v_cvt_pk_bf16_f32 v62, v72, v73
	v_cvt_pk_bf16_f32 v66, v66, v67
	v_add_f32_e32 v50, 1.0, v50
	v_add_f32_e32 v51, 1.0, v51
	v_rcp_f32_e32 v50, v50
	v_rcp_f32_e32 v51, v51
	s_nop 0
	v_pk_mul_f32 v[46:47], v[46:47], v[50:51]
	v_and_b32_e32 v51, 0xffff0000, v44
	v_and_b32_e32 v50, 0xffff0000, v48
	v_mov_b32_e32 v54, v51
	v_pk_fma_f32 v[50:51], v[102:103], v[50:51], v[104:105] op_sel_hi:[0,1,0]
	v_pk_fma_f32 v[50:51], v[106:107], v[54:55], v[50:51] op_sel_hi:[0,1,1]
	v_pk_fma_f32 v[50:51], v[108:109], v[128:129], v[50:51] op_sel_hi:[0,1,1]
	v_pk_fma_f32 v[50:51], v[110:111], v[130:131], v[50:51] op_sel_hi:[0,1,1]
	v_mul_f32_e32 v3, 0xbfb8aa3b, v50
	v_exp_f32_e32 v3, v3
	v_and_b32_e32 v44, 0xffff0000, v49
	v_add_f32_e32 v3, 1.0, v3
	v_rcp_f32_e32 v54, v3
	v_mul_f32_e32 v3, 0xbfb8aa3b, v51
	v_exp_f32_e32 v3, v3
	s_nop 0
	v_add_f32_e32 v3, 1.0, v3
	v_rcp_f32_e32 v55, v3
	s_nop 0
	v_pk_mul_f32 v[50:51], v[50:51], v[54:55]
	v_lshlrev_b32_e32 v54, 16, v49
	v_lshlrev_b32_e32 v55, 16, v45
	v_mov_b32_e32 v58, v55
	v_pk_fma_f32 v[54:55], v[4:5], v[54:55], v[20:21] op_sel_hi:[0,1,0]
	v_pk_fma_f32 v[54:55], v[8:9], v[58:59], v[54:55] op_sel_hi:[0,1,1]
	v_pk_fma_f32 v[54:55], v[12:13], v[132:133], v[54:55] op_sel_hi:[0,1,1]
	v_pk_fma_f32 v[54:55], v[16:17], v[134:135], v[54:55] op_sel_hi:[0,1,1]
	v_mul_f32_e32 v3, 0xbfb8aa3b, v54
	v_exp_f32_e32 v3, v3
	v_and_b32_e32 v45, 0xffff0000, v45
	v_and_b32_e32 v49, 0xffff0000, v53
	v_mov_b32_e32 v48, v45
	v_add_f32_e32 v3, 1.0, v3
	v_rcp_f32_e32 v58, v3
	v_mul_f32_e32 v3, 0xbfb8aa3b, v55
	v_exp_f32_e32 v3, v3
	v_pk_fma_f32 v[44:45], v[92:93], v[44:45], v[94:95] op_sel_hi:[0,1,0]
	v_mov_b32_e32 v136, v49
	v_pk_fma_f32 v[44:45], v[96:97], v[48:49], v[44:45] op_sel_hi:[0,1,1]
	v_pk_fma_f32 v[44:45], v[98:99], v[136:137], v[44:45] op_sel_hi:[0,1,1]
	v_add_f32_e32 v3, 1.0, v3
	v_pk_fma_f32 v[44:45], v[100:101], v[60:61], v[44:45] op_sel_hi:[0,1,1]
	v_rcp_f32_e32 v59, v3
	v_mul_f32_e32 v3, 0xbfb8aa3b, v44
	v_exp_f32_e32 v3, v3
	v_cvt_pk_bf16_f32 v50, v50, v51
	v_pk_mul_f32 v[74:75], v[54:55], v[58:59]
	v_cvt_pk_bf16_f32 v58, v42, v43
	v_add_f32_e32 v3, 1.0, v3
	v_rcp_f32_e32 v48, v3
	v_mul_f32_e32 v3, 0xbfb8aa3b, v45
	v_exp_f32_e32 v3, v3
	v_cvt_pk_bf16_f32 v54, v46, v47
	v_cvt_pk_bf16_f32 v46, v74, v75
	v_add_f32_e32 v3, 1.0, v3
	v_rcp_f32_e32 v49, v3
	s_nop 0
	v_pk_mul_f32 v[44:45], v[44:45], v[48:49]
	s_nop 0
	v_cvt_pk_bf16_f32 v42, v44, v45
	v_add_co_u32_e32 v44, vcc, s79, v80
	s_nop 1
	v_addc_co_u32_e32 v45, vcc, 0, v81, vcc
	global_load_dwordx4 v[72:75], v[44:45], off offset:3072
	v_add_co_u32_e32 v44, vcc, s81, v80
	s_waitcnt vmcnt(0)
	v_lshlrev_b32_e32 v206, 16, v72
	v_addc_co_u32_e32 v45, vcc, 0, v81, vcc
	global_load_dwordx4 v[76:79], v[44:45], off offset:2560
	v_pk_fma_f32 v[44:45], v[22:23], v[64:65], v[38:39] op_sel_hi:[0,1,0]
	v_pk_fma_f32 v[44:45], v[26:27], v[68:69], v[44:45] op_sel_hi:[0,1,1]
	v_and_b32_e32 v64, 0xffff0000, v72
	v_lshlrev_b32_e32 v204, 16, v73
	v_lshlrev_b32_e32 v56, 16, v74
	s_waitcnt vmcnt(0)
	v_lshlrev_b32_e32 v207, 16, v76
	v_pk_mov_b32 v[208:209], v[68:69], v[206:207] op_sel:[1,0]
	v_and_b32_e32 v65, 0xffff0000, v76
	v_pk_fma_f32 v[44:45], v[30:31], v[208:209], v[44:45] op_sel_hi:[0,1,1]
	v_pk_fma_f32 v[44:45], v[34:35], v[206:207], v[44:45] op_sel_hi:[0,1,1]
	v_mul_f32_e32 v3, 0xbfb8aa3b, v44
	v_exp_f32_e32 v3, v3
	v_pk_mov_b32 v[210:211], v[114:115], v[64:65] op_sel:[1,0]
	v_lshlrev_b32_e32 v205, 16, v77
	v_and_b32_e32 v69, 0xffff0000, v77
	v_add_f32_e32 v3, 1.0, v3
	v_rcp_f32_e32 v48, v3
	v_mul_f32_e32 v3, 0xbfb8aa3b, v45
	v_exp_f32_e32 v3, v3
	v_and_b32_e32 v68, 0xffff0000, v73
	v_lshlrev_b32_e32 v57, 16, v78
	v_add_f32_e32 v3, 1.0, v3
	v_rcp_f32_e32 v49, v3
	s_nop 0
	v_pk_mul_f32 v[228:229], v[44:45], v[48:49]
	v_pk_fma_f32 v[44:45], v[22:23], v[112:113], v[38:39] op_sel:[1,0,1]
	v_pk_mov_b32 v[112:113], v[126:127], v[56:57] op_sel:[1,0]
	v_pk_fma_f32 v[44:45], v[26:27], v[114:115], v[44:45] op_sel:[1,0,0]
	v_cvt_pk_bf16_f32 v71, v228, v229
	v_pk_fma_f32 v[44:45], v[30:31], v[210:211], v[44:45] op_sel:[1,0,0]
	s_nop 0
	v_pk_fma_f32 v[44:45], v[34:35], v[64:65], v[44:45] op_sel:[1,0,0]
	s_nop 0
	v_mul_f32_e32 v3, 0xbfb8aa3b, v44
	v_exp_f32_e32 v3, v3
	s_nop 0
	v_add_f32_e32 v3, 1.0, v3
	v_rcp_f32_e32 v48, v3
	v_mul_f32_e32 v3, 0xbfb8aa3b, v45
	v_exp_f32_e32 v3, v3
	s_nop 0
	v_add_f32_e32 v3, 1.0, v3
	v_rcp_f32_e32 v49, v3
	s_nop 0
	v_pk_mul_f32 v[230:231], v[44:45], v[48:49]
	v_pk_fma_f32 v[44:45], v[24:25], v[116:117], v[40:41] op_sel_hi:[0,1,0]
	v_pk_fma_f32 v[44:45], v[28:29], v[118:119], v[44:45] op_sel_hi:[0,1,1]
	v_pk_mov_b32 v[116:117], v[118:119], v[204:205] op_sel:[1,0]
	v_cvt_pk_bf16_f32 v67, v230, v231
	v_pk_fma_f32 v[44:45], v[32:33], v[116:117], v[44:45] op_sel_hi:[0,1,1]
	v_pk_fma_f32 v[44:45], v[36:37], v[204:205], v[44:45] op_sel_hi:[0,1,1]
	v_mul_f32_e32 v3, 0xbfb8aa3b, v44
	v_exp_f32_e32 v3, v3
	v_pk_fma_f32 v[116:117], v[24:25], v[116:117], v[40:41] op_sel_hi:[0,1,0]
	v_pk_fma_f32 v[116:117], v[28:29], v[204:205], v[116:117] op_sel_hi:[0,1,1]
	v_add_f32_e32 v3, 1.0, v3
	v_rcp_f32_e32 v48, v3
	v_mul_f32_e32 v3, 0xbfb8aa3b, v45
	v_exp_f32_e32 v3, v3
	s_nop 0
	v_add_f32_e32 v3, 1.0, v3
	v_rcp_f32_e32 v49, v3
	s_nop 0
	v_pk_mul_f32 v[232:233], v[44:45], v[48:49]
	v_pk_fma_f32 v[44:45], v[82:83], v[120:121], v[84:85] op_sel_hi:[0,1,0]
	v_pk_fma_f32 v[44:45], v[86:87], v[122:123], v[44:45] op_sel_hi:[0,1,1]
	v_pk_mov_b32 v[120:121], v[122:123], v[68:69] op_sel:[1,0]
; #define LAS __attribute__((address_space(3)))
; __device__ __forceinline__ unsigned pk2(float lo, float hi) { const f32x2 v = {lo, hi}; return __builtin_bit_cast(unsigned, __builtin_convertvector(v, hwbf16x2)); }
; __device__ __forceinline__ float fsigmoid(float x) { return __builtin_amdgcn_rcpf(1.0f + __expf(-x)); }
; __device__ __forceinline__ void unpack8(const v4u q, float (&d)[8]) { d[0] = bflo(q.x); d[1] = bfhi(q.x); d[2] = bflo(q.y); d[3] = bfhi(q.y); d[4] = bflo(q.z); d[5] = bfhi(q.z); d[6] = bflo(q.w); d[7] = bfhi(q.w); }
; template <bool TR, bool SCALE>
; __device__ __forceinline__ void conv_task(const Params& p, const bf16* proj, size_t trow0, int tl0, int run, int xcol, LAS bf16* dst, int d0, const LAS float* sc) {
;     ...
;     for (int i = 0; i < 8; i += 2) {
;         float r3[8], r4[8], o0[8], o1[8];
;         unpack8(*(const v4u*)(src + (size_t)i * PROJ_LD), r3); unpack8(*(const v4u*)(src + (size_t)(i + 1) * PROJ_LD), r4);
; #pragma unroll
;         for (int j = 0; j < 8; ++j) { const float a0 = bb[j] + w[0][j] * r0[j] + w[1][j] * r1[j] + w[2][j] * r2[j] + w[3][j] * r3[j];
;             const float a1 = bb[j] + w[0][j] * r1[j] + w[1][j] * r2[j] + w[2][j] * r3[j] + w[3][j] * r4[j];
;             o0[j] = a0 * fsigmoid(a0); o1[j] = a1 * fsigmoid(a1); }
;         if constexpr (TR) {
;             float s0 = 1.f, s1 = 1.f; if constexpr (SCALE) { s0 = sc[l0 + i]; s1 = sc[l0 + i + 1]; }
; #pragma unroll
;             for (int j = 0; j < 8; ++j) *(LAS unsigned*)(dst + (d0 + j) * SPT + l0 + i) = pk2(o0[j] * s0, o1[j] * s1);
;         } else {
;             *(LAS v4u*)(dst + (l0 + i) * SPT + d0) = (v4u){pk2(o0[0], o0[1]), pk2(o0[2], o0[3]), pk2(o0[4], o0[5]), pk2(o0[6], o0[7])};
;             *(LAS v4u*)(dst + (l0 + i + 1) * SPT + d0) = (v4u){pk2(o1[0], o1[1]), pk2(o1[2], o1[3]), pk2(o1[4], o1[5]), pk2(o1[6], o1[7])};
;         }
; #pragma unroll
;         for (int j = 0; j < 8; ++j) { r0[j] = r2[j]; r1[j] = r3[j]; r2[j] = r4[j]; }
	v_cvt_pk_bf16_f32 v63, v232, v233
	v_pk_fma_f32 v[44:45], v[88:89], v[120:121], v[44:45] op_sel_hi:[0,1,1]
	v_pk_fma_f32 v[44:45], v[90:91], v[68:69], v[44:45] op_sel_hi:[0,1,1]
	v_mul_f32_e32 v3, 0xbfb8aa3b, v44
	v_exp_f32_e32 v3, v3
	s_nop 0
	v_add_f32_e32 v3, 1.0, v3
	v_rcp_f32_e32 v48, v3
	v_mul_f32_e32 v3, 0xbfb8aa3b, v45
	v_exp_f32_e32 v3, v3
	s_nop 0
	v_add_f32_e32 v3, 1.0, v3
	v_rcp_f32_e32 v49, v3
	s_nop 0
	v_pk_mul_f32 v[72:73], v[44:45], v[48:49]
	v_pk_fma_f32 v[44:45], v[2:3], v[124:125], v[18:19] op_sel_hi:[0,1,0]
	v_pk_fma_f32 v[44:45], v[6:7], v[126:127], v[44:45] op_sel_hi:[0,1,1]
	v_pk_fma_f32 v[44:45], v[10:11], v[112:113], v[44:45] op_sel_hi:[0,1,1]
	v_pk_fma_f32 v[44:45], v[14:15], v[56:57], v[44:45] op_sel_hi:[0,1,1]
	v_mul_f32_e32 v3, 0xbfb8aa3b, v44
	v_exp_f32_e32 v3, v3
	v_cvt_pk_bf16_f32 v59, v72, v73
	v_add_co_u32_e32 v72, vcc, s82, v80
	v_add_f32_e32 v3, 1.0, v3
	v_rcp_f32_e32 v48, v3
	v_mul_f32_e32 v3, 0xbfb8aa3b, v45
	v_exp_f32_e32 v3, v3
	v_addc_co_u32_e32 v73, vcc, 0, v81, vcc
	v_add_f32_e32 v3, 1.0, v3
	v_rcp_f32_e32 v49, v3
	s_nop 0
	v_pk_mul_f32 v[76:77], v[44:45], v[48:49]
	v_and_b32_e32 v45, 0xffff0000, v78
	v_and_b32_e32 v44, 0xffff0000, v74
	v_pk_fma_f32 v[48:49], v[102:103], v[128:129], v[104:105] op_sel_hi:[0,1,0]
	v_pk_fma_f32 v[48:49], v[106:107], v[130:131], v[48:49] op_sel_hi:[0,1,1]
	v_pk_mov_b32 v[114:115], v[130:131], v[44:45] op_sel:[1,0]
	v_cvt_pk_bf16_f32 v55, v76, v77
	v_pk_fma_f32 v[48:49], v[108:109], v[114:115], v[48:49] op_sel_hi:[0,1,1]
	v_pk_fma_f32 v[48:49], v[110:111], v[44:45], v[48:49] op_sel_hi:[0,1,1]
	v_mul_f32_e32 v3, 0xbfb8aa3b, v48
	v_exp_f32_e32 v3, v3
	v_add_co_u32_e32 v76, vcc, s83, v80
	v_add_f32_e32 v3, 1.0, v3
	v_rcp_f32_e32 v52, v3
	v_mul_f32_e32 v3, 0xbfb8aa3b, v49
	v_exp_f32_e32 v3, v3
	v_addc_co_u32_e32 v77, vcc, 0, v81, vcc
	v_add_f32_e32 v3, 1.0, v3
	v_rcp_f32_e32 v53, v3
	s_nop 0
	v_pk_mul_f32 v[122:123], v[48:49], v[52:53]
	v_lshlrev_b32_e32 v53, 16, v79
	v_lshlrev_b32_e32 v52, 16, v75
	v_pk_fma_f32 v[48:49], v[4:5], v[132:133], v[20:21] op_sel_hi:[0,1,0]
	v_pk_fma_f32 v[48:49], v[8:9], v[134:135], v[48:49] op_sel_hi:[0,1,1]
	v_pk_mov_b32 v[118:119], v[134:135], v[52:53] op_sel:[1,0]
	v_cvt_pk_bf16_f32 v51, v122, v123
	v_pk_fma_f32 v[48:49], v[12:13], v[118:119], v[48:49] op_sel_hi:[0,1,1]
	v_pk_fma_f32 v[48:49], v[16:17], v[52:53], v[48:49] op_sel_hi:[0,1,1]
	v_mul_f32_e32 v3, 0xbfb8aa3b, v48
	v_exp_f32_e32 v3, v3
	v_pk_fma_f32 v[122:123], v[22:23], v[208:209], v[38:39] op_sel_hi:[0,1,0]
	v_pk_fma_f32 v[122:123], v[26:27], v[206:207], v[122:123] op_sel_hi:[0,1,1]
	v_add_f32_e32 v3, 1.0, v3
	v_rcp_f32_e32 v124, v3
	v_mul_f32_e32 v3, 0xbfb8aa3b, v49
	v_exp_f32_e32 v3, v3
	s_nop 0
	v_add_f32_e32 v3, 1.0, v3
	v_rcp_f32_e32 v125, v3
	s_nop 0
	v_pk_mul_f32 v[124:125], v[48:49], v[124:125]
	v_and_b32_e32 v49, 0xffff0000, v79
	v_and_b32_e32 v48, 0xffff0000, v75
	v_pk_fma_f32 v[74:75], v[92:93], v[136:137], v[94:95] op_sel_hi:[0,1,0]
	v_pk_fma_f32 v[74:75], v[96:97], v[60:61], v[74:75] op_sel_hi:[0,1,1]
	v_pk_mov_b32 v[60:61], v[60:61], v[48:49] op_sel:[1,0]
	v_cvt_pk_bf16_f32 v47, v124, v125
	v_pk_fma_f32 v[74:75], v[98:99], v[60:61], v[74:75] op_sel_hi:[0,1,1]
	v_pk_fma_f32 v[74:75], v[100:101], v[48:49], v[74:75] op_sel_hi:[0,1,1]
	v_mul_f32_e32 v3, 0xbfb8aa3b, v74
	v_exp_f32_e32 v3, v3
	s_nop 0
	v_add_f32_e32 v3, 1.0, v3
	v_rcp_f32_e32 v78, v3
	v_mul_f32_e32 v3, 0xbfb8aa3b, v75
	v_exp_f32_e32 v3, v3
	s_nop 0
	v_add_f32_e32 v3, 1.0, v3
	v_rcp_f32_e32 v79, v3
	s_nop 0
	v_pk_mul_f32 v[74:75], v[74:75], v[78:79]
	s_nop 0
	v_cvt_pk_bf16_f32 v43, v74, v75
	global_load_dwordx4 v[72:75], v[72:73], off offset:2048
	s_nop 0
	global_load_dwordx4 v[76:79], v[76:77], off offset:1536
	s_waitcnt vmcnt(1)
	v_lshlrev_b32_e32 v134, 16, v72
	v_and_b32_e32 v132, 0xffff0000, v72
	s_waitcnt vmcnt(0)
	v_lshlrev_b32_e32 v135, 16, v76
	v_pk_mov_b32 v[206:207], v[206:207], v[134:135] op_sel:[1,0]
	v_and_b32_e32 v133, 0xffff0000, v76
	v_pk_fma_f32 v[122:123], v[30:31], v[206:207], v[122:123] op_sel_hi:[0,1,1]
	v_pk_fma_f32 v[122:123], v[34:35], v[134:135], v[122:123] op_sel_hi:[0,1,1]
	v_mul_f32_e32 v3, 0xbfb8aa3b, v122
	v_exp_f32_e32 v3, v3
	v_pk_mov_b32 v[208:209], v[64:65], v[132:133] op_sel:[1,0]
	v_lshlrev_b32_e32 v131, 16, v77
	v_lshlrev_b32_e32 v130, 16, v73
	v_add_f32_e32 v3, 1.0, v3
	v_rcp_f32_e32 v124, v3
	v_mul_f32_e32 v3, 0xbfb8aa3b, v123
	v_exp_f32_e32 v3, v3
	v_pk_mov_b32 v[136:137], v[204:205], v[130:131] op_sel:[1,0]
	v_and_b32_e32 v129, 0xffff0000, v77
	v_pk_fma_f32 v[116:117], v[32:33], v[136:137], v[116:117] op_sel_hi:[0,1,1]
	v_add_f32_e32 v3, 1.0, v3
	v_rcp_f32_e32 v125, v3
	v_pk_fma_f32 v[116:117], v[36:37], v[130:131], v[116:117] op_sel_hi:[0,1,1]
	v_and_b32_e32 v128, 0xffff0000, v73
	v_pk_fma_f32 v[72:73], v[82:83], v[120:121], v[84:85] op_sel_hi:[0,1,0]
	v_pk_mul_f32 v[228:229], v[122:123], v[124:125]
	v_pk_fma_f32 v[122:123], v[22:23], v[210:211], v[38:39] op_sel:[1,0,1]
	v_pk_fma_f32 v[72:73], v[86:87], v[68:69], v[72:73] op_sel_hi:[0,1,1]
	v_pk_fma_f32 v[122:123], v[26:27], v[64:65], v[122:123] op_sel:[1,0,0]
	v_pk_mov_b32 v[204:205], v[68:69], v[128:129] op_sel:[1,0]
	v_pk_fma_f32 v[64:65], v[30:31], v[208:209], v[122:123] op_sel:[1,0,0]
	v_pk_fma_f32 v[68:69], v[88:89], v[204:205], v[72:73] op_sel_hi:[0,1,1]
	v_pk_fma_f32 v[64:65], v[34:35], v[132:133], v[64:65] op_sel:[1,0,0]
	v_pk_fma_f32 v[68:69], v[90:91], v[128:129], v[68:69] op_sel_hi:[0,1,1]
	v_mul_f32_e32 v3, 0xbfb8aa3b, v64
	v_exp_f32_e32 v3, v3
	v_lshlrev_b32_e32 v125, 16, v78
	v_lshlrev_b32_e32 v124, 16, v74
	v_pk_mov_b32 v[126:127], v[56:57], v[124:125] op_sel:[1,0]
	v_add_f32_e32 v3, 1.0, v3
; #define LAS __attribute__((address_space(3)))
; __device__ __forceinline__ unsigned pk2(float lo, float hi) { const f32x2 v = {lo, hi}; return __builtin_bit_cast(unsigned, __builtin_convertvector(v, hwbf16x2)); }
; __device__ __forceinline__ float fsigmoid(float x) { return __builtin_amdgcn_rcpf(1.0f + __expf(-x)); }
; __device__ __forceinline__ void unpack8(const v4u q, float (&d)[8]) { d[0] = bflo(q.x); d[1] = bfhi(q.x); d[2] = bflo(q.y); d[3] = bfhi(q.y); d[4] = bflo(q.z); d[5] = bfhi(q.z); d[6] = bflo(q.w); d[7] = bfhi(q.w); }
; template <bool TR, bool SCALE>
; __device__ __forceinline__ void conv_task(const Params& p, const bf16* proj, size_t trow0, int tl0, int run, int xcol, LAS bf16* dst, int d0, const LAS float* sc) {
;     ...
;     for (int i = 0; i < 8; i += 2) {
;         float r3[8], r4[8], o0[8], o1[8];
;         unpack8(*(const v4u*)(src + (size_t)i * PROJ_LD), r3); unpack8(*(const v4u*)(src + (size_t)(i + 1) * PROJ_LD), r4);
; #pragma unroll
;         for (int j = 0; j < 8; ++j) { const float a0 = bb[j] + w[0][j] * r0[j] + w[1][j] * r1[j] + w[2][j] * r2[j] + w[3][j] * r3[j];
;             const float a1 = bb[j] + w[0][j] * r1[j] + w[1][j] * r2[j] + w[2][j] * r3[j] + w[3][j] * r4[j];
;             o0[j] = a0 * fsigmoid(a0); o1[j] = a1 * fsigmoid(a1); }
;         if constexpr (TR) {
;             float s0 = 1.f, s1 = 1.f; if constexpr (SCALE) { s0 = sc[l0 + i]; s1 = sc[l0 + i + 1]; }
; #pragma unroll
;             for (int j = 0; j < 8; ++j) *(LAS unsigned*)(dst + (d0 + j) * SPT + l0 + i) = pk2(o0[j] * s0, o1[j] * s1);
;         } else {
;             *(LAS v4u*)(dst + (l0 + i) * SPT + d0) = (v4u){pk2(o0[0], o0[1]), pk2(o0[2], o0[3]), pk2(o0[4], o0[5]), pk2(o0[6], o0[7])};
;             *(LAS v4u*)(dst + (l0 + i + 1) * SPT + d0) = (v4u){pk2(o1[0], o1[1]), pk2(o1[2], o1[3]), pk2(o1[4], o1[5]), pk2(o1[6], o1[7])};
;         }
; #pragma unroll
;         for (int j = 0; j < 8; ++j) { r0[j] = r2[j]; r1[j] = r3[j]; r2[j] = r4[j]; }
	v_rcp_f32_e32 v122, v3
	v_mul_f32_e32 v3, 0xbfb8aa3b, v65
	v_exp_f32_e32 v3, v3
	v_and_b32_e32 v121, 0xffff0000, v78
	v_and_b32_e32 v120, 0xffff0000, v74
	v_pk_fma_f32 v[206:207], v[22:23], v[206:207], v[38:39] op_sel_hi:[0,1,0]
	v_add_f32_e32 v3, 1.0, v3
	v_rcp_f32_e32 v123, v3
	v_mul_f32_e32 v3, 0xbfb8aa3b, v116
	v_exp_f32_e32 v3, v3
	v_pk_fma_f32 v[206:207], v[26:27], v[134:135], v[206:207] op_sel_hi:[0,1,1]
	v_pk_mul_f32 v[64:65], v[64:65], v[122:123]
	v_pk_fma_f32 v[22:23], v[22:23], v[208:209], v[38:39] op_sel:[1,0,1]
	v_add_f32_e32 v3, 1.0, v3
	v_rcp_f32_e32 v122, v3
	v_mul_f32_e32 v3, 0xbfb8aa3b, v117
	v_exp_f32_e32 v3, v3
	v_pk_fma_f32 v[22:23], v[26:27], v[132:133], v[22:23] op_sel:[1,0,0]
	v_pk_fma_f32 v[24:25], v[24:25], v[136:137], v[40:41] op_sel_hi:[0,1,0]
	v_pk_fma_f32 v[24:25], v[28:29], v[130:131], v[24:25] op_sel_hi:[0,1,1]
	v_add_f32_e32 v3, 1.0, v3
	v_rcp_f32_e32 v123, v3
	v_mul_f32_e32 v3, 0xbfb8aa3b, v68
	v_exp_f32_e32 v3, v3
	v_pk_mul_f32 v[210:211], v[116:117], v[122:123]
	v_pk_mov_b32 v[122:123], v[44:45], v[120:121] op_sel:[1,0]
	v_add_f32_e32 v3, 1.0, v3
	v_rcp_f32_e32 v72, v3
	v_mul_f32_e32 v3, 0xbfb8aa3b, v69
	v_exp_f32_e32 v3, v3
	v_lshlrev_b32_e32 v117, 16, v79
	v_lshlrev_b32_e32 v116, 16, v75
	v_add_f32_e32 v3, 1.0, v3
	v_rcp_f32_e32 v73, v3
	s_nop 0
	v_pk_mul_f32 v[76:77], v[68:69], v[72:73]
	v_pk_fma_f32 v[68:69], v[2:3], v[112:113], v[18:19] op_sel_hi:[0,1,0]
	v_pk_fma_f32 v[68:69], v[6:7], v[56:57], v[68:69] op_sel_hi:[0,1,1]
	v_pk_fma_f32 v[56:57], v[10:11], v[126:127], v[68:69] op_sel_hi:[0,1,1]
	v_pk_fma_f32 v[56:57], v[14:15], v[124:125], v[56:57] op_sel_hi:[0,1,1]
	v_mul_f32_e32 v3, 0xbfb8aa3b, v56
	v_exp_f32_e32 v3, v3
	v_and_b32_e32 v113, 0xffff0000, v79
	v_and_b32_e32 v112, 0xffff0000, v75
	v_cvt_pk_bf16_f32 v72, v228, v229
	v_add_f32_e32 v3, 1.0, v3
	v_rcp_f32_e32 v68, v3
	v_mul_f32_e32 v3, 0xbfb8aa3b, v57
	v_exp_f32_e32 v3, v3
	s_nop 0
	v_add_f32_e32 v3, 1.0, v3
	v_rcp_f32_e32 v69, v3
	s_nop 0
	v_pk_mul_f32 v[56:57], v[56:57], v[68:69]
	v_pk_fma_f32 v[68:69], v[102:103], v[114:115], v[104:105] op_sel_hi:[0,1,0]
	v_pk_fma_f32 v[68:69], v[106:107], v[44:45], v[68:69] op_sel_hi:[0,1,1]
	v_pk_fma_f32 v[44:45], v[108:109], v[122:123], v[68:69] op_sel_hi:[0,1,1]
	v_pk_fma_f32 v[44:45], v[110:111], v[120:121], v[44:45] op_sel_hi:[0,1,1]
	v_mul_f32_e32 v3, 0xbfb8aa3b, v44
	v_exp_f32_e32 v3, v3
	v_pk_mov_b32 v[114:115], v[48:49], v[112:113] op_sel:[1,0]
	v_cvt_pk_bf16_f32 v56, v56, v57
	v_add_f32_e32 v3, 1.0, v3
	v_rcp_f32_e32 v68, v3
	v_mul_f32_e32 v3, 0xbfb8aa3b, v45
	v_exp_f32_e32 v3, v3
	s_nop 0
	v_add_f32_e32 v3, 1.0, v3
	v_rcp_f32_e32 v69, v3
	s_nop 0
	v_pk_mul_f32 v[44:45], v[44:45], v[68:69]
	v_pk_fma_f32 v[68:69], v[4:5], v[118:119], v[20:21] op_sel_hi:[0,1,0]
	v_pk_fma_f32 v[68:69], v[8:9], v[52:53], v[68:69] op_sel_hi:[0,1,1]
	v_pk_mov_b32 v[118:119], v[52:53], v[116:117] op_sel:[1,0]
	s_nop 0
	v_pk_fma_f32 v[52:53], v[12:13], v[118:119], v[68:69] op_sel_hi:[0,1,1]
	v_pk_fma_f32 v[52:53], v[16:17], v[116:117], v[52:53] op_sel_hi:[0,1,1]
	v_mul_f32_e32 v3, 0xbfb8aa3b, v52
	v_exp_f32_e32 v3, v3
	s_nop 0
	v_add_f32_e32 v3, 1.0, v3
	v_rcp_f32_e32 v68, v3
	v_mul_f32_e32 v3, 0xbfb8aa3b, v53
	v_exp_f32_e32 v3, v3
	s_nop 0
	v_add_f32_e32 v3, 1.0, v3
	v_rcp_f32_e32 v69, v3
	s_nop 0
	v_pk_mul_f32 v[230:231], v[52:53], v[68:69]
	v_pk_fma_f32 v[52:53], v[92:93], v[60:61], v[94:95] op_sel_hi:[0,1,0]
	v_pk_fma_f32 v[52:53], v[96:97], v[48:49], v[52:53] op_sel_hi:[0,1,1]
	v_pk_fma_f32 v[48:49], v[98:99], v[114:115], v[52:53] op_sel_hi:[0,1,1]
	v_pk_fma_f32 v[48:49], v[100:101], v[112:113], v[48:49] op_sel_hi:[0,1,1]
	v_mul_f32_e32 v3, 0xbfb8aa3b, v48
	v_exp_f32_e32 v3, v3
	v_cvt_pk_bf16_f32 v60, v76, v77
	v_cvt_pk_bf16_f32 v68, v64, v65
	v_cvt_pk_bf16_f32 v64, v210, v211
	v_add_f32_e32 v3, 1.0, v3
	v_rcp_f32_e32 v52, v3
	v_mul_f32_e32 v3, 0xbfb8aa3b, v49
	v_exp_f32_e32 v3, v3
	s_nop 0
	v_add_f32_e32 v3, 1.0, v3
	v_rcp_f32_e32 v53, v3
	s_nop 0
	v_pk_mul_f32 v[74:75], v[48:49], v[52:53]
	v_cvt_pk_bf16_f32 v52, v44, v45
	v_cvt_pk_bf16_f32 v44, v74, v75
	v_add_co_u32_e32 v74, vcc, s92, v80
	v_cvt_pk_bf16_f32 v48, v230, v231
	s_nop 0
	v_addc_co_u32_e32 v75, vcc, 0, v81, vcc
	v_add_co_u32_e32 v78, vcc, s93, v80
	global_load_dwordx4 v[74:77], v[74:75], off offset:1024
	s_nop 0
	v_addc_co_u32_e32 v79, vcc, 0, v81, vcc
	global_load_dwordx4 v[78:81], v[78:79], off offset:512
	s_waitcnt vmcnt(1)
	v_lshlrev_b32_e32 v210, 16, v74
	s_waitcnt vmcnt(0)
; #define LAS __attribute__((address_space(3)))
; __device__ __forceinline__ unsigned pk2(float lo, float hi) { const f32x2 v = {lo, hi}; return __builtin_bit_cast(unsigned, __builtin_convertvector(v, hwbf16x2)); }
; __device__ __forceinline__ float fsigmoid(float x) { return __builtin_amdgcn_rcpf(1.0f + __expf(-x)); }
; __device__ __forceinline__ void unpack8(const v4u q, float (&d)[8]) { d[0] = bflo(q.x); d[1] = bfhi(q.x); d[2] = bflo(q.y); d[3] = bfhi(q.y); d[4] = bflo(q.z); d[5] = bfhi(q.z); d[6] = bflo(q.w); d[7] = bfhi(q.w); }
; template <bool TR, bool SCALE>
; __device__ __forceinline__ void conv_task(const Params& p, const bf16* proj, size_t trow0, int tl0, int run, int xcol, LAS bf16* dst, int d0, const LAS float* sc) {
;     ...
;     for (int i = 0; i < 8; i += 2) {
;         float r3[8], r4[8], o0[8], o1[8];
;         unpack8(*(const v4u*)(src + (size_t)i * PROJ_LD), r3); unpack8(*(const v4u*)(src + (size_t)(i + 1) * PROJ_LD), r4);
; #pragma unroll
;         for (int j = 0; j < 8; ++j) { const float a0 = bb[j] + w[0][j] * r0[j] + w[1][j] * r1[j] + w[2][j] * r2[j] + w[3][j] * r3[j];
;             const float a1 = bb[j] + w[0][j] * r1[j] + w[1][j] * r2[j] + w[2][j] * r3[j] + w[3][j] * r4[j];
;             o0[j] = a0 * fsigmoid(a0); o1[j] = a1 * fsigmoid(a1); }
;         if constexpr (TR) {
;             float s0 = 1.f, s1 = 1.f; if constexpr (SCALE) { s0 = sc[l0 + i]; s1 = sc[l0 + i + 1]; }
; #pragma unroll
;             for (int j = 0; j < 8; ++j) *(LAS unsigned*)(dst + (d0 + j) * SPT + l0 + i) = pk2(o0[j] * s0, o1[j] * s1);
;         } else {
;             *(LAS v4u*)(dst + (l0 + i) * SPT + d0) = (v4u){pk2(o0[0], o0[1]), pk2(o0[2], o0[3]), pk2(o0[4], o0[5]), pk2(o0[6], o0[7])};
;             *(LAS v4u*)(dst + (l0 + i + 1) * SPT + d0) = (v4u){pk2(o1[0], o1[1]), pk2(o1[2], o1[3]), pk2(o1[4], o1[5]), pk2(o1[6], o1[7])};
;         }
; #pragma unroll
;         for (int j = 0; j < 8; ++j) { r0[j] = r2[j]; r1[j] = r3[j]; r2[j] = r4[j]; }
;     }
	v_lshlrev_b32_e32 v211, 16, v78
	v_pk_mov_b32 v[134:135], v[134:135], v[210:211] op_sel:[1,0]
	s_nop 0
	v_pk_fma_f32 v[134:135], v[30:31], v[134:135], v[206:207] op_sel_hi:[0,1,1]
	v_pk_fma_f32 v[134:135], v[34:35], v[210:211], v[134:135] op_sel_hi:[0,1,1]
	v_mul_f32_e32 v3, 0xbfb8aa3b, v134
	v_exp_f32_e32 v3, v3
	s_nop 0
	v_add_f32_e32 v3, 1.0, v3
	v_rcp_f32_e32 v206, v3
	v_mul_f32_e32 v3, 0xbfb8aa3b, v135
	v_exp_f32_e32 v3, v3
	s_nop 0
	v_add_f32_e32 v3, 1.0, v3
	v_rcp_f32_e32 v207, v3
	s_nop 0
	v_pk_mul_f32 v[134:135], v[134:135], v[206:207]
	v_and_b32_e32 v207, 0xffff0000, v78
	v_and_b32_e32 v206, 0xffff0000, v74
	v_pk_mov_b32 v[26:27], v[132:133], v[206:207] op_sel:[1,0]
	v_cvt_pk_bf16_f32 v73, v134, v135
	v_pk_fma_f32 v[22:23], v[30:31], v[26:27], v[22:23] op_sel:[1,0,0]
	ds_write_b128 v1, v[70:73]
	v_pk_fma_f32 v[22:23], v[34:35], v[206:207], v[22:23] op_sel:[1,0,0]
	s_nop 0
	v_mul_f32_e32 v3, 0xbfb8aa3b, v22
	v_exp_f32_e32 v3, v3
	s_nop 0
	v_add_f32_e32 v3, 1.0, v3
	v_rcp_f32_e32 v26, v3
	v_mul_f32_e32 v3, 0xbfb8aa3b, v23
	v_exp_f32_e32 v3, v3
	s_nop 0
	v_add_f32_e32 v3, 1.0, v3
	v_rcp_f32_e32 v27, v3
	s_nop 0
	v_pk_mul_f32 v[22:23], v[22:23], v[26:27]
	v_lshlrev_b32_e32 v26, 16, v75
	v_lshlrev_b32_e32 v27, 16, v79
	v_pk_mov_b32 v[28:29], v[130:131], v[26:27] op_sel:[1,0]
	v_cvt_pk_bf16_f32 v69, v22, v23
	v_pk_fma_f32 v[24:25], v[32:33], v[28:29], v[24:25] op_sel_hi:[0,1,1]
	v_pk_fma_f32 v[24:25], v[36:37], v[26:27], v[24:25] op_sel_hi:[0,1,1]
	v_mul_f32_e32 v3, 0xbfb8aa3b, v24
	v_exp_f32_e32 v3, v3
	v_pk_fma_f32 v[28:29], v[82:83], v[204:205], v[84:85] op_sel_hi:[0,1,0]
	v_pk_fma_f32 v[28:29], v[86:87], v[128:129], v[28:29] op_sel_hi:[0,1,1]
	ds_write_b128 v1, v[66:69] offset:272
	v_add_f32_e32 v3, 1.0, v3
	v_rcp_f32_e32 v26, v3
	v_mul_f32_e32 v3, 0xbfb8aa3b, v25
	v_exp_f32_e32 v3, v3
	s_nop 0
	v_add_f32_e32 v3, 1.0, v3
	v_rcp_f32_e32 v27, v3
	s_nop 0
	v_pk_mul_f32 v[24:25], v[24:25], v[26:27]
	v_and_b32_e32 v27, 0xffff0000, v79
	v_and_b32_e32 v26, 0xffff0000, v75
	v_pk_mov_b32 v[30:31], v[128:129], v[26:27] op_sel:[1,0]
	v_cvt_pk_bf16_f32 v65, v24, v25
	v_pk_fma_f32 v[28:29], v[88:89], v[30:31], v[28:29] op_sel_hi:[0,1,1]
	v_pk_fma_f32 v[26:27], v[90:91], v[26:27], v[28:29] op_sel_hi:[0,1,1]
	v_mul_f32_e32 v3, 0xbfb8aa3b, v26
	v_exp_f32_e32 v3, v3
	ds_write_b128 v1, v[62:65] offset:544
	v_add_f32_e32 v3, 1.0, v3
	v_rcp_f32_e32 v28, v3
	v_mul_f32_e32 v3, 0xbfb8aa3b, v27
	v_exp_f32_e32 v3, v3
	s_nop 0
	v_add_f32_e32 v3, 1.0, v3
	v_rcp_f32_e32 v29, v3
	v_pk_fma_f32 v[2:3], v[2:3], v[126:127], v[18:19] op_sel_hi:[0,1,0]
	v_pk_fma_f32 v[2:3], v[6:7], v[124:125], v[2:3] op_sel_hi:[0,1,1]
	v_pk_mul_f32 v[26:27], v[26:27], v[28:29]
	v_lshlrev_b32_e32 v28, 16, v76
	v_lshlrev_b32_e32 v29, 16, v80
	v_pk_mov_b32 v[6:7], v[124:125], v[28:29] op_sel:[1,0]
	v_cvt_pk_bf16_f32 v61, v26, v27
	v_pk_fma_f32 v[2:3], v[10:11], v[6:7], v[2:3] op_sel_hi:[0,1,1]
	v_pk_fma_f32 v[2:3], v[14:15], v[28:29], v[2:3] op_sel_hi:[0,1,1]
	v_mul_f32_e32 v5, 0xbfb8aa3b, v2
	v_exp_f32_e32 v5, v5
	v_pk_fma_f32 v[10:11], v[102:103], v[122:123], v[104:105] op_sel_hi:[0,1,0]
	v_pk_fma_f32 v[10:11], v[106:107], v[120:121], v[10:11] op_sel_hi:[0,1,1]
	ds_write_b128 v1, v[58:61] offset:816
	v_add_f32_e32 v5, 1.0, v5
	v_rcp_f32_e32 v6, v5
	v_mul_f32_e32 v5, 0xbfb8aa3b, v3
	v_exp_f32_e32 v5, v5
	s_nop 0
	v_add_f32_e32 v5, 1.0, v5
	v_rcp_f32_e32 v7, v5
	s_nop 0
	v_pk_mul_f32 v[2:3], v[2:3], v[6:7]
	v_and_b32_e32 v7, 0xffff0000, v80
	v_and_b32_e32 v6, 0xffff0000, v76
	v_pk_mov_b32 v[14:15], v[120:121], v[6:7] op_sel:[1,0]
	v_cvt_pk_bf16_f32 v57, v2, v3
	v_pk_fma_f32 v[10:11], v[108:109], v[14:15], v[10:11] op_sel_hi:[0,1,1]
	v_pk_fma_f32 v[6:7], v[110:111], v[6:7], v[10:11] op_sel_hi:[0,1,1]
	v_mul_f32_e32 v5, 0xbfb8aa3b, v6
	v_exp_f32_e32 v5, v5
	ds_write_b128 v1, v[54:57] offset:1088
	v_add_f32_e32 v5, 1.0, v5
	v_rcp_f32_e32 v10, v5
	v_mul_f32_e32 v5, 0xbfb8aa3b, v7
	v_exp_f32_e32 v5, v5
	s_nop 0
	v_add_f32_e32 v5, 1.0, v5
	v_rcp_f32_e32 v11, v5
	v_pk_fma_f32 v[4:5], v[4:5], v[118:119], v[20:21] op_sel_hi:[0,1,0]
	v_pk_fma_f32 v[4:5], v[8:9], v[116:117], v[4:5] op_sel_hi:[0,1,1]
	v_pk_mul_f32 v[6:7], v[6:7], v[10:11]
	v_lshlrev_b32_e32 v10, 16, v77
	v_lshlrev_b32_e32 v11, 16, v81
	v_pk_mov_b32 v[8:9], v[116:117], v[10:11] op_sel:[1,0]
	v_cvt_pk_bf16_f32 v53, v6, v7
	v_pk_fma_f32 v[4:5], v[12:13], v[8:9], v[4:5] op_sel_hi:[0,1,1]
	v_pk_fma_f32 v[4:5], v[16:17], v[10:11], v[4:5] op_sel_hi:[0,1,1]
	v_mul_f32_e32 v8, 0xbfb8aa3b, v4
	v_mul_f32_e32 v9, 0xbfb8aa3b, v5
	v_exp_f32_e32 v8, v8
	v_exp_f32_e32 v9, v9
	v_pk_fma_f32 v[10:11], v[92:93], v[114:115], v[94:95] op_sel_hi:[0,1,0]
	v_pk_fma_f32 v[10:11], v[96:97], v[112:113], v[10:11] op_sel_hi:[0,1,1]
	v_add_f32_e32 v8, 1.0, v8
	v_add_f32_e32 v9, 1.0, v9
	v_rcp_f32_e32 v8, v8
	v_rcp_f32_e32 v9, v9
	ds_write_b128 v1, v[50:53] offset:1360
	v_pk_mul_f32 v[4:5], v[4:5], v[8:9]
	v_and_b32_e32 v9, 0xffff0000, v81
	v_and_b32_e32 v8, 0xffff0000, v77
	v_pk_mov_b32 v[12:13], v[112:113], v[8:9] op_sel:[1,0]
	v_cvt_pk_bf16_f32 v49, v4, v5
	v_pk_fma_f32 v[10:11], v[98:99], v[12:13], v[10:11] op_sel_hi:[0,1,1]
	v_pk_fma_f32 v[8:9], v[100:101], v[8:9], v[10:11] op_sel_hi:[0,1,1]
	v_mul_f32_e32 v10, 0xbfb8aa3b, v8
	v_mul_f32_e32 v11, 0xbfb8aa3b, v9
	v_exp_f32_e32 v10, v10
	v_exp_f32_e32 v11, v11
	ds_write_b128 v1, v[46:49] offset:1632
	v_mov_b32_e32 v5, v139
	v_add_f32_e32 v10, 1.0, v10
	v_add_f32_e32 v11, 1.0, v11
	v_rcp_f32_e32 v10, v10
	v_rcp_f32_e32 v11, v11
	s_nop 0
	v_pk_mul_f32 v[8:9], v[8:9], v[10:11]
	s_nop 0
	v_cvt_pk_bf16_f32 v45, v8, v9
	ds_write_b128 v1, v[42:45] offset:1904
	v_mov_b32_e32 v1, v0
	s_waitcnt lgkmcnt(0)
	s_barrier
; #define LAS __attribute__((address_space(3)))
; #define MFMA32(a, b, c) __builtin_amdgcn_mfma_f32_32x32x16_bf16(a, b, c, 0, 0, 0)
; __device__ __forceinline__ void ssd_out_pass(const Params& p, const bf16* proj, const bf16* sinp  , const LAS bf16* Cs, const LAS bf16* CB, const LAS bf16* XT, ...
;     ...
; #pragma unroll
;     for (int pt = 0; pt < 2; ++pt) {
;         bf16x8 af[8];
; #pragma unroll
;         for (int ks = 0; ks < 8; ++ks) af[ks] = *(const bf16x8*)(sinp + (pt * 32 + r) * 128 + ks * 16 + 8 * hf);
; #pragma unroll
;         for (int j = 0; j < 2; ++j) { const int lt = j == 0 ? (lsel ? 1 : 0) : (lsel ? 2 : 3);
; #pragma unroll
;             for (int ks = 0; ks < 8; ++ks) { const bf16x8 bq = *(const LAS bf16x8*)(Cs + (lt * 32 + r) * SPT + ks * 16 + 8 * hf); acc[pt][j] = MFMA32(af[ks], bq, acc[pt][j]); } }
;     }
; #pragma unroll
;     for (int j = 0; j < 2; ++j) { const int lt = j == 0 ? (lsel ? 1 : 0) : (lsel ? 2 : 3); const float el = __expf(csh[lt * 32 + r]);
; #pragma unroll
;         for (int pt = 0; pt < 2; ++pt) acc[pt][j] = acc[pt][j] * el; }
	s_nop 0
	v_readfirstlane_b32 s0, v1
	s_ashr_i32 s1, s0, 7
	s_add_i32 s10, s1, s8
	s_bfe_u32 s11, s0, 0x10006
	s_ashr_i32 s6, s10, 31
	s_add_u32 s4, s4, s10
	s_addc_u32 s5, s5, s6
	s_lshl_b64 s[4:5], s[4:5], 14
	s_add_u32 s6, s3, s4
	s_addc_u32 s7, s35, s5
	s_and_b32 s5, s0, 0xffffff80
	s_addk_i32 s5, 0x200
	s_ashr_i32 s4, s1, 31
	s_add_u32 s12, s1, s16
	s_addc_u32 s13, s4, 0
	v_bfe_u32 v209, v1, 5, 1
	s_lshl_b64 s[12:13], s[12:13], 2
	v_and_b32_e32 v205, 31, v1
	s_add_u32 s12, s44, s12
	v_lshlrev_b32_e32 v138, 4, v209
	s_addc_u32 s13, s45, s13
	v_lshl_add_u64 v[2:3], s[6:7], 0, v[138:139]
	s_xor_b32 s4, s11, 3
	v_lshlrev_b32_e32 v4, 8, v205
	v_lshl_add_u64 v[50:51], v[2:3], 0, v[4:5]
	s_lshl_b32 s9, s11, 5
	s_lshl_b32 s6, s4, 5
	global_load_dword v206, v139, s[12:13] offset:16
	v_add_u32_e32 v1, 0, v138
	global_load_dwordx4 v[94:97], v[50:51], off
	global_load_dwordx4 v[90:93], v[50:51], off offset:32
	global_load_dwordx4 v[86:89], v[50:51], off offset:64
	global_load_dwordx4 v[82:85], v[50:51], off offset:96
	global_load_dwordx4 v[78:81], v[50:51], off offset:128
	global_load_dwordx4 v[74:77], v[50:51], off offset:160
	global_load_dwordx4 v[70:73], v[50:51], off offset:192
	global_load_dwordx4 v[66:69], v[50:51], off offset:224
	v_or_b32_e32 v210, s9, v205
	v_or_b32_e32 v208, s6, v205
	v_add_co_u32_e32 v50, vcc, s94, v50
	v_mad_u32_u24 v46, v210, s80, v1
	v_mad_u32_u24 v1, v208, s80, v1
	v_addc_co_u32_e32 v51, vcc, 0, v51, vcc
	ds_read_b128 v[18:21], v46
	ds_read_b128 v[22:25], v46 offset:32
	ds_read_b128 v[26:29], v46 offset:64
	ds_read_b128 v[30:33], v46 offset:96
	ds_read_b128 v[34:37], v46 offset:128
	ds_read_b128 v[38:41], v46 offset:160
	ds_read_b128 v[42:45], v46 offset:192
	ds_read_b128 v[46:49], v46 offset:224
	ds_read_b128 v[126:129], v1
	ds_read_b128 v[122:125], v1 offset:32
	ds_read_b128 v[118:121], v1 offset:64
	ds_read_b128 v[114:117], v1 offset:96
	ds_read_b128 v[110:113], v1 offset:128
	ds_read_b128 v[106:109], v1 offset:160
	ds_read_b128 v[102:105], v1 offset:192
	ds_read_b128 v[98:101], v1 offset:224
	global_load_dwordx4 v[230:233], v[50:51], off
	global_load_dwordx4 v[234:237], v[50:51], off offset:32
	global_load_dwordx4 v[238:241], v[50:51], off offset:64
	global_load_dwordx4 v[242:245], v[50:51], off offset:96
	global_load_dwordx4 v[246:249], v[50:51], off offset:128
	global_load_dwordx4 v[250:253], v[50:51], off offset:160
	global_load_dwordx4 v[134:137], v[50:51], off offset:192
	global_load_dwordx4 v[130:133], v[50:51], off offset:224
	s_waitcnt vmcnt(15) lgkmcnt(14)
	v_mfma_f32_32x32x16_bf16 v[2:17], v[94:97], v[18:21], 0
	s_add_i32 s7, 0, 0x23000
	v_lshl_add_u32 v1, v205, 2, s7
	s_lshl_b32 s12, s11, 7
	s_lshl_b32 s7, s5, 2
	s_or_b32 s5, s7, s12
	s_lshl_b32 s0, s0, 2
	s_mulk_i32 s1, 0x4400
	s_waitcnt vmcnt(7)
	v_mfma_f32_32x32x16_bf16 v[50:65], v[230:233], v[18:21], 0
	v_add_u32_e32 v18, s5, v1
	ds_read_b32 v229, v18
	s_lshl_b32 s5, s4, 7
	s_or_b32 s5, s7, s5
	s_and_b32 s0, s0, 0xfffffe00
	v_lshlrev_b32_e32 v204, 3, v209
	s_waitcnt lgkmcnt(0)
	v_mul_f32_e32 v18, 0x3fb8aa3b, v229
	v_mfma_f32_32x32x16_bf16 v[2:17], v[90:93], v[22:25], v[2:17]
	v_mul_u32_u24_e32 v254, 0x110, v210
	v_lshl_or_b32 v227, v209, 5, s0
	v_mul_u32_u24_e32 v228, 0x110, v208
	v_mov_b32_e32 v207, v206
	s_waitcnt vmcnt(6)
	v_mfma_f32_32x32x16_bf16 v[50:65], v[234:237], v[22:25], v[50:65]
	v_mfma_f32_32x32x16_bf16 v[2:17], v[86:89], v[26:29], v[2:17]
	s_waitcnt vmcnt(5)
	v_mfma_f32_32x32x16_bf16 v[50:65], v[238:241], v[26:29], v[50:65]
	v_mfma_f32_32x32x16_bf16 v[2:17], v[82:85], v[30:33], v[2:17]
	s_waitcnt vmcnt(4)
	v_mfma_f32_32x32x16_bf16 v[50:65], v[242:245], v[30:33], v[50:65]
	v_mfma_f32_32x32x16_bf16 v[2:17], v[78:81], v[34:37], v[2:17]
	s_waitcnt vmcnt(3)
	v_mfma_f32_32x32x16_bf16 v[50:65], v[246:249], v[34:37], v[50:65]
	v_mfma_f32_32x32x16_bf16 v[2:17], v[74:77], v[38:41], v[2:17]
	s_waitcnt vmcnt(2)
	v_mfma_f32_32x32x16_bf16 v[50:65], v[250:253], v[38:41], v[50:65]
	v_mfma_f32_32x32x16_bf16 v[2:17], v[70:73], v[42:45], v[2:17]
	s_waitcnt vmcnt(1)
	v_mfma_f32_32x32x16_bf16 v[50:65], v[134:137], v[42:45], v[50:65]
	v_mfma_f32_32x32x16_bf16 v[2:17], v[66:69], v[46:49], v[2:17]
	s_waitcnt vmcnt(0)
	v_mfma_f32_32x32x16_bf16 v[50:65], v[130:133], v[46:49], v[50:65]
	v_mfma_f32_32x32x16_bf16 v[34:49], v[230:233], v[126:129], 0
	v_exp_f32_e32 v230, v18
	s_nop 7
	v_pk_mul_f32 v[18:19], v[2:3], v[230:231] op_sel_hi:[1,0]
	v_pk_mul_f32 v[32:33], v[16:17], v[230:231] op_sel_hi:[1,0]
	v_pk_mul_f32 v[30:31], v[14:15], v[230:231] op_sel_hi:[1,0]
	v_mfma_f32_32x32x16_bf16 v[34:49], v[234:237], v[122:125], v[34:49]
	v_mul_f32_e64 v28, v12, v230
	v_mul_f32_e64 v29, v13, v230
	v_mul_f32_e64 v26, v10, v230
	v_mul_f32_e64 v27, v11, v230
	v_mul_f32_e64 v24, v8, v230
	v_mul_f32_e64 v25, v9, v230
	v_pk_mul_f32 v[22:23], v[6:7], v[230:231] op_sel_hi:[1,0]
	v_pk_mul_f32 v[20:21], v[4:5], v[230:231] op_sel_hi:[1,0]
	v_pk_mul_f32 v[16:17], v[64:65], v[230:231] op_sel_hi:[1,0]
	v_pk_mul_f32 v[14:15], v[62:63], v[230:231] op_sel_hi:[1,0]
	v_mfma_f32_32x32x16_bf16 v[34:49], v[238:241], v[118:121], v[34:49]
	v_mul_f32_e64 v12, v60, v230
	v_mul_f32_e64 v13, v61, v230
	v_mul_f32_e64 v10, v58, v230
	v_mul_f32_e64 v11, v59, v230
	v_mul_f32_e64 v8, v56, v230
	v_mul_f32_e64 v9, v57, v230
	v_pk_mul_f32 v[6:7], v[54:55], v[230:231] op_sel_hi:[1,0]
	v_pk_mul_f32 v[4:5], v[52:53], v[230:231] op_sel_hi:[1,0]
	v_pk_mul_f32 v[2:3], v[50:51], v[230:231] op_sel_hi:[1,0]
	v_add_u32_e32 v230, s5, v1
	v_mfma_f32_32x32x16_bf16 v[34:49], v[242:245], v[114:117], v[34:49]
	ds_read_b32 v231, v230
	v_mul_u32_u24_e32 v50, 0x110, v205
	s_lshl_b32 s5, s11, 1
	v_add3_u32 v211, s1, v50, v138
	v_mov_b32_e32 v1, v210
	s_add_i32 s5, s5, 2
	v_add3_u32 v62, v254, v138, s95
	v_mfma_f32_32x32x16_bf16 v[34:49], v[246:249], v[110:113], v[34:49]
	v_mov_b32_e32 v63, v204
	v_mov_b32_e32 v64, v227
	v_mov_b32_e32 v65, v211
	v_mfma_f32_32x32x16_bf16 v[34:49], v[250:253], v[106:109], v[34:49]
